# diff-attention combine (O1 - lam*O2, rmsnorm, gain) fused into the c=1 attention epilogue; stand-alone combine phase and its grid barrier skipped; P2 state stores as full rows; P1 store drain off the
# speedup vs baseline: 1.1121x; 1.0083x over previous
.Lfa_entry:
	s_waitcnt lgkmcnt(0)
	s_load_dwordx2 s[0:1], s[30:31], 0xd8
	v_mbcnt_lo_u32_b32 v0, -1, 0
	v_mbcnt_hi_u32_b32 v0, -1, v0
	s_lshr_b32 s15, s3, 6
	s_lshl_b32 s20, s15, 10
	s_mul_i32 s21, s15, 0xc00
	s_add_i32 s21, s21, 0x18800
	v_lshlrev_b32_e32 v1, 2, v0
	v_add_u32_e32 v1, s21, v1
	ds_write_b32 v1, v162 offset:0
	ds_write_b32 v1, v163 offset:256
	ds_write_b32 v1, v164 offset:512
	ds_write_b32 v1, v165 offset:768
	ds_write_b32 v1, v166 offset:1024
	ds_write_b32 v1, v167 offset:1280
	ds_write_b32 v1, v168 offset:1536
	ds_write_b32 v1, v169 offset:1792
	ds_write_b32 v1, v170 offset:2048
	ds_write_b32 v1, v171 offset:2304
	ds_write_b32 v1, v172 offset:2560
	ds_write_b32 v1, v173 offset:2816
	v_and_b32_e32 v2, 31, v0
	v_lshrrev_b32_e32 v3, 5, v0
	v_lshlrev_b32_e32 v208, 8, v2
	v_and_b32_e32 v4, 7, v2
	v_lshlrev_b32_e32 v4, 4, v4
	v_lshlrev_b32_e32 v5, 4, v3
	v_xor_b32_e32 v209, v4, v5
	v_and_b32_e32 v4, 3, v0
	v_lshlrev_b32_e32 v4, 3, v4
	v_bfe_u32 v5, v0, 2, 2
	v_lshl_or_b32 v4, v5, 6, v4
	v_bfe_u32 v5, v0, 4, 1
	v_lshl_or_b32 v4, v5, 5, v4
	v_lshl_or_b32 v210, v3, 8, v4
	s_add_i32 s21, s20, 0x1e800
	v_lshl_add_u32 v11, v0, 2, s21
	v_lshrrev_b32_e32 v4, 4, v0
	v_and_b32_e32 v5, 15, v0
	s_add_i32 s21, s15, 0
	s_lshl_b32 s21, s21, 2
	v_add_u32_e32 v6, s21, v4
	v_and_b32_e32 v7, 7, v6
	v_xor_b32_e32 v7, v5, v7
	v_lshlrev_b32_e32 v7, 4, v7
	v_lshl_or_b32 v12, v6, 8, v7
	ds_write_b32 v11, v12 offset:0
	s_add_i32 s21, s15, 8
	s_lshl_b32 s21, s21, 2
	v_add_u32_e32 v6, s21, v4
	v_and_b32_e32 v7, 7, v6
	v_xor_b32_e32 v7, v5, v7
	v_lshlrev_b32_e32 v7, 4, v7
	v_lshl_or_b32 v12, v6, 8, v7
	ds_write_b32 v11, v12 offset:256
	v_bfe_u32 v4, v0, 2, 3
	v_and_b32_e32 v5, 3, v0
	v_lshlrev_b32_e32 v5, 4, v5
	s_add_i32 s21, s15, 0
	s_lshl_b32 s21, s21, 1
	v_add_u32_e32 v6, s21, v3
	v_lshrrev_b32_e32 v7, 2, v6
	v_lshl_or_b32 v7, v7, 3, v4
	v_and_b32_e32 v8, 3, v6
	v_lshl_or_b32 v8, v8, 6, v5
	v_and_b32_e32 v9, 0xfffffff3, v7
	v_bfe_u32 v10, v7, 2, 1
	v_lshl_or_b32 v9, v10, 3, v9
	v_bfe_u32 v10, v7, 3, 1
	v_lshl_or_b32 v9, v10, 2, v9
	v_lshl_or_b32 v12, v9, 8, v8
	ds_write_b32 v11, v12 offset:512
	s_add_i32 s21, s15, 8
	s_lshl_b32 s21, s21, 1
	v_add_u32_e32 v6, s21, v3
	v_lshrrev_b32_e32 v7, 2, v6
	v_lshl_or_b32 v7, v7, 3, v4
	v_and_b32_e32 v8, 3, v6
	v_lshl_or_b32 v8, v8, 6, v5
	v_and_b32_e32 v9, 0xfffffff3, v7
	v_bfe_u32 v10, v7, 2, 1
	v_lshl_or_b32 v9, v10, 3, v9
	v_bfe_u32 v10, v7, 3, 1
	v_lshl_or_b32 v9, v10, 2, v9
	v_lshl_or_b32 v12, v9, 8, v8
	ds_write_b32 v11, v12 offset:768
	s_waitcnt lgkmcnt(0)
	s_load_dwordx2 s[48:49], s[30:31], 0x90
	s_sub_i32 s21, s11, 2
	s_lshl_b32 s52, s21, 11
	v_lshlrev_b32_e32 v12, 2, v0
	s_waitcnt lgkmcnt(0)
	s_add_u32 s48, s48, s52
	s_addc_u32 s49, s49, 0
	global_load_dword v4, v12, s[48:49] offset:0
	global_load_dword v5, v12, s[48:49] offset:256
	global_load_dword v6, v12, s[48:49] offset:512
	global_load_dword v7, v12, s[48:49] offset:768
	global_load_dword v8, v12, s[48:49] offset:1024
	global_load_dword v9, v12, s[48:49] offset:1280
	global_load_dword v10, v12, s[48:49] offset:1536
	global_load_dword v11, v12, s[48:49] offset:1792
	s_waitcnt vmcnt(0)
	v_mul_f32_e32 v13, v4, v6
	v_fmac_f32_e32 v13, v5, v7
	v_mul_f32_e32 v14, v8, v10
	v_fmac_f32_e32 v14, v9, v11
	s_nop 1
	v_add_f32_dpp v13, v13, v13 quad_perm:[1,0,3,2] row_mask:0xf bank_mask:0xf bound_ctrl:1
	s_nop 1
	v_add_f32_dpp v13, v13, v13 quad_perm:[2,3,0,1] row_mask:0xf bank_mask:0xf bound_ctrl:1
	s_nop 1
	v_add_f32_dpp v13, v13, v13 row_half_mirror row_mask:0xf bank_mask:0xf bound_ctrl:1
	s_nop 1
	v_add_f32_dpp v13, v13, v13 row_mirror row_mask:0xf bank_mask:0xf bound_ctrl:1
	v_mov_b32_e32 v15, 0
	s_nop 1
	v_mov_b32_dpp v15, v13 row_bcast:15 row_mask:0xa bank_mask:0xf
	v_add_f32_e32 v13, v13, v15
	v_mov_b32_e32 v15, 0
	s_nop 1
	v_mov_b32_dpp v15, v13 row_bcast:31 row_mask:0xc bank_mask:0xf
	v_add_f32_e32 v13, v13, v15
	s_nop 1
	v_readlane_b32 s48, v13, 63
	s_nop 1
	v_add_f32_dpp v14, v14, v14 quad_perm:[1,0,3,2] row_mask:0xf bank_mask:0xf bound_ctrl:1
	s_nop 1
	v_add_f32_dpp v14, v14, v14 quad_perm:[2,3,0,1] row_mask:0xf bank_mask:0xf bound_ctrl:1
	s_nop 1
	v_add_f32_dpp v14, v14, v14 row_half_mirror row_mask:0xf bank_mask:0xf bound_ctrl:1
	s_nop 1
	v_add_f32_dpp v14, v14, v14 row_mirror row_mask:0xf bank_mask:0xf bound_ctrl:1
	v_mov_b32_e32 v15, 0
	s_nop 1
	v_mov_b32_dpp v15, v14 row_bcast:15 row_mask:0xa bank_mask:0xf
	v_add_f32_e32 v14, v14, v15
	v_mov_b32_e32 v15, 0
	s_nop 1
	v_mov_b32_dpp v15, v14 row_bcast:31 row_mask:0xc bank_mask:0xf
	v_add_f32_e32 v14, v14, v15
	s_nop 1
	v_readlane_b32 s49, v14, 63
	s_nop 1
	v_mov_b32_e32 v13, s48
	v_mov_b32_e32 v14, s49
	v_mul_f32_e32 v13, 0x3fb8aa3b, v13
	v_mul_f32_e32 v14, 0x3fb8aa3b, v14
	v_exp_f32_e32 v13, v13
	v_exp_f32_e32 v14, v14
	s_mov_b32 s21, 0x3f0e59d5
	s_mov_b32 s52, 0x3ef1014c
	s_cmp_eq_u32 s11, 2
	s_cselect_b32 s21, s52, s21
	v_sub_f32_e32 v13, v13, v14
	v_add_f32_e32 v13, s21, v13
	v_sub_f32_e64 v14, 1.0, s21
	s_nop 0
	v_readfirstlane_b32 s79, v13
	v_readfirstlane_b32 s88, v14
	s_mov_b32 s2, s94
.Lfa_task:
	s_cmpk_lt_u32 s2, 0x100
	s_cbranch_scc0 .Lfa_done
	s_and_b32 s21, s2, 7
	s_lshr_b32 s74, s2, 3
	s_lshr_b32 s10, s74, 4
	s_lshl_b32 s21, s21, 1
	s_add_i32 s10, s10, s21
	s_lshl_b32 s10, s10, 1
	s_and_b32 s89, s74, 15
	s_mov_b32 s9, 0
.Lfa_block:
	s_sub_i32 s21, 31, s89
	s_cmp_lt_u32 s9, 2
	s_cselect_b32 s8, s89, s21
	s_and_b32 s21, s9, 1
	s_and_b32 s10, s10, 0xfffffffe
	s_or_b32 s10, s10, s21
	s_lshl_b32 s21, s10, 21
	s_add_u32 s28, s0, 0x402ac000
	s_addc_u32 s29, s1, 0
	s_add_u32 s28, s28, s21
	s_addc_u32 s29, s29, 0
	s_lshr_b32 s74, s10, 1
	s_lshl_b32 s74, s74, 22
	s_add_u32 s34, s0, 0x442ac000
	s_addc_u32 s35, s1, 0
	s_add_u32 s34, s34, s74
	s_addc_u32 s35, s35, 0
	s_add_u32 s38, s34, 0x200000
	s_addc_u32 s39, s35, 0
	s_lshl_b32 s74, s8, 16
	s_add_u32 s40, s0, 0x482ac000
	s_addc_u32 s41, s1, 0
	s_add_u32 s40, s40, s21
	s_addc_u32 s41, s41, 0
	s_add_u32 s40, s40, s74
	s_addc_u32 s41, s41, 0
	s_lshl_b32 s21, s10, 22
	s_add_u32 s42, s0, 0x382ac000
	s_addc_u32 s43, s1, 0
	s_add_u32 s42, s42, s21
	s_addc_u32 s43, s43, 0
	s_add_u32 s42, s42, s74
	s_addc_u32 s43, s43, 0
	s_add_u32 s44, s42, 0x200000
	s_addc_u32 s45, s43, 0
	v_mbcnt_lo_u32_b32 v0, -1, 0
	v_mbcnt_hi_u32_b32 v0, -1, v0
	v_and_b32_e32 v2, 31, v0
	v_lshrrev_b32_e32 v3, 5, v0
	s_lshl_b32 s21, s15, 5
	v_add_u32_e32 v2, s21, v2
	v_lshlrev_b32_e32 v2, 8, v2
	v_lshl_or_b32 v2, v3, 4, v2
	global_load_dwordx4 v[162:165], v2, s[40:41] offset:0
	global_load_dwordx4 v[166:169], v2, s[40:41] offset:32
	global_load_dwordx4 v[170:173], v2, s[40:41] offset:64
	global_load_dwordx4 v[174:177], v2, s[40:41] offset:96
	global_load_dwordx4 v[178:181], v2, s[40:41] offset:128
	global_load_dwordx4 v[182:185], v2, s[40:41] offset:160
	global_load_dwordx4 v[186:189], v2, s[40:41] offset:192
	global_load_dwordx4 v[190:193], v2, s[40:41] offset:224
	v_mov_b32_e32 v0, 0
	v_mov_b32_e32 v1, 0
	v_mov_b32_e32 v3, 0
	v_mov_b32_e32 v4, 0
	v_mov_b32_e32 v5, 0
	v_mov_b32_e32 v6, 0
	v_mov_b32_e32 v7, 0
	v_mov_b32_e32 v8, 0
	v_mov_b32_e32 v9, 0
	v_mov_b32_e32 v10, 0
	v_mov_b32_e32 v11, 0
	v_mov_b32_e32 v12, 0
	v_mov_b32_e32 v13, 0
	v_mov_b32_e32 v14, 0
	v_mov_b32_e32 v15, 0
	v_mov_b32_e32 v16, 0
	v_mov_b32_e32 v17, 0
	v_mov_b32_e32 v18, 0
	v_mov_b32_e32 v19, 0
	v_mov_b32_e32 v20, 0
	v_mov_b32_e32 v21, 0
	v_mov_b32_e32 v22, 0
	v_mov_b32_e32 v23, 0
	v_mov_b32_e32 v24, 0
	v_mov_b32_e32 v25, 0
	v_mov_b32_e32 v26, 0
	v_mov_b32_e32 v27, 0
	v_mov_b32_e32 v28, 0
	v_mov_b32_e32 v29, 0
	v_mov_b32_e32 v30, 0
	v_mov_b32_e32 v31, 0
	v_mov_b32_e32 v32, 0
	v_mov_b32_e32 v33, 0
	v_mov_b32_e32 v34, 0
	v_mov_b32_e32 v35, 0
	v_mov_b32_e32 v36, 0
	v_mov_b32_e32 v37, 0
	v_mov_b32_e32 v38, 0
	v_mov_b32_e32 v39, 0
	v_mov_b32_e32 v40, 0
	v_mov_b32_e32 v41, 0
	v_mov_b32_e32 v42, 0
	v_mov_b32_e32 v43, 0
	v_mov_b32_e32 v44, 0
	v_mov_b32_e32 v45, 0
	v_mov_b32_e32 v46, 0
	v_mov_b32_e32 v47, 0
	v_mov_b32_e32 v48, 0
	v_mov_b32_e32 v49, 0
	v_mov_b32_e32 v50, 0
	v_mov_b32_e32 v51, 0
	v_mov_b32_e32 v52, 0
	v_mov_b32_e32 v53, 0
	v_mov_b32_e32 v54, 0
	v_mov_b32_e32 v55, 0
	v_mov_b32_e32 v56, 0
	v_mov_b32_e32 v57, 0
	v_mov_b32_e32 v58, 0
	v_mov_b32_e32 v59, 0
	v_mov_b32_e32 v60, 0
	v_mov_b32_e32 v61, 0
	v_mov_b32_e32 v62, 0
	v_mov_b32_e32 v63, 0
	v_mov_b32_e32 v64, 0
	v_mov_b32_e32 v65, 0
	v_mov_b32_e32 v66, 0
	v_mov_b32_e32 v67, 0
	v_mov_b32_e32 v68, 0
	v_mov_b32_e32 v69, 0
	v_mov_b32_e32 v70, 0
	v_mov_b32_e32 v71, 0
	v_mov_b32_e32 v72, 0
	v_mov_b32_e32 v73, 0
	v_mov_b32_e32 v74, 0
	v_mov_b32_e32 v75, 0
	v_mov_b32_e32 v76, 0
	v_mov_b32_e32 v77, 0
	v_mov_b32_e32 v78, 0
	v_mov_b32_e32 v79, 0
	v_mov_b32_e32 v80, 0
	v_mov_b32_e32 v81, 0
	v_mov_b32_e32 v82, 0
	v_mov_b32_e32 v83, 0
	v_mov_b32_e32 v84, 0
	v_mov_b32_e32 v85, 0
	v_mov_b32_e32 v86, 0
	v_mov_b32_e32 v87, 0
	v_mov_b32_e32 v88, 0
	v_mov_b32_e32 v89, 0
	v_mov_b32_e32 v90, 0
	v_mov_b32_e32 v91, 0
	v_mov_b32_e32 v92, 0
	v_mov_b32_e32 v93, 0
	v_mov_b32_e32 v94, 0
	v_mov_b32_e32 v95, 0
	v_mov_b32_e32 v98, 0
	v_mov_b32_e32 v99, 0
	v_mov_b32_e32 v100, 0
	v_mov_b32_e32 v101, 0
	v_mov_b32_e32 v102, 0
	v_mov_b32_e32 v103, 0
	v_mov_b32_e32 v104, 0
	v_mov_b32_e32 v105, 0
	v_mov_b32_e32 v106, 0
	v_mov_b32_e32 v107, 0
	v_mov_b32_e32 v108, 0
	v_mov_b32_e32 v109, 0
	v_mov_b32_e32 v110, 0
	v_mov_b32_e32 v111, 0
	v_mov_b32_e32 v112, 0
	v_mov_b32_e32 v113, 0
	v_mov_b32_e32 v114, 0
	v_mov_b32_e32 v115, 0
	v_mov_b32_e32 v116, 0
	v_mov_b32_e32 v117, 0
	v_mov_b32_e32 v118, 0
	v_mov_b32_e32 v119, 0
	v_mov_b32_e32 v120, 0
	v_mov_b32_e32 v121, 0
	v_mov_b32_e32 v122, 0
	v_mov_b32_e32 v123, 0
	v_mov_b32_e32 v124, 0
	v_mov_b32_e32 v125, 0
	v_mov_b32_e32 v126, 0
	v_mov_b32_e32 v127, 0
	v_mov_b32_e32 v128, 0
	v_mov_b32_e32 v129, 0
	v_mov_b32_e32 v2, 0
	v_mov_b32_e32 v96, 0xf149f2ca
	v_mov_b32_e32 v202, 0
	s_add_i32 s5, s8, 1
	s_lshl_b32 s5, s5, 2
	s_lshl_b32 s14, s8, 2
	s_lshr_b32 s21, s15, 1
	s_add_i32 s14, s14, s21
	s_lshl_b32 s24, s8, 8
	s_lshl_b32 s21, s15, 5
	s_add_i32 s24, s24, s21
	s_mov_b32 s4, 0
	v_mbcnt_lo_u32_b32 v216, -1, 0
	v_mbcnt_hi_u32_b32 v216, -1, v216
	s_add_i32 s21, s20, 0x1e800
	v_lshl_add_u32 v216, v216, 2, s21
	ds_read_b32 v212, v216
	ds_read_b32 v213, v216 offset:256
	ds_read_b32 v214, v216 offset:512
	ds_read_b32 v215, v216 offset:768
	s_waitcnt lgkmcnt(0)
	s_mov_b32 s64, 0x0
	s_add_i32 s21, s64, s20
	s_mov_b32 m0, s21
	s_nop 0
	global_load_lds_dwordx4 v212, s[28:29]
	s_add_i32 m0, s21, 0x2000
	s_nop 0
	global_load_lds_dwordx4 v213, s[28:29]
	s_add_u32 s28, s28, 0x4000
	s_addc_u32 s29, s29, 0
	s_mov_b32 s65, 0x8000
	s_add_i32 s21, s65, s20
	s_mov_b32 m0, s21
	s_nop 0
	global_load_lds_dwordx4 v214, s[34:35]
	s_add_i32 m0, s21, 0x2000
	s_nop 0
	global_load_lds_dwordx4 v215, s[34:35]
	s_add_i32 m0, s21, 0x4000
	s_nop 0
	global_load_lds_dwordx4 v214, s[38:39]
	s_add_i32 m0, s21, 0x6000
	s_nop 0
	global_load_lds_dwordx4 v215, s[38:39]
	s_add_u32 s34, s34, 0x4000
	s_addc_u32 s35, s35, 0
	s_add_u32 s38, s38, 0x4000
	s_addc_u32 s39, s39, 0

.Lfa_noresc_t:
	s_waitcnt lgkmcnt(8)
	v_mfma_f32_32x32x16_bf16 v[0:15], v[212:215], v[228:231], v[0:15]
	v_mfma_f32_32x32x16_bf16 v[0:15], v[216:219], v[232:235], v[0:15]
	v_mfma_f32_32x32x16_bf16 v[0:15], v[220:223], v[236:239], v[0:15]
	v_mfma_f32_32x32x16_bf16 v[0:15], v[224:227], v[240:243], v[0:15]
	ds_read_b64_tr_b16 v[228:229], v253 offset:1024
	ds_read_b64_tr_b16 v[230:231], v253 offset:3072
	ds_read_b64_tr_b16 v[232:233], v253 offset:5120
	ds_read_b64_tr_b16 v[234:235], v253 offset:7168
	ds_read_b64_tr_b16 v[236:237], v253 offset:9216
	ds_read_b64_tr_b16 v[238:239], v253 offset:11264
	ds_read_b64_tr_b16 v[240:241], v253 offset:13312
	ds_read_b64_tr_b16 v[242:243], v253 offset:15360
	s_waitcnt lgkmcnt(8)
	v_mfma_f32_32x32x16_bf16 v[16:31], v[212:215], v[244:247], v[16:31]
	v_mfma_f32_32x32x16_bf16 v[16:31], v[216:219], v[248:251], v[16:31]
	v_mfma_f32_32x32x16_bf16 v[16:31], v[220:223], v[194:197], v[16:31]
	v_mfma_f32_32x32x16_bf16 v[16:31], v[224:227], v[198:201], v[16:31]
	ds_read_b64_tr_b16 v[244:245], v253 offset:1536
	ds_read_b64_tr_b16 v[246:247], v253 offset:3584
	ds_read_b64_tr_b16 v[248:249], v253 offset:5632
	ds_read_b64_tr_b16 v[250:251], v253 offset:7680
	ds_read_b64_tr_b16 v[194:195], v253 offset:9728
	ds_read_b64_tr_b16 v[196:197], v253 offset:11776
	ds_read_b64_tr_b16 v[198:199], v253 offset:13824
	ds_read_b64_tr_b16 v[200:201], v253 offset:15872
	s_waitcnt lgkmcnt(8)
	v_mfma_f32_32x32x16_bf16 v[32:47], v[212:215], v[228:231], v[32:47]
	v_mfma_f32_32x32x16_bf16 v[32:47], v[216:219], v[232:235], v[32:47]
	v_mfma_f32_32x32x16_bf16 v[32:47], v[220:223], v[236:239], v[32:47]
	v_mfma_f32_32x32x16_bf16 v[32:47], v[224:227], v[240:243], v[32:47]
	ds_read_b64_tr_b16 v[228:229], v253 offset:16384
	ds_read_b64_tr_b16 v[230:231], v253 offset:18432
	ds_read_b64_tr_b16 v[232:233], v253 offset:20480
	ds_read_b64_tr_b16 v[234:235], v253 offset:22528
	ds_read_b64_tr_b16 v[236:237], v253 offset:24576
	ds_read_b64_tr_b16 v[238:239], v253 offset:26624
	ds_read_b64_tr_b16 v[240:241], v253 offset:28672
	ds_read_b64_tr_b16 v[242:243], v253 offset:30720
	s_waitcnt lgkmcnt(8)
	v_mfma_f32_32x32x16_bf16 v[48:63], v[212:215], v[244:247], v[48:63]
	v_mfma_f32_32x32x16_bf16 v[48:63], v[216:219], v[248:251], v[48:63]
	v_mfma_f32_32x32x16_bf16 v[48:63], v[220:223], v[194:197], v[48:63]
	v_mfma_f32_32x32x16_bf16 v[48:63], v[224:227], v[198:201], v[48:63]
	ds_read_b64_tr_b16 v[244:245], v253 offset:16896
	ds_read_b64_tr_b16 v[246:247], v253 offset:18944
	ds_read_b64_tr_b16 v[248:249], v253 offset:20992
	ds_read_b64_tr_b16 v[250:251], v253 offset:23040
	ds_read_b64_tr_b16 v[194:195], v253 offset:25088
	ds_read_b64_tr_b16 v[196:197], v253 offset:27136
	ds_read_b64_tr_b16 v[198:199], v253 offset:29184
	ds_read_b64_tr_b16 v[200:201], v253 offset:31232
	s_waitcnt lgkmcnt(8)
	v_mfma_f32_32x32x16_bf16 v[64:79], v[212:215], v[228:231], v[64:79]
	v_mfma_f32_32x32x16_bf16 v[64:79], v[216:219], v[232:235], v[64:79]
	v_mfma_f32_32x32x16_bf16 v[64:79], v[220:223], v[236:239], v[64:79]
	v_mfma_f32_32x32x16_bf16 v[64:79], v[224:227], v[240:243], v[64:79]
	ds_read_b64_tr_b16 v[228:229], v253 offset:17408
	ds_read_b64_tr_b16 v[230:231], v253 offset:19456
	ds_read_b64_tr_b16 v[232:233], v253 offset:21504
	ds_read_b64_tr_b16 v[234:235], v253 offset:23552
	ds_read_b64_tr_b16 v[236:237], v253 offset:25600
	ds_read_b64_tr_b16 v[238:239], v253 offset:27648
	ds_read_b64_tr_b16 v[240:241], v253 offset:29696
	ds_read_b64_tr_b16 v[242:243], v253 offset:31744
	s_waitcnt lgkmcnt(8)
	v_mfma_f32_32x32x16_bf16 v[80:95], v[212:215], v[244:247], v[80:95]
	v_mfma_f32_32x32x16_bf16 v[80:95], v[216:219], v[248:251], v[80:95]
	v_mfma_f32_32x32x16_bf16 v[80:95], v[220:223], v[194:197], v[80:95]
	v_mfma_f32_32x32x16_bf16 v[80:95], v[224:227], v[198:201], v[80:95]
	ds_read_b64_tr_b16 v[244:245], v253 offset:17920
	ds_read_b64_tr_b16 v[246:247], v253 offset:19968
	ds_read_b64_tr_b16 v[248:249], v253 offset:22016
	ds_read_b64_tr_b16 v[250:251], v253 offset:24064
	ds_read_b64_tr_b16 v[194:195], v253 offset:26112
	ds_read_b64_tr_b16 v[196:197], v253 offset:28160
	ds_read_b64_tr_b16 v[198:199], v253 offset:30208
	ds_read_b64_tr_b16 v[200:201], v253 offset:32256
	s_waitcnt lgkmcnt(8)
	v_mfma_f32_32x32x16_bf16 v[98:113], v[212:215], v[228:231], v[98:113]
	v_mfma_f32_32x32x16_bf16 v[98:113], v[216:219], v[232:235], v[98:113]
	v_mfma_f32_32x32x16_bf16 v[98:113], v[220:223], v[236:239], v[98:113]
	v_mfma_f32_32x32x16_bf16 v[98:113], v[224:227], v[240:243], v[98:113]
	s_waitcnt lgkmcnt(0)
	v_mfma_f32_32x32x16_bf16 v[114:129], v[212:215], v[244:247], v[114:129]
	v_mfma_f32_32x32x16_bf16 v[114:129], v[216:219], v[248:251], v[114:129]
	v_mfma_f32_32x32x16_bf16 v[114:129], v[220:223], v[194:197], v[114:129]
	v_mfma_f32_32x32x16_bf16 v[114:129], v[224:227], v[198:201], v[114:129]
	s_add_i32 s4, s4, 1
	s_cmp_lt_u32 s4, s5
	s_cbranch_scc1 .Lfa_tile
	s_bitcmp1_b32 s9, 0
	s_cbranch_scc1 .Lfa_epi_c1
	s_nop 7
	s_nop 7
	v_mbcnt_lo_u32_b32 v229, -1, 0
	v_mbcnt_hi_u32_b32 v229, -1, v229
	s_lshl_b32 s21, s15, 8
	s_add_i32 s21, s21, 0x18000
	v_and_b32_e32 v231, 31, v229
	v_lshl_add_u32 v230, v231, 2, s21
	v_lshrrev_b32_e32 v229, 5, v229
	v_lshl_add_u32 v232, v229, 4, s21
	ds_write_b32 v230, v202 offset:128
	s_waitcnt lgkmcnt(0)
	ds_read_b128 v[236:239], v232 offset:128
	ds_read_b128 v[240:243], v232 offset:160
	ds_read_b128 v[244:247], v232 offset:192
	ds_read_b128 v[248:251], v232 offset:224
	s_waitcnt lgkmcnt(0)
	v_rcp_f32_e32 v236, v236
	v_rcp_f32_e32 v237, v237
	v_rcp_f32_e32 v238, v238
	v_rcp_f32_e32 v239, v239
	v_rcp_f32_e32 v240, v240
	v_rcp_f32_e32 v241, v241
	v_rcp_f32_e32 v242, v242
	v_rcp_f32_e32 v243, v243
	v_rcp_f32_e32 v244, v244
	v_rcp_f32_e32 v245, v245
	v_rcp_f32_e32 v246, v246
	v_rcp_f32_e32 v247, v247
	v_rcp_f32_e32 v248, v248
	v_rcp_f32_e32 v249, v249
	v_rcp_f32_e32 v250, v250
	v_rcp_f32_e32 v251, v251
	s_nop 0
	v_mul_f32_dpp v228, v0, v236 quad_perm:[1,0,3,2] row_mask:0xf bank_mask:0xf
	v_mul_f32_e32 v0, v0, v236
	v_cvt_pk_bf16_f32 v0, v0, v228
	v_mul_f32_dpp v228, v1, v237 quad_perm:[1,0,3,2] row_mask:0xf bank_mask:0xf
	v_mul_f32_e32 v1, v1, v237
	v_cvt_pk_bf16_f32 v1, v1, v228
	v_mul_f32_dpp v228, v2, v238 quad_perm:[1,0,3,2] row_mask:0xf bank_mask:0xf
	v_mul_f32_e32 v2, v2, v238
	v_cvt_pk_bf16_f32 v2, v2, v228
	v_mul_f32_dpp v228, v3, v239 quad_perm:[1,0,3,2] row_mask:0xf bank_mask:0xf
	v_mul_f32_e32 v3, v3, v239
	v_cvt_pk_bf16_f32 v3, v3, v228
	v_mul_f32_dpp v228, v4, v240 quad_perm:[1,0,3,2] row_mask:0xf bank_mask:0xf
	v_mul_f32_e32 v4, v4, v240
	v_cvt_pk_bf16_f32 v4, v4, v228
	v_mul_f32_dpp v228, v5, v241 quad_perm:[1,0,3,2] row_mask:0xf bank_mask:0xf
	v_mul_f32_e32 v5, v5, v241
	v_cvt_pk_bf16_f32 v5, v5, v228
	v_mul_f32_dpp v228, v6, v242 quad_perm:[1,0,3,2] row_mask:0xf bank_mask:0xf
	v_mul_f32_e32 v6, v6, v242
	v_cvt_pk_bf16_f32 v6, v6, v228
	v_mul_f32_dpp v228, v7, v243 quad_perm:[1,0,3,2] row_mask:0xf bank_mask:0xf
	v_mul_f32_e32 v7, v7, v243
	v_cvt_pk_bf16_f32 v7, v7, v228
	v_mul_f32_dpp v228, v8, v244 quad_perm:[1,0,3,2] row_mask:0xf bank_mask:0xf
	v_mul_f32_e32 v8, v8, v244
	v_cvt_pk_bf16_f32 v8, v8, v228
	v_mul_f32_dpp v228, v9, v245 quad_perm:[1,0,3,2] row_mask:0xf bank_mask:0xf
	v_mul_f32_e32 v9, v9, v245
	v_cvt_pk_bf16_f32 v9, v9, v228
	v_mul_f32_dpp v228, v10, v246 quad_perm:[1,0,3,2] row_mask:0xf bank_mask:0xf
	v_mul_f32_e32 v10, v10, v246
	v_cvt_pk_bf16_f32 v10, v10, v228
	v_mul_f32_dpp v228, v11, v247 quad_perm:[1,0,3,2] row_mask:0xf bank_mask:0xf
	v_mul_f32_e32 v11, v11, v247
	v_cvt_pk_bf16_f32 v11, v11, v228
	v_mul_f32_dpp v228, v12, v248 quad_perm:[1,0,3,2] row_mask:0xf bank_mask:0xf
	v_mul_f32_e32 v12, v12, v248
	v_cvt_pk_bf16_f32 v12, v12, v228
	v_mul_f32_dpp v228, v13, v249 quad_perm:[1,0,3,2] row_mask:0xf bank_mask:0xf
	v_mul_f32_e32 v13, v13, v249
	v_cvt_pk_bf16_f32 v13, v13, v228
	v_mul_f32_dpp v228, v14, v250 quad_perm:[1,0,3,2] row_mask:0xf bank_mask:0xf
	v_mul_f32_e32 v14, v14, v250
	v_cvt_pk_bf16_f32 v14, v14, v228
	v_mul_f32_dpp v228, v15, v251 quad_perm:[1,0,3,2] row_mask:0xf bank_mask:0xf
	v_mul_f32_e32 v15, v15, v251
	v_cvt_pk_bf16_f32 v15, v15, v228
	v_mul_f32_dpp v228, v16, v236 quad_perm:[1,0,3,2] row_mask:0xf bank_mask:0xf
	v_mul_f32_e32 v16, v16, v236
	v_cvt_pk_bf16_f32 v16, v16, v228
	v_mul_f32_dpp v228, v17, v237 quad_perm:[1,0,3,2] row_mask:0xf bank_mask:0xf
	v_mul_f32_e32 v17, v17, v237
	v_cvt_pk_bf16_f32 v17, v17, v228
	v_mul_f32_dpp v228, v18, v238 quad_perm:[1,0,3,2] row_mask:0xf bank_mask:0xf
	v_mul_f32_e32 v18, v18, v238
	v_cvt_pk_bf16_f32 v18, v18, v228
	v_mul_f32_dpp v228, v19, v239 quad_perm:[1,0,3,2] row_mask:0xf bank_mask:0xf
	v_mul_f32_e32 v19, v19, v239
	v_cvt_pk_bf16_f32 v19, v19, v228
	v_mul_f32_dpp v228, v20, v240 quad_perm:[1,0,3,2] row_mask:0xf bank_mask:0xf
	v_mul_f32_e32 v20, v20, v240
	v_cvt_pk_bf16_f32 v20, v20, v228
	v_mul_f32_dpp v228, v21, v241 quad_perm:[1,0,3,2] row_mask:0xf bank_mask:0xf
	v_mul_f32_e32 v21, v21, v241
	v_cvt_pk_bf16_f32 v21, v21, v228
	v_mul_f32_dpp v228, v22, v242 quad_perm:[1,0,3,2] row_mask:0xf bank_mask:0xf
	v_mul_f32_e32 v22, v22, v242
	v_cvt_pk_bf16_f32 v22, v22, v228
	v_mul_f32_dpp v228, v23, v243 quad_perm:[1,0,3,2] row_mask:0xf bank_mask:0xf
	v_mul_f32_e32 v23, v23, v243
	v_cvt_pk_bf16_f32 v23, v23, v228
	v_mul_f32_dpp v228, v24, v244 quad_perm:[1,0,3,2] row_mask:0xf bank_mask:0xf
	v_mul_f32_e32 v24, v24, v244
	v_cvt_pk_bf16_f32 v24, v24, v228
	v_mul_f32_dpp v228, v25, v245 quad_perm:[1,0,3,2] row_mask:0xf bank_mask:0xf
	v_mul_f32_e32 v25, v25, v245
	v_cvt_pk_bf16_f32 v25, v25, v228
	v_mul_f32_dpp v228, v26, v246 quad_perm:[1,0,3,2] row_mask:0xf bank_mask:0xf
	v_mul_f32_e32 v26, v26, v246
	v_cvt_pk_bf16_f32 v26, v26, v228
	v_mul_f32_dpp v228, v27, v247 quad_perm:[1,0,3,2] row_mask:0xf bank_mask:0xf
	v_mul_f32_e32 v27, v27, v247
	v_cvt_pk_bf16_f32 v27, v27, v228
	v_mul_f32_dpp v228, v28, v248 quad_perm:[1,0,3,2] row_mask:0xf bank_mask:0xf
	v_mul_f32_e32 v28, v28, v248
	v_cvt_pk_bf16_f32 v28, v28, v228
	v_mul_f32_dpp v228, v29, v249 quad_perm:[1,0,3,2] row_mask:0xf bank_mask:0xf
	v_mul_f32_e32 v29, v29, v249
	v_cvt_pk_bf16_f32 v29, v29, v228
	v_mul_f32_dpp v228, v30, v250 quad_perm:[1,0,3,2] row_mask:0xf bank_mask:0xf
	v_mul_f32_e32 v30, v30, v250
	v_cvt_pk_bf16_f32 v30, v30, v228
	v_mul_f32_dpp v228, v31, v251 quad_perm:[1,0,3,2] row_mask:0xf bank_mask:0xf
	v_mul_f32_e32 v31, v31, v251
	v_cvt_pk_bf16_f32 v31, v31, v228
	v_mul_f32_dpp v228, v32, v236 quad_perm:[1,0,3,2] row_mask:0xf bank_mask:0xf
	v_mul_f32_e32 v32, v32, v236
	v_cvt_pk_bf16_f32 v32, v32, v228
	v_mul_f32_dpp v228, v33, v237 quad_perm:[1,0,3,2] row_mask:0xf bank_mask:0xf
	v_mul_f32_e32 v33, v33, v237
	v_cvt_pk_bf16_f32 v33, v33, v228
	v_mul_f32_dpp v228, v34, v238 quad_perm:[1,0,3,2] row_mask:0xf bank_mask:0xf
	v_mul_f32_e32 v34, v34, v238
	v_cvt_pk_bf16_f32 v34, v34, v228
	v_mul_f32_dpp v228, v35, v239 quad_perm:[1,0,3,2] row_mask:0xf bank_mask:0xf
	v_mul_f32_e32 v35, v35, v239
	v_cvt_pk_bf16_f32 v35, v35, v228
	v_mul_f32_dpp v228, v36, v240 quad_perm:[1,0,3,2] row_mask:0xf bank_mask:0xf
	v_mul_f32_e32 v36, v36, v240
	v_cvt_pk_bf16_f32 v36, v36, v228
	v_mul_f32_dpp v228, v37, v241 quad_perm:[1,0,3,2] row_mask:0xf bank_mask:0xf
	v_mul_f32_e32 v37, v37, v241
	v_cvt_pk_bf16_f32 v37, v37, v228
	v_mul_f32_dpp v228, v38, v242 quad_perm:[1,0,3,2] row_mask:0xf bank_mask:0xf
	v_mul_f32_e32 v38, v38, v242
	v_cvt_pk_bf16_f32 v38, v38, v228
	v_mul_f32_dpp v228, v39, v243 quad_perm:[1,0,3,2] row_mask:0xf bank_mask:0xf
	v_mul_f32_e32 v39, v39, v243
	v_cvt_pk_bf16_f32 v39, v39, v228
	v_mul_f32_dpp v228, v40, v244 quad_perm:[1,0,3,2] row_mask:0xf bank_mask:0xf
	v_mul_f32_e32 v40, v40, v244
	v_cvt_pk_bf16_f32 v40, v40, v228
	v_mul_f32_dpp v228, v41, v245 quad_perm:[1,0,3,2] row_mask:0xf bank_mask:0xf
	v_mul_f32_e32 v41, v41, v245
	v_cvt_pk_bf16_f32 v41, v41, v228
	v_mul_f32_dpp v228, v42, v246 quad_perm:[1,0,3,2] row_mask:0xf bank_mask:0xf
	v_mul_f32_e32 v42, v42, v246
	v_cvt_pk_bf16_f32 v42, v42, v228
	v_mul_f32_dpp v228, v43, v247 quad_perm:[1,0,3,2] row_mask:0xf bank_mask:0xf
	v_mul_f32_e32 v43, v43, v247
	v_cvt_pk_bf16_f32 v43, v43, v228
	v_mul_f32_dpp v228, v44, v248 quad_perm:[1,0,3,2] row_mask:0xf bank_mask:0xf
	v_mul_f32_e32 v44, v44, v248
	v_cvt_pk_bf16_f32 v44, v44, v228
	v_mul_f32_dpp v228, v45, v249 quad_perm:[1,0,3,2] row_mask:0xf bank_mask:0xf
	v_mul_f32_e32 v45, v45, v249
	v_cvt_pk_bf16_f32 v45, v45, v228
	v_mul_f32_dpp v228, v46, v250 quad_perm:[1,0,3,2] row_mask:0xf bank_mask:0xf
	v_mul_f32_e32 v46, v46, v250
	v_cvt_pk_bf16_f32 v46, v46, v228
	v_mul_f32_dpp v228, v47, v251 quad_perm:[1,0,3,2] row_mask:0xf bank_mask:0xf
	v_mul_f32_e32 v47, v47, v251
	v_cvt_pk_bf16_f32 v47, v47, v228
	v_mul_f32_dpp v228, v48, v236 quad_perm:[1,0,3,2] row_mask:0xf bank_mask:0xf
	v_mul_f32_e32 v48, v48, v236
	v_cvt_pk_bf16_f32 v48, v48, v228
	v_mul_f32_dpp v228, v49, v237 quad_perm:[1,0,3,2] row_mask:0xf bank_mask:0xf
	v_mul_f32_e32 v49, v49, v237
	v_cvt_pk_bf16_f32 v49, v49, v228
	v_mul_f32_dpp v228, v50, v238 quad_perm:[1,0,3,2] row_mask:0xf bank_mask:0xf
	v_mul_f32_e32 v50, v50, v238
	v_cvt_pk_bf16_f32 v50, v50, v228
	v_mul_f32_dpp v228, v51, v239 quad_perm:[1,0,3,2] row_mask:0xf bank_mask:0xf
	v_mul_f32_e32 v51, v51, v239
	v_cvt_pk_bf16_f32 v51, v51, v228
	v_mul_f32_dpp v228, v52, v240 quad_perm:[1,0,3,2] row_mask:0xf bank_mask:0xf
	v_mul_f32_e32 v52, v52, v240
	v_cvt_pk_bf16_f32 v52, v52, v228
	v_mul_f32_dpp v228, v53, v241 quad_perm:[1,0,3,2] row_mask:0xf bank_mask:0xf
	v_mul_f32_e32 v53, v53, v241
	v_cvt_pk_bf16_f32 v53, v53, v228
	v_mul_f32_dpp v228, v54, v242 quad_perm:[1,0,3,2] row_mask:0xf bank_mask:0xf
	v_mul_f32_e32 v54, v54, v242
	v_cvt_pk_bf16_f32 v54, v54, v228
	v_mul_f32_dpp v228, v55, v243 quad_perm:[1,0,3,2] row_mask:0xf bank_mask:0xf
	v_mul_f32_e32 v55, v55, v243
	v_cvt_pk_bf16_f32 v55, v55, v228
	v_mul_f32_dpp v228, v56, v244 quad_perm:[1,0,3,2] row_mask:0xf bank_mask:0xf
	v_mul_f32_e32 v56, v56, v244
	v_cvt_pk_bf16_f32 v56, v56, v228
	v_mul_f32_dpp v228, v57, v245 quad_perm:[1,0,3,2] row_mask:0xf bank_mask:0xf
	v_mul_f32_e32 v57, v57, v245
	v_cvt_pk_bf16_f32 v57, v57, v228
	v_mul_f32_dpp v228, v58, v246 quad_perm:[1,0,3,2] row_mask:0xf bank_mask:0xf
	v_mul_f32_e32 v58, v58, v246
	v_cvt_pk_bf16_f32 v58, v58, v228
	v_mul_f32_dpp v228, v59, v247 quad_perm:[1,0,3,2] row_mask:0xf bank_mask:0xf
	v_mul_f32_e32 v59, v59, v247
	v_cvt_pk_bf16_f32 v59, v59, v228
	v_mul_f32_dpp v228, v60, v248 quad_perm:[1,0,3,2] row_mask:0xf bank_mask:0xf
	v_mul_f32_e32 v60, v60, v248
	v_cvt_pk_bf16_f32 v60, v60, v228
	v_mul_f32_dpp v228, v61, v249 quad_perm:[1,0,3,2] row_mask:0xf bank_mask:0xf
	v_mul_f32_e32 v61, v61, v249
	v_cvt_pk_bf16_f32 v61, v61, v228
	v_mul_f32_dpp v228, v62, v250 quad_perm:[1,0,3,2] row_mask:0xf bank_mask:0xf
	v_mul_f32_e32 v62, v62, v250
	v_cvt_pk_bf16_f32 v62, v62, v228
	v_mul_f32_dpp v228, v63, v251 quad_perm:[1,0,3,2] row_mask:0xf bank_mask:0xf
	v_mul_f32_e32 v63, v63, v251
	v_cvt_pk_bf16_f32 v63, v63, v228
	v_mul_f32_dpp v228, v64, v236 quad_perm:[1,0,3,2] row_mask:0xf bank_mask:0xf
	v_mul_f32_e32 v64, v64, v236
	v_cvt_pk_bf16_f32 v64, v64, v228
	v_mul_f32_dpp v228, v65, v237 quad_perm:[1,0,3,2] row_mask:0xf bank_mask:0xf
	v_mul_f32_e32 v65, v65, v237
	v_cvt_pk_bf16_f32 v65, v65, v228
	v_mul_f32_dpp v228, v66, v238 quad_perm:[1,0,3,2] row_mask:0xf bank_mask:0xf
	v_mul_f32_e32 v66, v66, v238
	v_cvt_pk_bf16_f32 v66, v66, v228
	v_mul_f32_dpp v228, v67, v239 quad_perm:[1,0,3,2] row_mask:0xf bank_mask:0xf
	v_mul_f32_e32 v67, v67, v239
	v_cvt_pk_bf16_f32 v67, v67, v228
	v_mul_f32_dpp v228, v68, v240 quad_perm:[1,0,3,2] row_mask:0xf bank_mask:0xf
	v_mul_f32_e32 v68, v68, v240
	v_cvt_pk_bf16_f32 v68, v68, v228
	v_mul_f32_dpp v228, v69, v241 quad_perm:[1,0,3,2] row_mask:0xf bank_mask:0xf
	v_mul_f32_e32 v69, v69, v241
	v_cvt_pk_bf16_f32 v69, v69, v228
	v_mul_f32_dpp v228, v70, v242 quad_perm:[1,0,3,2] row_mask:0xf bank_mask:0xf
	v_mul_f32_e32 v70, v70, v242
	v_cvt_pk_bf16_f32 v70, v70, v228
	v_mul_f32_dpp v228, v71, v243 quad_perm:[1,0,3,2] row_mask:0xf bank_mask:0xf
	v_mul_f32_e32 v71, v71, v243
	v_cvt_pk_bf16_f32 v71, v71, v228
	v_mul_f32_dpp v228, v72, v244 quad_perm:[1,0,3,2] row_mask:0xf bank_mask:0xf
	v_mul_f32_e32 v72, v72, v244
	v_cvt_pk_bf16_f32 v72, v72, v228
	v_mul_f32_dpp v228, v73, v245 quad_perm:[1,0,3,2] row_mask:0xf bank_mask:0xf
	v_mul_f32_e32 v73, v73, v245
	v_cvt_pk_bf16_f32 v73, v73, v228
	v_mul_f32_dpp v228, v74, v246 quad_perm:[1,0,3,2] row_mask:0xf bank_mask:0xf
	v_mul_f32_e32 v74, v74, v246
	v_cvt_pk_bf16_f32 v74, v74, v228
	v_mul_f32_dpp v228, v75, v247 quad_perm:[1,0,3,2] row_mask:0xf bank_mask:0xf
	v_mul_f32_e32 v75, v75, v247
	v_cvt_pk_bf16_f32 v75, v75, v228
	v_mul_f32_dpp v228, v76, v248 quad_perm:[1,0,3,2] row_mask:0xf bank_mask:0xf
	v_mul_f32_e32 v76, v76, v248
	v_cvt_pk_bf16_f32 v76, v76, v228
	v_mul_f32_dpp v228, v77, v249 quad_perm:[1,0,3,2] row_mask:0xf bank_mask:0xf
	v_mul_f32_e32 v77, v77, v249
	v_cvt_pk_bf16_f32 v77, v77, v228
	v_mul_f32_dpp v228, v78, v250 quad_perm:[1,0,3,2] row_mask:0xf bank_mask:0xf
	v_mul_f32_e32 v78, v78, v250
	v_cvt_pk_bf16_f32 v78, v78, v228
	v_mul_f32_dpp v228, v79, v251 quad_perm:[1,0,3,2] row_mask:0xf bank_mask:0xf
	v_mul_f32_e32 v79, v79, v251
	v_cvt_pk_bf16_f32 v79, v79, v228
	v_mul_f32_dpp v228, v80, v236 quad_perm:[1,0,3,2] row_mask:0xf bank_mask:0xf
	v_mul_f32_e32 v80, v80, v236
	v_cvt_pk_bf16_f32 v80, v80, v228
	v_mul_f32_dpp v228, v81, v237 quad_perm:[1,0,3,2] row_mask:0xf bank_mask:0xf
	v_mul_f32_e32 v81, v81, v237
	v_cvt_pk_bf16_f32 v81, v81, v228
	v_mul_f32_dpp v228, v82, v238 quad_perm:[1,0,3,2] row_mask:0xf bank_mask:0xf
	v_mul_f32_e32 v82, v82, v238
	v_cvt_pk_bf16_f32 v82, v82, v228
	v_mul_f32_dpp v228, v83, v239 quad_perm:[1,0,3,2] row_mask:0xf bank_mask:0xf
	v_mul_f32_e32 v83, v83, v239
	v_cvt_pk_bf16_f32 v83, v83, v228
	v_mul_f32_dpp v228, v84, v240 quad_perm:[1,0,3,2] row_mask:0xf bank_mask:0xf
	v_mul_f32_e32 v84, v84, v240
	v_cvt_pk_bf16_f32 v84, v84, v228
	v_mul_f32_dpp v228, v85, v241 quad_perm:[1,0,3,2] row_mask:0xf bank_mask:0xf
	v_mul_f32_e32 v85, v85, v241
	v_cvt_pk_bf16_f32 v85, v85, v228
	v_mul_f32_dpp v228, v86, v242 quad_perm:[1,0,3,2] row_mask:0xf bank_mask:0xf
	v_mul_f32_e32 v86, v86, v242
	v_cvt_pk_bf16_f32 v86, v86, v228
	v_mul_f32_dpp v228, v87, v243 quad_perm:[1,0,3,2] row_mask:0xf bank_mask:0xf
	v_mul_f32_e32 v87, v87, v243
	v_cvt_pk_bf16_f32 v87, v87, v228
	v_mul_f32_dpp v228, v88, v244 quad_perm:[1,0,3,2] row_mask:0xf bank_mask:0xf
	v_mul_f32_e32 v88, v88, v244
	v_cvt_pk_bf16_f32 v88, v88, v228
	v_mul_f32_dpp v228, v89, v245 quad_perm:[1,0,3,2] row_mask:0xf bank_mask:0xf
	v_mul_f32_e32 v89, v89, v245
	v_cvt_pk_bf16_f32 v89, v89, v228
	v_mul_f32_dpp v228, v90, v246 quad_perm:[1,0,3,2] row_mask:0xf bank_mask:0xf
	v_mul_f32_e32 v90, v90, v246
	v_cvt_pk_bf16_f32 v90, v90, v228
	v_mul_f32_dpp v228, v91, v247 quad_perm:[1,0,3,2] row_mask:0xf bank_mask:0xf
	v_mul_f32_e32 v91, v91, v247
	v_cvt_pk_bf16_f32 v91, v91, v228
	v_mul_f32_dpp v228, v92, v248 quad_perm:[1,0,3,2] row_mask:0xf bank_mask:0xf
	v_mul_f32_e32 v92, v92, v248
	v_cvt_pk_bf16_f32 v92, v92, v228
	v_mul_f32_dpp v228, v93, v249 quad_perm:[1,0,3,2] row_mask:0xf bank_mask:0xf
	v_mul_f32_e32 v93, v93, v249
	v_cvt_pk_bf16_f32 v93, v93, v228
	v_mul_f32_dpp v228, v94, v250 quad_perm:[1,0,3,2] row_mask:0xf bank_mask:0xf
	v_mul_f32_e32 v94, v94, v250
	v_cvt_pk_bf16_f32 v94, v94, v228
	v_mul_f32_dpp v228, v95, v251 quad_perm:[1,0,3,2] row_mask:0xf bank_mask:0xf
	v_mul_f32_e32 v95, v95, v251
	v_cvt_pk_bf16_f32 v95, v95, v228
	v_mul_f32_dpp v228, v98, v236 quad_perm:[1,0,3,2] row_mask:0xf bank_mask:0xf
	v_mul_f32_e32 v98, v98, v236
	v_cvt_pk_bf16_f32 v98, v98, v228
	v_mul_f32_dpp v228, v99, v237 quad_perm:[1,0,3,2] row_mask:0xf bank_mask:0xf
	v_mul_f32_e32 v99, v99, v237
	v_cvt_pk_bf16_f32 v99, v99, v228
	v_mul_f32_dpp v228, v100, v238 quad_perm:[1,0,3,2] row_mask:0xf bank_mask:0xf
	v_mul_f32_e32 v100, v100, v238
	v_cvt_pk_bf16_f32 v100, v100, v228
	v_mul_f32_dpp v228, v101, v239 quad_perm:[1,0,3,2] row_mask:0xf bank_mask:0xf
	v_mul_f32_e32 v101, v101, v239
	v_cvt_pk_bf16_f32 v101, v101, v228
	v_mul_f32_dpp v228, v102, v240 quad_perm:[1,0,3,2] row_mask:0xf bank_mask:0xf
	v_mul_f32_e32 v102, v102, v240
	v_cvt_pk_bf16_f32 v102, v102, v228
	v_mul_f32_dpp v228, v103, v241 quad_perm:[1,0,3,2] row_mask:0xf bank_mask:0xf
	v_mul_f32_e32 v103, v103, v241
	v_cvt_pk_bf16_f32 v103, v103, v228
	v_mul_f32_dpp v228, v104, v242 quad_perm:[1,0,3,2] row_mask:0xf bank_mask:0xf
	v_mul_f32_e32 v104, v104, v242
	v_cvt_pk_bf16_f32 v104, v104, v228
	v_mul_f32_dpp v228, v105, v243 quad_perm:[1,0,3,2] row_mask:0xf bank_mask:0xf
	v_mul_f32_e32 v105, v105, v243
	v_cvt_pk_bf16_f32 v105, v105, v228
	v_mul_f32_dpp v228, v106, v244 quad_perm:[1,0,3,2] row_mask:0xf bank_mask:0xf
	v_mul_f32_e32 v106, v106, v244
	v_cvt_pk_bf16_f32 v106, v106, v228
	v_mul_f32_dpp v228, v107, v245 quad_perm:[1,0,3,2] row_mask:0xf bank_mask:0xf
	v_mul_f32_e32 v107, v107, v245
	v_cvt_pk_bf16_f32 v107, v107, v228
	v_mul_f32_dpp v228, v108, v246 quad_perm:[1,0,3,2] row_mask:0xf bank_mask:0xf
	v_mul_f32_e32 v108, v108, v246
	v_cvt_pk_bf16_f32 v108, v108, v228
	v_mul_f32_dpp v228, v109, v247 quad_perm:[1,0,3,2] row_mask:0xf bank_mask:0xf
	v_mul_f32_e32 v109, v109, v247
	v_cvt_pk_bf16_f32 v109, v109, v228
	v_mul_f32_dpp v228, v110, v248 quad_perm:[1,0,3,2] row_mask:0xf bank_mask:0xf
	v_mul_f32_e32 v110, v110, v248
	v_cvt_pk_bf16_f32 v110, v110, v228
	v_mul_f32_dpp v228, v111, v249 quad_perm:[1,0,3,2] row_mask:0xf bank_mask:0xf
	v_mul_f32_e32 v111, v111, v249
	v_cvt_pk_bf16_f32 v111, v111, v228
	v_mul_f32_dpp v228, v112, v250 quad_perm:[1,0,3,2] row_mask:0xf bank_mask:0xf
	v_mul_f32_e32 v112, v112, v250
	v_cvt_pk_bf16_f32 v112, v112, v228
	v_mul_f32_dpp v228, v113, v251 quad_perm:[1,0,3,2] row_mask:0xf bank_mask:0xf
	v_mul_f32_e32 v113, v113, v251
	v_cvt_pk_bf16_f32 v113, v113, v228
	v_mul_f32_dpp v228, v114, v236 quad_perm:[1,0,3,2] row_mask:0xf bank_mask:0xf
	v_mul_f32_e32 v114, v114, v236
	v_cvt_pk_bf16_f32 v114, v114, v228
	v_mul_f32_dpp v228, v115, v237 quad_perm:[1,0,3,2] row_mask:0xf bank_mask:0xf
	v_mul_f32_e32 v115, v115, v237
	v_cvt_pk_bf16_f32 v115, v115, v228
	v_mul_f32_dpp v228, v116, v238 quad_perm:[1,0,3,2] row_mask:0xf bank_mask:0xf
	v_mul_f32_e32 v116, v116, v238
	v_cvt_pk_bf16_f32 v116, v116, v228
	v_mul_f32_dpp v228, v117, v239 quad_perm:[1,0,3,2] row_mask:0xf bank_mask:0xf
	v_mul_f32_e32 v117, v117, v239
	v_cvt_pk_bf16_f32 v117, v117, v228
	v_mul_f32_dpp v228, v118, v240 quad_perm:[1,0,3,2] row_mask:0xf bank_mask:0xf
	v_mul_f32_e32 v118, v118, v240
	v_cvt_pk_bf16_f32 v118, v118, v228
	v_mul_f32_dpp v228, v119, v241 quad_perm:[1,0,3,2] row_mask:0xf bank_mask:0xf
	v_mul_f32_e32 v119, v119, v241
	v_cvt_pk_bf16_f32 v119, v119, v228
	v_mul_f32_dpp v228, v120, v242 quad_perm:[1,0,3,2] row_mask:0xf bank_mask:0xf
	v_mul_f32_e32 v120, v120, v242
	v_cvt_pk_bf16_f32 v120, v120, v228
	v_mul_f32_dpp v228, v121, v243 quad_perm:[1,0,3,2] row_mask:0xf bank_mask:0xf
	v_mul_f32_e32 v121, v121, v243
	v_cvt_pk_bf16_f32 v121, v121, v228
	v_mul_f32_dpp v228, v122, v244 quad_perm:[1,0,3,2] row_mask:0xf bank_mask:0xf
	v_mul_f32_e32 v122, v122, v244
	v_cvt_pk_bf16_f32 v122, v122, v228
	v_mul_f32_dpp v228, v123, v245 quad_perm:[1,0,3,2] row_mask:0xf bank_mask:0xf
	v_mul_f32_e32 v123, v123, v245
	v_cvt_pk_bf16_f32 v123, v123, v228
	v_mul_f32_dpp v228, v124, v246 quad_perm:[1,0,3,2] row_mask:0xf bank_mask:0xf
	v_mul_f32_e32 v124, v124, v246
	v_cvt_pk_bf16_f32 v124, v124, v228
	v_mul_f32_dpp v228, v125, v247 quad_perm:[1,0,3,2] row_mask:0xf bank_mask:0xf
	v_mul_f32_e32 v125, v125, v247
	v_cvt_pk_bf16_f32 v125, v125, v228
	v_mul_f32_dpp v228, v126, v248 quad_perm:[1,0,3,2] row_mask:0xf bank_mask:0xf
	v_mul_f32_e32 v126, v126, v248
	v_cvt_pk_bf16_f32 v126, v126, v228
	v_mul_f32_dpp v228, v127, v249 quad_perm:[1,0,3,2] row_mask:0xf bank_mask:0xf
	v_mul_f32_e32 v127, v127, v249
	v_cvt_pk_bf16_f32 v127, v127, v228
	v_mul_f32_dpp v228, v128, v250 quad_perm:[1,0,3,2] row_mask:0xf bank_mask:0xf
	v_mul_f32_e32 v128, v128, v250
	v_cvt_pk_bf16_f32 v128, v128, v228
	v_mul_f32_dpp v228, v129, v251 quad_perm:[1,0,3,2] row_mask:0xf bank_mask:0xf
	v_mul_f32_e32 v129, v129, v251
	v_cvt_pk_bf16_f32 v129, v129, v228
	s_barrier
	s_lshl_b32 s21, s15, 13
	v_lshlrev_b32_e32 v233, 10, v229
	v_lshl_add_u32 v233, v231, 1, v233
	v_add_u32_e32 v233, s21, v233
	v_mbcnt_lo_u32_b32 v234, -1, 0
	v_mbcnt_hi_u32_b32 v234, -1, v234
	v_lshlrev_b32_e32 v234, 4, v234
	v_add_u32_e32 v230, s21, v234
	v_add_u32_e32 v232, 0x1000, v230
	v_add_u32_e32 v234, s21, v234
	s_mov_b64 s[48:49], exec
	s_mov_b32 s50, 0x55555555
	s_mov_b32 s51, 0x55555555
	s_mov_b64 exec, s[50:51]
	ds_write_b32 v233, v0 offset:0
	ds_write_b32 v233, v1 offset:256
	ds_write_b32 v233, v2 offset:512
	ds_write_b32 v233, v3 offset:768
	ds_write_b32 v233, v4 offset:2048
	ds_write_b32 v233, v5 offset:2304
	ds_write_b32 v233, v6 offset:2560
	ds_write_b32 v233, v7 offset:2816
	ds_write_b32 v233, v8 offset:4096
	ds_write_b32 v233, v9 offset:4352
	ds_write_b32 v233, v10 offset:4608
	ds_write_b32 v233, v11 offset:4864
	ds_write_b32 v233, v12 offset:6144
	ds_write_b32 v233, v13 offset:6400
	ds_write_b32 v233, v14 offset:6656
	ds_write_b32 v233, v15 offset:6912
	ds_write_b32 v233, v16 offset:64
	ds_write_b32 v233, v17 offset:320
	ds_write_b32 v233, v18 offset:576
	ds_write_b32 v233, v19 offset:832
	ds_write_b32 v233, v20 offset:2112
	ds_write_b32 v233, v21 offset:2368
	ds_write_b32 v233, v22 offset:2624
	ds_write_b32 v233, v23 offset:2880
	ds_write_b32 v233, v24 offset:4160
	ds_write_b32 v233, v25 offset:4416
	ds_write_b32 v233, v26 offset:4672
	ds_write_b32 v233, v27 offset:4928
	ds_write_b32 v233, v28 offset:6208
	ds_write_b32 v233, v29 offset:6464
	ds_write_b32 v233, v30 offset:6720
	ds_write_b32 v233, v31 offset:6976
	ds_write_b32 v233, v32 offset:128
	ds_write_b32 v233, v33 offset:384
	ds_write_b32 v233, v34 offset:640
	ds_write_b32 v233, v35 offset:896
	ds_write_b32 v233, v36 offset:2176
	ds_write_b32 v233, v37 offset:2432
	ds_write_b32 v233, v38 offset:2688
	ds_write_b32 v233, v39 offset:2944
	ds_write_b32 v233, v40 offset:4224
	ds_write_b32 v233, v41 offset:4480
	ds_write_b32 v233, v42 offset:4736
	ds_write_b32 v233, v43 offset:4992
	ds_write_b32 v233, v44 offset:6272
	ds_write_b32 v233, v45 offset:6528
	ds_write_b32 v233, v46 offset:6784
	ds_write_b32 v233, v47 offset:7040
	ds_write_b32 v233, v48 offset:192
	ds_write_b32 v233, v49 offset:448
	ds_write_b32 v233, v50 offset:704
	ds_write_b32 v233, v51 offset:960
	ds_write_b32 v233, v52 offset:2240
	ds_write_b32 v233, v53 offset:2496
	ds_write_b32 v233, v54 offset:2752
	ds_write_b32 v233, v55 offset:3008
	ds_write_b32 v233, v56 offset:4288
	ds_write_b32 v233, v57 offset:4544
	ds_write_b32 v233, v58 offset:4800
	ds_write_b32 v233, v59 offset:5056
	ds_write_b32 v233, v60 offset:6336
	ds_write_b32 v233, v61 offset:6592
	ds_write_b32 v233, v62 offset:6848
	ds_write_b32 v233, v63 offset:7104
	s_mov_b64 exec, s[48:49]
	s_waitcnt lgkmcnt(0)
	ds_read_b128 v[236:239], v234 offset:0
	ds_read_b128 v[240:243], v234 offset:1024
	ds_read_b128 v[244:247], v234 offset:2048
	ds_read_b128 v[248:251], v234 offset:3072
	ds_read_b128 v[194:197], v234 offset:4096
	ds_read_b128 v[198:201], v234 offset:5120
	ds_read_b128 v[212:215], v234 offset:6144
	ds_read_b128 v[216:219], v234 offset:7168
	s_waitcnt lgkmcnt(0)
	global_store_dwordx4 v230, v[236:239], s[42:43] offset:0
	global_store_dwordx4 v230, v[240:243], s[42:43] offset:1024
	global_store_dwordx4 v230, v[244:247], s[42:43] offset:2048
	global_store_dwordx4 v230, v[248:251], s[42:43] offset:3072
	global_store_dwordx4 v232, v[194:197], s[42:43] offset:0
	global_store_dwordx4 v232, v[198:201], s[42:43] offset:1024
	global_store_dwordx4 v232, v[212:215], s[42:43] offset:2048
	global_store_dwordx4 v232, v[216:219], s[42:43] offset:3072
	s_nop 1
	s_mov_b64 exec, s[50:51]
	ds_write_b32 v233, v64 offset:0
	ds_write_b32 v233, v65 offset:256
	ds_write_b32 v233, v66 offset:512
	ds_write_b32 v233, v67 offset:768
	ds_write_b32 v233, v68 offset:2048
	ds_write_b32 v233, v69 offset:2304
	ds_write_b32 v233, v70 offset:2560
	ds_write_b32 v233, v71 offset:2816
	ds_write_b32 v233, v72 offset:4096
	ds_write_b32 v233, v73 offset:4352
	ds_write_b32 v233, v74 offset:4608
	ds_write_b32 v233, v75 offset:4864
	ds_write_b32 v233, v76 offset:6144
	ds_write_b32 v233, v77 offset:6400
	ds_write_b32 v233, v78 offset:6656
	ds_write_b32 v233, v79 offset:6912
	ds_write_b32 v233, v80 offset:64
	ds_write_b32 v233, v81 offset:320
	ds_write_b32 v233, v82 offset:576
	ds_write_b32 v233, v83 offset:832
	ds_write_b32 v233, v84 offset:2112
	ds_write_b32 v233, v85 offset:2368
	ds_write_b32 v233, v86 offset:2624
	ds_write_b32 v233, v87 offset:2880
	ds_write_b32 v233, v88 offset:4160
	ds_write_b32 v233, v89 offset:4416
	ds_write_b32 v233, v90 offset:4672
	ds_write_b32 v233, v91 offset:4928
	ds_write_b32 v233, v92 offset:6208
	ds_write_b32 v233, v93 offset:6464
	ds_write_b32 v233, v94 offset:6720
	ds_write_b32 v233, v95 offset:6976
	ds_write_b32 v233, v98 offset:128
	ds_write_b32 v233, v99 offset:384
	ds_write_b32 v233, v100 offset:640
	ds_write_b32 v233, v101 offset:896
	ds_write_b32 v233, v102 offset:2176
	ds_write_b32 v233, v103 offset:2432
	ds_write_b32 v233, v104 offset:2688
	ds_write_b32 v233, v105 offset:2944
	ds_write_b32 v233, v106 offset:4224
	ds_write_b32 v233, v107 offset:4480
	ds_write_b32 v233, v108 offset:4736
	ds_write_b32 v233, v109 offset:4992
	ds_write_b32 v233, v110 offset:6272
	ds_write_b32 v233, v111 offset:6528
	ds_write_b32 v233, v112 offset:6784
	ds_write_b32 v233, v113 offset:7040
	ds_write_b32 v233, v114 offset:192
	ds_write_b32 v233, v115 offset:448
	ds_write_b32 v233, v116 offset:704
	ds_write_b32 v233, v117 offset:960
	ds_write_b32 v233, v118 offset:2240
	ds_write_b32 v233, v119 offset:2496
	ds_write_b32 v233, v120 offset:2752
	ds_write_b32 v233, v121 offset:3008
	ds_write_b32 v233, v122 offset:4288
	ds_write_b32 v233, v123 offset:4544
	ds_write_b32 v233, v124 offset:4800
	ds_write_b32 v233, v125 offset:5056
	ds_write_b32 v233, v126 offset:6336
	ds_write_b32 v233, v127 offset:6592
	ds_write_b32 v233, v128 offset:6848
	ds_write_b32 v233, v129 offset:7104
	s_mov_b64 exec, s[48:49]
	s_waitcnt lgkmcnt(0)
	ds_read_b128 v[236:239], v234 offset:0
	ds_read_b128 v[240:243], v234 offset:1024
	ds_read_b128 v[244:247], v234 offset:2048
	ds_read_b128 v[248:251], v234 offset:3072
	ds_read_b128 v[194:197], v234 offset:4096
	ds_read_b128 v[198:201], v234 offset:5120
	ds_read_b128 v[212:215], v234 offset:6144
	ds_read_b128 v[216:219], v234 offset:7168
	s_waitcnt lgkmcnt(0)
	global_store_dwordx4 v230, v[236:239], s[44:45] offset:0
	global_store_dwordx4 v230, v[240:243], s[44:45] offset:1024
	global_store_dwordx4 v230, v[244:247], s[44:45] offset:2048
	global_store_dwordx4 v230, v[248:251], s[44:45] offset:3072
	global_store_dwordx4 v232, v[194:197], s[44:45] offset:0
	global_store_dwordx4 v232, v[198:201], s[44:45] offset:1024
	global_store_dwordx4 v232, v[212:215], s[44:45] offset:2048
	global_store_dwordx4 v232, v[216:219], s[44:45] offset:3072
	s_nop 1
	s_barrier
	s_branch .Lfa_epi_done
.Lfa_epi_c1:
	s_nop 7
	s_nop 7
	v_mbcnt_lo_u32_b32 v229, -1, 0
	v_mbcnt_hi_u32_b32 v229, -1, v229
	s_lshl_b32 s21, s15, 8
	s_add_i32 s21, s21, 0x18000
	v_and_b32_e32 v231, 31, v229
	v_lshl_add_u32 v230, v231, 2, s21
	v_lshrrev_b32_e32 v229, 5, v229
	v_lshl_add_u32 v232, v229, 4, s21
	ds_write_b32 v230, v202 offset:128
	s_waitcnt lgkmcnt(0)
	ds_read_b128 v[236:239], v232 offset:128
	ds_read_b128 v[240:243], v232 offset:160
	ds_read_b128 v[244:247], v232 offset:192
	ds_read_b128 v[248:251], v232 offset:224
	s_load_dwordx2 s[52:53], s[30:31], 0x98
	s_sub_i32 s21, s11, 2
	s_lshl_b32 s21, s21, 10
	v_lshlrev_b32_e32 v222, 2, v231
	s_waitcnt lgkmcnt(0)
	s_add_u32 s52, s52, s21
	s_addc_u32 s53, s53, 0
	global_load_dword v212, v222, s[52:53] offset:0
	global_load_dword v213, v222, s[52:53] offset:128
	global_load_dword v214, v222, s[52:53] offset:256
	global_load_dword v215, v222, s[52:53] offset:384
	global_load_dword v216, v222, s[52:53] offset:512
	global_load_dword v217, v222, s[52:53] offset:640
	global_load_dword v218, v222, s[52:53] offset:768
	global_load_dword v219, v222, s[52:53] offset:896
	s_lshl_b32 s21, s15, 13
	v_lshlrev_b32_e32 v221, 10, v229
	v_and_b32_e32 v222, 30, v231
	v_lshl_add_u32 v221, v222, 1, v221
	v_add_u32_e32 v221, s21, v221
	v_add_u32_e32 v234, 0x1000, v221
	v_and_b32_e32 v220, 1, v231
	v_xor_b32_e32 v220, 1, v220
	v_lshlrev_b32_e32 v220, 4, v220
	s_sub_u32 s48, s42, 0x400000
	s_subb_u32 s49, s43, 0
	s_sub_u32 s50, s44, 0x400000
	s_subb_u32 s51, s45, 0
	s_waitcnt vmcnt(0)
	v_rcp_f32_e32 v236, v236
	v_rcp_f32_e32 v237, v237
	v_rcp_f32_e32 v238, v238
	v_rcp_f32_e32 v239, v239
	v_rcp_f32_e32 v240, v240
	v_rcp_f32_e32 v241, v241
	v_rcp_f32_e32 v242, v242
	v_rcp_f32_e32 v243, v243
	v_rcp_f32_e32 v244, v244
	v_rcp_f32_e32 v245, v245
	v_rcp_f32_e32 v246, v246
	v_rcp_f32_e32 v247, v247
	v_rcp_f32_e32 v248, v248
	v_rcp_f32_e32 v249, v249
	v_rcp_f32_e32 v250, v250
	v_rcp_f32_e32 v251, v251
	v_mov_b32_e32 v146, 0
	v_mov_b32_e32 v147, 0
	v_mov_b32_e32 v148, 0
	v_mov_b32_e32 v149, 0
	v_mov_b32_e32 v150, 0
	v_mov_b32_e32 v151, 0
	v_mov_b32_e32 v152, 0
	v_mov_b32_e32 v153, 0
	v_mov_b32_e32 v154, 0
	v_mov_b32_e32 v155, 0
	v_mov_b32_e32 v156, 0
	v_mov_b32_e32 v157, 0
	v_mov_b32_e32 v158, 0
	v_mov_b32_e32 v159, 0
	v_mov_b32_e32 v160, 0
	v_mov_b32_e32 v161, 0
	global_load_dword v130, v221, s[48:49] offset:0 sc1
	global_load_dword v131, v221, s[48:49] offset:256 sc1
	global_load_dword v132, v221, s[48:49] offset:512 sc1
	global_load_dword v133, v221, s[48:49] offset:768 sc1
	global_load_dword v134, v221, s[48:49] offset:2048 sc1
	global_load_dword v135, v221, s[48:49] offset:2304 sc1
	global_load_dword v136, v221, s[48:49] offset:2560 sc1
	global_load_dword v137, v221, s[48:49] offset:2816 sc1
	global_load_dword v138, v234, s[48:49] offset:0 sc1
	global_load_dword v139, v234, s[48:49] offset:256 sc1
	global_load_dword v140, v234, s[48:49] offset:512 sc1
	global_load_dword v141, v234, s[48:49] offset:768 sc1
	global_load_dword v142, v234, s[48:49] offset:2048 sc1
	global_load_dword v143, v234, s[48:49] offset:2304 sc1
	global_load_dword v144, v234, s[48:49] offset:2560 sc1
	global_load_dword v145, v234, s[48:49] offset:2816 sc1
	v_mul_f32_e32 v0, v0, v236
	v_mul_f32_e32 v1, v1, v237
	v_mul_f32_e32 v2, v2, v238
	v_mul_f32_e32 v3, v3, v239
	v_mul_f32_e32 v4, v4, v240
	v_mul_f32_e32 v5, v5, v241
	v_mul_f32_e32 v6, v6, v242
	v_mul_f32_e32 v7, v7, v243
	v_mul_f32_e32 v8, v8, v244
	v_mul_f32_e32 v9, v9, v245
	v_mul_f32_e32 v10, v10, v246
	v_mul_f32_e32 v11, v11, v247
	v_mul_f32_e32 v12, v12, v248
	v_mul_f32_e32 v13, v13, v249
	v_mul_f32_e32 v14, v14, v250
	v_mul_f32_e32 v15, v15, v251
	s_waitcnt vmcnt(15)
	v_lshlrev_b32_e32 v130, v220, v130
	v_and_b32_e32 v130, 0xffff0000, v130
	v_fma_f32 v0, -v0, s79, v130
	v_fmac_f32_e32 v146, v0, v0
	s_waitcnt vmcnt(14)
	v_lshlrev_b32_e32 v131, v220, v131
	v_and_b32_e32 v131, 0xffff0000, v131
	v_fma_f32 v1, -v1, s79, v131
	v_fmac_f32_e32 v147, v1, v1
	s_waitcnt vmcnt(13)
	v_lshlrev_b32_e32 v132, v220, v132
	v_and_b32_e32 v132, 0xffff0000, v132
	v_fma_f32 v2, -v2, s79, v132
	v_fmac_f32_e32 v148, v2, v2
	s_waitcnt vmcnt(12)
	v_lshlrev_b32_e32 v133, v220, v133
	v_and_b32_e32 v133, 0xffff0000, v133
	v_fma_f32 v3, -v3, s79, v133
	v_fmac_f32_e32 v149, v3, v3
	s_waitcnt vmcnt(11)
	v_lshlrev_b32_e32 v134, v220, v134
	v_and_b32_e32 v134, 0xffff0000, v134
	v_fma_f32 v4, -v4, s79, v134
	v_fmac_f32_e32 v150, v4, v4
	s_waitcnt vmcnt(10)
	v_lshlrev_b32_e32 v135, v220, v135
	v_and_b32_e32 v135, 0xffff0000, v135
	v_fma_f32 v5, -v5, s79, v135
	v_fmac_f32_e32 v151, v5, v5
	s_waitcnt vmcnt(9)
	v_lshlrev_b32_e32 v136, v220, v136
	v_and_b32_e32 v136, 0xffff0000, v136
	v_fma_f32 v6, -v6, s79, v136
	v_fmac_f32_e32 v152, v6, v6
	s_waitcnt vmcnt(8)
	v_lshlrev_b32_e32 v137, v220, v137
	v_and_b32_e32 v137, 0xffff0000, v137
	v_fma_f32 v7, -v7, s79, v137
	v_fmac_f32_e32 v153, v7, v7
	s_waitcnt vmcnt(7)
	v_lshlrev_b32_e32 v138, v220, v138
	v_and_b32_e32 v138, 0xffff0000, v138
	v_fma_f32 v8, -v8, s79, v138
	v_fmac_f32_e32 v154, v8, v8
	s_waitcnt vmcnt(6)
	v_lshlrev_b32_e32 v139, v220, v139
	v_and_b32_e32 v139, 0xffff0000, v139
	v_fma_f32 v9, -v9, s79, v139
	v_fmac_f32_e32 v155, v9, v9
	s_waitcnt vmcnt(5)
	v_lshlrev_b32_e32 v140, v220, v140
	v_and_b32_e32 v140, 0xffff0000, v140
	v_fma_f32 v10, -v10, s79, v140
	v_fmac_f32_e32 v156, v10, v10
	s_waitcnt vmcnt(4)
	v_lshlrev_b32_e32 v141, v220, v141
	v_and_b32_e32 v141, 0xffff0000, v141
	v_fma_f32 v11, -v11, s79, v141
	v_fmac_f32_e32 v157, v11, v11
	s_waitcnt vmcnt(3)
	v_lshlrev_b32_e32 v142, v220, v142
	v_and_b32_e32 v142, 0xffff0000, v142
	v_fma_f32 v12, -v12, s79, v142
	v_fmac_f32_e32 v158, v12, v12
	s_waitcnt vmcnt(2)
	v_lshlrev_b32_e32 v143, v220, v143
	v_and_b32_e32 v143, 0xffff0000, v143
	v_fma_f32 v13, -v13, s79, v143
	v_fmac_f32_e32 v159, v13, v13
	s_waitcnt vmcnt(1)
	v_lshlrev_b32_e32 v144, v220, v144
	v_and_b32_e32 v144, 0xffff0000, v144
	v_fma_f32 v14, -v14, s79, v144
	v_fmac_f32_e32 v160, v14, v14
	s_waitcnt vmcnt(0)
	v_lshlrev_b32_e32 v145, v220, v145
	v_and_b32_e32 v145, 0xffff0000, v145
	v_fma_f32 v15, -v15, s79, v145
	v_fmac_f32_e32 v161, v15, v15
	global_load_dword v130, v221, s[48:49] offset:64 sc1
	global_load_dword v131, v221, s[48:49] offset:320 sc1
	global_load_dword v132, v221, s[48:49] offset:576 sc1
	global_load_dword v133, v221, s[48:49] offset:832 sc1
	global_load_dword v134, v221, s[48:49] offset:2112 sc1
	global_load_dword v135, v221, s[48:49] offset:2368 sc1
	global_load_dword v136, v221, s[48:49] offset:2624 sc1
	global_load_dword v137, v221, s[48:49] offset:2880 sc1
	global_load_dword v138, v234, s[48:49] offset:64 sc1
	global_load_dword v139, v234, s[48:49] offset:320 sc1
	global_load_dword v140, v234, s[48:49] offset:576 sc1
	global_load_dword v141, v234, s[48:49] offset:832 sc1
	global_load_dword v142, v234, s[48:49] offset:2112 sc1
	global_load_dword v143, v234, s[48:49] offset:2368 sc1
	global_load_dword v144, v234, s[48:49] offset:2624 sc1
	global_load_dword v145, v234, s[48:49] offset:2880 sc1
	v_mul_f32_e32 v16, v16, v236
	v_mul_f32_e32 v17, v17, v237
	v_mul_f32_e32 v18, v18, v238
	v_mul_f32_e32 v19, v19, v239
	v_mul_f32_e32 v20, v20, v240
	v_mul_f32_e32 v21, v21, v241
	v_mul_f32_e32 v22, v22, v242
	v_mul_f32_e32 v23, v23, v243
	v_mul_f32_e32 v24, v24, v244
	v_mul_f32_e32 v25, v25, v245
	v_mul_f32_e32 v26, v26, v246
	v_mul_f32_e32 v27, v27, v247
	v_mul_f32_e32 v28, v28, v248
	v_mul_f32_e32 v29, v29, v249
	v_mul_f32_e32 v30, v30, v250
	v_mul_f32_e32 v31, v31, v251
	s_waitcnt vmcnt(15)
	v_lshlrev_b32_e32 v130, v220, v130
	v_and_b32_e32 v130, 0xffff0000, v130
	v_fma_f32 v16, -v16, s79, v130
	v_fmac_f32_e32 v146, v16, v16
	s_waitcnt vmcnt(14)
	v_lshlrev_b32_e32 v131, v220, v131
	v_and_b32_e32 v131, 0xffff0000, v131
	v_fma_f32 v17, -v17, s79, v131
	v_fmac_f32_e32 v147, v17, v17
	s_waitcnt vmcnt(13)
	v_lshlrev_b32_e32 v132, v220, v132
	v_and_b32_e32 v132, 0xffff0000, v132
	v_fma_f32 v18, -v18, s79, v132
	v_fmac_f32_e32 v148, v18, v18
	s_waitcnt vmcnt(12)
	v_lshlrev_b32_e32 v133, v220, v133
	v_and_b32_e32 v133, 0xffff0000, v133
	v_fma_f32 v19, -v19, s79, v133
	v_fmac_f32_e32 v149, v19, v19
	s_waitcnt vmcnt(11)
	v_lshlrev_b32_e32 v134, v220, v134
	v_and_b32_e32 v134, 0xffff0000, v134
	v_fma_f32 v20, -v20, s79, v134
	v_fmac_f32_e32 v150, v20, v20
	s_waitcnt vmcnt(10)
	v_lshlrev_b32_e32 v135, v220, v135
	v_and_b32_e32 v135, 0xffff0000, v135
	v_fma_f32 v21, -v21, s79, v135
	v_fmac_f32_e32 v151, v21, v21
	s_waitcnt vmcnt(9)
	v_lshlrev_b32_e32 v136, v220, v136
	v_and_b32_e32 v136, 0xffff0000, v136
	v_fma_f32 v22, -v22, s79, v136
	v_fmac_f32_e32 v152, v22, v22
	s_waitcnt vmcnt(8)
	v_lshlrev_b32_e32 v137, v220, v137
	v_and_b32_e32 v137, 0xffff0000, v137
	v_fma_f32 v23, -v23, s79, v137
	v_fmac_f32_e32 v153, v23, v23
	s_waitcnt vmcnt(7)
	v_lshlrev_b32_e32 v138, v220, v138
	v_and_b32_e32 v138, 0xffff0000, v138
	v_fma_f32 v24, -v24, s79, v138
	v_fmac_f32_e32 v154, v24, v24
	s_waitcnt vmcnt(6)
	v_lshlrev_b32_e32 v139, v220, v139
	v_and_b32_e32 v139, 0xffff0000, v139
	v_fma_f32 v25, -v25, s79, v139
	v_fmac_f32_e32 v155, v25, v25
	s_waitcnt vmcnt(5)
	v_lshlrev_b32_e32 v140, v220, v140
	v_and_b32_e32 v140, 0xffff0000, v140
	v_fma_f32 v26, -v26, s79, v140
	v_fmac_f32_e32 v156, v26, v26
	s_waitcnt vmcnt(4)
	v_lshlrev_b32_e32 v141, v220, v141
	v_and_b32_e32 v141, 0xffff0000, v141
	v_fma_f32 v27, -v27, s79, v141
	v_fmac_f32_e32 v157, v27, v27
	s_waitcnt vmcnt(3)
	v_lshlrev_b32_e32 v142, v220, v142
	v_and_b32_e32 v142, 0xffff0000, v142
	v_fma_f32 v28, -v28, s79, v142
	v_fmac_f32_e32 v158, v28, v28
	s_waitcnt vmcnt(2)
	v_lshlrev_b32_e32 v143, v220, v143
	v_and_b32_e32 v143, 0xffff0000, v143
	v_fma_f32 v29, -v29, s79, v143
	v_fmac_f32_e32 v159, v29, v29
	s_waitcnt vmcnt(1)
	v_lshlrev_b32_e32 v144, v220, v144
	v_and_b32_e32 v144, 0xffff0000, v144
	v_fma_f32 v30, -v30, s79, v144
	v_fmac_f32_e32 v160, v30, v30
	s_waitcnt vmcnt(0)
	v_lshlrev_b32_e32 v145, v220, v145
	v_and_b32_e32 v145, 0xffff0000, v145
	v_fma_f32 v31, -v31, s79, v145
	v_fmac_f32_e32 v161, v31, v31
	global_load_dword v130, v221, s[48:49] offset:128 sc1
	global_load_dword v131, v221, s[48:49] offset:384 sc1
	global_load_dword v132, v221, s[48:49] offset:640 sc1
	global_load_dword v133, v221, s[48:49] offset:896 sc1
	global_load_dword v134, v221, s[48:49] offset:2176 sc1
	global_load_dword v135, v221, s[48:49] offset:2432 sc1
	global_load_dword v136, v221, s[48:49] offset:2688 sc1
	global_load_dword v137, v221, s[48:49] offset:2944 sc1
	global_load_dword v138, v234, s[48:49] offset:128 sc1
	global_load_dword v139, v234, s[48:49] offset:384 sc1
	global_load_dword v140, v234, s[48:49] offset:640 sc1
	global_load_dword v141, v234, s[48:49] offset:896 sc1
	global_load_dword v142, v234, s[48:49] offset:2176 sc1
	global_load_dword v143, v234, s[48:49] offset:2432 sc1
	global_load_dword v144, v234, s[48:49] offset:2688 sc1
	global_load_dword v145, v234, s[48:49] offset:2944 sc1
	v_mul_f32_e32 v32, v32, v236
	v_mul_f32_e32 v33, v33, v237
	v_mul_f32_e32 v34, v34, v238
	v_mul_f32_e32 v35, v35, v239
	v_mul_f32_e32 v36, v36, v240
	v_mul_f32_e32 v37, v37, v241
	v_mul_f32_e32 v38, v38, v242
	v_mul_f32_e32 v39, v39, v243
	v_mul_f32_e32 v40, v40, v244
	v_mul_f32_e32 v41, v41, v245
	v_mul_f32_e32 v42, v42, v246
	v_mul_f32_e32 v43, v43, v247
	v_mul_f32_e32 v44, v44, v248
	v_mul_f32_e32 v45, v45, v249
	v_mul_f32_e32 v46, v46, v250
	v_mul_f32_e32 v47, v47, v251
	s_waitcnt vmcnt(15)
	v_lshlrev_b32_e32 v130, v220, v130
	v_and_b32_e32 v130, 0xffff0000, v130
	v_fma_f32 v32, -v32, s79, v130
	v_fmac_f32_e32 v146, v32, v32
	s_waitcnt vmcnt(14)
	v_lshlrev_b32_e32 v131, v220, v131
	v_and_b32_e32 v131, 0xffff0000, v131
	v_fma_f32 v33, -v33, s79, v131
	v_fmac_f32_e32 v147, v33, v33
	s_waitcnt vmcnt(13)
	v_lshlrev_b32_e32 v132, v220, v132
	v_and_b32_e32 v132, 0xffff0000, v132
	v_fma_f32 v34, -v34, s79, v132
	v_fmac_f32_e32 v148, v34, v34
	s_waitcnt vmcnt(12)
	v_lshlrev_b32_e32 v133, v220, v133
	v_and_b32_e32 v133, 0xffff0000, v133
	v_fma_f32 v35, -v35, s79, v133
	v_fmac_f32_e32 v149, v35, v35
	s_waitcnt vmcnt(11)
	v_lshlrev_b32_e32 v134, v220, v134
	v_and_b32_e32 v134, 0xffff0000, v134
	v_fma_f32 v36, -v36, s79, v134
	v_fmac_f32_e32 v150, v36, v36
	s_waitcnt vmcnt(10)
	v_lshlrev_b32_e32 v135, v220, v135
	v_and_b32_e32 v135, 0xffff0000, v135
	v_fma_f32 v37, -v37, s79, v135
	v_fmac_f32_e32 v151, v37, v37
	s_waitcnt vmcnt(9)
	v_lshlrev_b32_e32 v136, v220, v136
	v_and_b32_e32 v136, 0xffff0000, v136
	v_fma_f32 v38, -v38, s79, v136
	v_fmac_f32_e32 v152, v38, v38
	s_waitcnt vmcnt(8)
	v_lshlrev_b32_e32 v137, v220, v137
	v_and_b32_e32 v137, 0xffff0000, v137
	v_fma_f32 v39, -v39, s79, v137
	v_fmac_f32_e32 v153, v39, v39
	s_waitcnt vmcnt(7)
	v_lshlrev_b32_e32 v138, v220, v138
	v_and_b32_e32 v138, 0xffff0000, v138
	v_fma_f32 v40, -v40, s79, v138
	v_fmac_f32_e32 v154, v40, v40
	s_waitcnt vmcnt(6)
	v_lshlrev_b32_e32 v139, v220, v139
	v_and_b32_e32 v139, 0xffff0000, v139
	v_fma_f32 v41, -v41, s79, v139
	v_fmac_f32_e32 v155, v41, v41
	s_waitcnt vmcnt(5)
	v_lshlrev_b32_e32 v140, v220, v140
	v_and_b32_e32 v140, 0xffff0000, v140
	v_fma_f32 v42, -v42, s79, v140
	v_fmac_f32_e32 v156, v42, v42
	s_waitcnt vmcnt(4)
	v_lshlrev_b32_e32 v141, v220, v141
	v_and_b32_e32 v141, 0xffff0000, v141
	v_fma_f32 v43, -v43, s79, v141
	v_fmac_f32_e32 v157, v43, v43
	s_waitcnt vmcnt(3)
	v_lshlrev_b32_e32 v142, v220, v142
	v_and_b32_e32 v142, 0xffff0000, v142
	v_fma_f32 v44, -v44, s79, v142
	v_fmac_f32_e32 v158, v44, v44
	s_waitcnt vmcnt(2)
	v_lshlrev_b32_e32 v143, v220, v143
	v_and_b32_e32 v143, 0xffff0000, v143
	v_fma_f32 v45, -v45, s79, v143
	v_fmac_f32_e32 v159, v45, v45
	s_waitcnt vmcnt(1)
	v_lshlrev_b32_e32 v144, v220, v144
	v_and_b32_e32 v144, 0xffff0000, v144
	v_fma_f32 v46, -v46, s79, v144
	v_fmac_f32_e32 v160, v46, v46
	s_waitcnt vmcnt(0)
	v_lshlrev_b32_e32 v145, v220, v145
	v_and_b32_e32 v145, 0xffff0000, v145
	v_fma_f32 v47, -v47, s79, v145
	v_fmac_f32_e32 v161, v47, v47
	global_load_dword v130, v221, s[48:49] offset:192 sc1
	global_load_dword v131, v221, s[48:49] offset:448 sc1
	global_load_dword v132, v221, s[48:49] offset:704 sc1
	global_load_dword v133, v221, s[48:49] offset:960 sc1
	global_load_dword v134, v221, s[48:49] offset:2240 sc1
	global_load_dword v135, v221, s[48:49] offset:2496 sc1
	global_load_dword v136, v221, s[48:49] offset:2752 sc1
	global_load_dword v137, v221, s[48:49] offset:3008 sc1
	global_load_dword v138, v234, s[48:49] offset:192 sc1
	global_load_dword v139, v234, s[48:49] offset:448 sc1
	global_load_dword v140, v234, s[48:49] offset:704 sc1
	global_load_dword v141, v234, s[48:49] offset:960 sc1
	global_load_dword v142, v234, s[48:49] offset:2240 sc1
	global_load_dword v143, v234, s[48:49] offset:2496 sc1
	global_load_dword v144, v234, s[48:49] offset:2752 sc1
	global_load_dword v145, v234, s[48:49] offset:3008 sc1
	v_mul_f32_e32 v48, v48, v236
	v_mul_f32_e32 v49, v49, v237
	v_mul_f32_e32 v50, v50, v238
	v_mul_f32_e32 v51, v51, v239
	v_mul_f32_e32 v52, v52, v240
	v_mul_f32_e32 v53, v53, v241
	v_mul_f32_e32 v54, v54, v242
	v_mul_f32_e32 v55, v55, v243
	v_mul_f32_e32 v56, v56, v244
	v_mul_f32_e32 v57, v57, v245
	v_mul_f32_e32 v58, v58, v246
	v_mul_f32_e32 v59, v59, v247
	v_mul_f32_e32 v60, v60, v248
	v_mul_f32_e32 v61, v61, v249
	v_mul_f32_e32 v62, v62, v250
	v_mul_f32_e32 v63, v63, v251
	s_waitcnt vmcnt(15)
	v_lshlrev_b32_e32 v130, v220, v130
	v_and_b32_e32 v130, 0xffff0000, v130
	v_fma_f32 v48, -v48, s79, v130
	v_fmac_f32_e32 v146, v48, v48
	s_waitcnt vmcnt(14)
	v_lshlrev_b32_e32 v131, v220, v131
	v_and_b32_e32 v131, 0xffff0000, v131
	v_fma_f32 v49, -v49, s79, v131
	v_fmac_f32_e32 v147, v49, v49
	s_waitcnt vmcnt(13)
	v_lshlrev_b32_e32 v132, v220, v132
	v_and_b32_e32 v132, 0xffff0000, v132
	v_fma_f32 v50, -v50, s79, v132
	v_fmac_f32_e32 v148, v50, v50
	s_waitcnt vmcnt(12)
	v_lshlrev_b32_e32 v133, v220, v133
	v_and_b32_e32 v133, 0xffff0000, v133
	v_fma_f32 v51, -v51, s79, v133
	v_fmac_f32_e32 v149, v51, v51
	s_waitcnt vmcnt(11)
	v_lshlrev_b32_e32 v134, v220, v134
	v_and_b32_e32 v134, 0xffff0000, v134
	v_fma_f32 v52, -v52, s79, v134
	v_fmac_f32_e32 v150, v52, v52
	s_waitcnt vmcnt(10)
	v_lshlrev_b32_e32 v135, v220, v135
	v_and_b32_e32 v135, 0xffff0000, v135
	v_fma_f32 v53, -v53, s79, v135
	v_fmac_f32_e32 v151, v53, v53
	s_waitcnt vmcnt(9)
	v_lshlrev_b32_e32 v136, v220, v136
	v_and_b32_e32 v136, 0xffff0000, v136
	v_fma_f32 v54, -v54, s79, v136
	v_fmac_f32_e32 v152, v54, v54
	s_waitcnt vmcnt(8)
	v_lshlrev_b32_e32 v137, v220, v137
	v_and_b32_e32 v137, 0xffff0000, v137
	v_fma_f32 v55, -v55, s79, v137
	v_fmac_f32_e32 v153, v55, v55
	s_waitcnt vmcnt(7)
	v_lshlrev_b32_e32 v138, v220, v138
	v_and_b32_e32 v138, 0xffff0000, v138
	v_fma_f32 v56, -v56, s79, v138
	v_fmac_f32_e32 v154, v56, v56
	s_waitcnt vmcnt(6)
	v_lshlrev_b32_e32 v139, v220, v139
	v_and_b32_e32 v139, 0xffff0000, v139
	v_fma_f32 v57, -v57, s79, v139
	v_fmac_f32_e32 v155, v57, v57
	s_waitcnt vmcnt(5)
	v_lshlrev_b32_e32 v140, v220, v140
	v_and_b32_e32 v140, 0xffff0000, v140
	v_fma_f32 v58, -v58, s79, v140
	v_fmac_f32_e32 v156, v58, v58
	s_waitcnt vmcnt(4)
	v_lshlrev_b32_e32 v141, v220, v141
	v_and_b32_e32 v141, 0xffff0000, v141
	v_fma_f32 v59, -v59, s79, v141
	v_fmac_f32_e32 v157, v59, v59
	s_waitcnt vmcnt(3)
	v_lshlrev_b32_e32 v142, v220, v142
	v_and_b32_e32 v142, 0xffff0000, v142
	v_fma_f32 v60, -v60, s79, v142
	v_fmac_f32_e32 v158, v60, v60
	s_waitcnt vmcnt(2)
	v_lshlrev_b32_e32 v143, v220, v143
	v_and_b32_e32 v143, 0xffff0000, v143
	v_fma_f32 v61, -v61, s79, v143
	v_fmac_f32_e32 v159, v61, v61
	s_waitcnt vmcnt(1)
	v_lshlrev_b32_e32 v144, v220, v144
	v_and_b32_e32 v144, 0xffff0000, v144
	v_fma_f32 v62, -v62, s79, v144
	v_fmac_f32_e32 v160, v62, v62
	s_waitcnt vmcnt(0)
	v_lshlrev_b32_e32 v145, v220, v145
	v_and_b32_e32 v145, 0xffff0000, v145
	v_fma_f32 v63, -v63, s79, v145
	v_fmac_f32_e32 v161, v63, v63
	global_load_dword v130, v221, s[50:51] offset:0 sc1
	global_load_dword v131, v221, s[50:51] offset:256 sc1
	global_load_dword v132, v221, s[50:51] offset:512 sc1
	global_load_dword v133, v221, s[50:51] offset:768 sc1
	global_load_dword v134, v221, s[50:51] offset:2048 sc1
	global_load_dword v135, v221, s[50:51] offset:2304 sc1
	global_load_dword v136, v221, s[50:51] offset:2560 sc1
	global_load_dword v137, v221, s[50:51] offset:2816 sc1
	global_load_dword v138, v234, s[50:51] offset:0 sc1
	global_load_dword v139, v234, s[50:51] offset:256 sc1
	global_load_dword v140, v234, s[50:51] offset:512 sc1
	global_load_dword v141, v234, s[50:51] offset:768 sc1
	global_load_dword v142, v234, s[50:51] offset:2048 sc1
	global_load_dword v143, v234, s[50:51] offset:2304 sc1
	global_load_dword v144, v234, s[50:51] offset:2560 sc1
	global_load_dword v145, v234, s[50:51] offset:2816 sc1
	v_mul_f32_e32 v64, v64, v236
	v_mul_f32_e32 v65, v65, v237
	v_mul_f32_e32 v66, v66, v238
	v_mul_f32_e32 v67, v67, v239
	v_mul_f32_e32 v68, v68, v240
	v_mul_f32_e32 v69, v69, v241
	v_mul_f32_e32 v70, v70, v242
	v_mul_f32_e32 v71, v71, v243
	v_mul_f32_e32 v72, v72, v244
	v_mul_f32_e32 v73, v73, v245
	v_mul_f32_e32 v74, v74, v246
	v_mul_f32_e32 v75, v75, v247
	v_mul_f32_e32 v76, v76, v248
	v_mul_f32_e32 v77, v77, v249
	v_mul_f32_e32 v78, v78, v250
	v_mul_f32_e32 v79, v79, v251
	s_waitcnt vmcnt(15)
	v_lshlrev_b32_e32 v130, v220, v130
	v_and_b32_e32 v130, 0xffff0000, v130
	v_fma_f32 v64, -v64, s79, v130
	v_fmac_f32_e32 v146, v64, v64
	s_waitcnt vmcnt(14)
	v_lshlrev_b32_e32 v131, v220, v131
	v_and_b32_e32 v131, 0xffff0000, v131
	v_fma_f32 v65, -v65, s79, v131
	v_fmac_f32_e32 v147, v65, v65
	s_waitcnt vmcnt(13)
	v_lshlrev_b32_e32 v132, v220, v132
	v_and_b32_e32 v132, 0xffff0000, v132
	v_fma_f32 v66, -v66, s79, v132
	v_fmac_f32_e32 v148, v66, v66
	s_waitcnt vmcnt(12)
	v_lshlrev_b32_e32 v133, v220, v133
	v_and_b32_e32 v133, 0xffff0000, v133
	v_fma_f32 v67, -v67, s79, v133
	v_fmac_f32_e32 v149, v67, v67
	s_waitcnt vmcnt(11)
	v_lshlrev_b32_e32 v134, v220, v134
	v_and_b32_e32 v134, 0xffff0000, v134
	v_fma_f32 v68, -v68, s79, v134
	v_fmac_f32_e32 v150, v68, v68
	s_waitcnt vmcnt(10)
	v_lshlrev_b32_e32 v135, v220, v135
	v_and_b32_e32 v135, 0xffff0000, v135
	v_fma_f32 v69, -v69, s79, v135
	v_fmac_f32_e32 v151, v69, v69
	s_waitcnt vmcnt(9)
	v_lshlrev_b32_e32 v136, v220, v136
	v_and_b32_e32 v136, 0xffff0000, v136
	v_fma_f32 v70, -v70, s79, v136
	v_fmac_f32_e32 v152, v70, v70
	s_waitcnt vmcnt(8)
	v_lshlrev_b32_e32 v137, v220, v137
	v_and_b32_e32 v137, 0xffff0000, v137
	v_fma_f32 v71, -v71, s79, v137
	v_fmac_f32_e32 v153, v71, v71
	s_waitcnt vmcnt(7)
	v_lshlrev_b32_e32 v138, v220, v138
	v_and_b32_e32 v138, 0xffff0000, v138
	v_fma_f32 v72, -v72, s79, v138
	v_fmac_f32_e32 v154, v72, v72
	s_waitcnt vmcnt(6)
	v_lshlrev_b32_e32 v139, v220, v139
	v_and_b32_e32 v139, 0xffff0000, v139
	v_fma_f32 v73, -v73, s79, v139
	v_fmac_f32_e32 v155, v73, v73
	s_waitcnt vmcnt(5)
	v_lshlrev_b32_e32 v140, v220, v140
	v_and_b32_e32 v140, 0xffff0000, v140
	v_fma_f32 v74, -v74, s79, v140
	v_fmac_f32_e32 v156, v74, v74
	s_waitcnt vmcnt(4)
	v_lshlrev_b32_e32 v141, v220, v141
	v_and_b32_e32 v141, 0xffff0000, v141
	v_fma_f32 v75, -v75, s79, v141
	v_fmac_f32_e32 v157, v75, v75
	s_waitcnt vmcnt(3)
	v_lshlrev_b32_e32 v142, v220, v142
	v_and_b32_e32 v142, 0xffff0000, v142
	v_fma_f32 v76, -v76, s79, v142
	v_fmac_f32_e32 v158, v76, v76
	s_waitcnt vmcnt(2)
	v_lshlrev_b32_e32 v143, v220, v143
	v_and_b32_e32 v143, 0xffff0000, v143
	v_fma_f32 v77, -v77, s79, v143
	v_fmac_f32_e32 v159, v77, v77
	s_waitcnt vmcnt(1)
	v_lshlrev_b32_e32 v144, v220, v144
	v_and_b32_e32 v144, 0xffff0000, v144
	v_fma_f32 v78, -v78, s79, v144
	v_fmac_f32_e32 v160, v78, v78
	s_waitcnt vmcnt(0)
	v_lshlrev_b32_e32 v145, v220, v145
	v_and_b32_e32 v145, 0xffff0000, v145
	v_fma_f32 v79, -v79, s79, v145
	v_fmac_f32_e32 v161, v79, v79
	global_load_dword v130, v221, s[50:51] offset:64 sc1
	global_load_dword v131, v221, s[50:51] offset:320 sc1
	global_load_dword v132, v221, s[50:51] offset:576 sc1
	global_load_dword v133, v221, s[50:51] offset:832 sc1
	global_load_dword v134, v221, s[50:51] offset:2112 sc1
	global_load_dword v135, v221, s[50:51] offset:2368 sc1
	global_load_dword v136, v221, s[50:51] offset:2624 sc1
	global_load_dword v137, v221, s[50:51] offset:2880 sc1
	global_load_dword v138, v234, s[50:51] offset:64 sc1
	global_load_dword v139, v234, s[50:51] offset:320 sc1
	global_load_dword v140, v234, s[50:51] offset:576 sc1
	global_load_dword v141, v234, s[50:51] offset:832 sc1
	global_load_dword v142, v234, s[50:51] offset:2112 sc1
	global_load_dword v143, v234, s[50:51] offset:2368 sc1
	global_load_dword v144, v234, s[50:51] offset:2624 sc1
	global_load_dword v145, v234, s[50:51] offset:2880 sc1
	v_mul_f32_e32 v80, v80, v236
	v_mul_f32_e32 v81, v81, v237
	v_mul_f32_e32 v82, v82, v238
	v_mul_f32_e32 v83, v83, v239
	v_mul_f32_e32 v84, v84, v240
	v_mul_f32_e32 v85, v85, v241
	v_mul_f32_e32 v86, v86, v242
	v_mul_f32_e32 v87, v87, v243
	v_mul_f32_e32 v88, v88, v244
	v_mul_f32_e32 v89, v89, v245
	v_mul_f32_e32 v90, v90, v246
	v_mul_f32_e32 v91, v91, v247
	v_mul_f32_e32 v92, v92, v248
	v_mul_f32_e32 v93, v93, v249
	v_mul_f32_e32 v94, v94, v250
	v_mul_f32_e32 v95, v95, v251
	s_waitcnt vmcnt(15)
	v_lshlrev_b32_e32 v130, v220, v130
	v_and_b32_e32 v130, 0xffff0000, v130
	v_fma_f32 v80, -v80, s79, v130
	v_fmac_f32_e32 v146, v80, v80
	s_waitcnt vmcnt(14)
	v_lshlrev_b32_e32 v131, v220, v131
	v_and_b32_e32 v131, 0xffff0000, v131
	v_fma_f32 v81, -v81, s79, v131
	v_fmac_f32_e32 v147, v81, v81
	s_waitcnt vmcnt(13)
	v_lshlrev_b32_e32 v132, v220, v132
	v_and_b32_e32 v132, 0xffff0000, v132
	v_fma_f32 v82, -v82, s79, v132
	v_fmac_f32_e32 v148, v82, v82
	s_waitcnt vmcnt(12)
	v_lshlrev_b32_e32 v133, v220, v133
	v_and_b32_e32 v133, 0xffff0000, v133
	v_fma_f32 v83, -v83, s79, v133
	v_fmac_f32_e32 v149, v83, v83
	s_waitcnt vmcnt(11)
	v_lshlrev_b32_e32 v134, v220, v134
	v_and_b32_e32 v134, 0xffff0000, v134
	v_fma_f32 v84, -v84, s79, v134
	v_fmac_f32_e32 v150, v84, v84
	s_waitcnt vmcnt(10)
	v_lshlrev_b32_e32 v135, v220, v135
	v_and_b32_e32 v135, 0xffff0000, v135
	v_fma_f32 v85, -v85, s79, v135
	v_fmac_f32_e32 v151, v85, v85
	s_waitcnt vmcnt(9)
	v_lshlrev_b32_e32 v136, v220, v136
	v_and_b32_e32 v136, 0xffff0000, v136
	v_fma_f32 v86, -v86, s79, v136
	v_fmac_f32_e32 v152, v86, v86
	s_waitcnt vmcnt(8)
	v_lshlrev_b32_e32 v137, v220, v137
	v_and_b32_e32 v137, 0xffff0000, v137
	v_fma_f32 v87, -v87, s79, v137
	v_fmac_f32_e32 v153, v87, v87
	s_waitcnt vmcnt(7)
	v_lshlrev_b32_e32 v138, v220, v138
	v_and_b32_e32 v138, 0xffff0000, v138
	v_fma_f32 v88, -v88, s79, v138
	v_fmac_f32_e32 v154, v88, v88
	s_waitcnt vmcnt(6)
	v_lshlrev_b32_e32 v139, v220, v139
	v_and_b32_e32 v139, 0xffff0000, v139
	v_fma_f32 v89, -v89, s79, v139
	v_fmac_f32_e32 v155, v89, v89
	s_waitcnt vmcnt(5)
	v_lshlrev_b32_e32 v140, v220, v140
	v_and_b32_e32 v140, 0xffff0000, v140
	v_fma_f32 v90, -v90, s79, v140
	v_fmac_f32_e32 v156, v90, v90
	s_waitcnt vmcnt(4)
	v_lshlrev_b32_e32 v141, v220, v141
	v_and_b32_e32 v141, 0xffff0000, v141
	v_fma_f32 v91, -v91, s79, v141
	v_fmac_f32_e32 v157, v91, v91
	s_waitcnt vmcnt(3)
	v_lshlrev_b32_e32 v142, v220, v142
	v_and_b32_e32 v142, 0xffff0000, v142
	v_fma_f32 v92, -v92, s79, v142
	v_fmac_f32_e32 v158, v92, v92
	s_waitcnt vmcnt(2)
	v_lshlrev_b32_e32 v143, v220, v143
	v_and_b32_e32 v143, 0xffff0000, v143
	v_fma_f32 v93, -v93, s79, v143
	v_fmac_f32_e32 v159, v93, v93
	s_waitcnt vmcnt(1)
	v_lshlrev_b32_e32 v144, v220, v144
	v_and_b32_e32 v144, 0xffff0000, v144
	v_fma_f32 v94, -v94, s79, v144
	v_fmac_f32_e32 v160, v94, v94
	s_waitcnt vmcnt(0)
	v_lshlrev_b32_e32 v145, v220, v145
	v_and_b32_e32 v145, 0xffff0000, v145
	v_fma_f32 v95, -v95, s79, v145
	v_fmac_f32_e32 v161, v95, v95
	global_load_dword v130, v221, s[50:51] offset:128 sc1
	global_load_dword v131, v221, s[50:51] offset:384 sc1
	global_load_dword v132, v221, s[50:51] offset:640 sc1
	global_load_dword v133, v221, s[50:51] offset:896 sc1
	global_load_dword v134, v221, s[50:51] offset:2176 sc1
	global_load_dword v135, v221, s[50:51] offset:2432 sc1
	global_load_dword v136, v221, s[50:51] offset:2688 sc1
	global_load_dword v137, v221, s[50:51] offset:2944 sc1
	global_load_dword v138, v234, s[50:51] offset:128 sc1
	global_load_dword v139, v234, s[50:51] offset:384 sc1
	global_load_dword v140, v234, s[50:51] offset:640 sc1
	global_load_dword v141, v234, s[50:51] offset:896 sc1
	global_load_dword v142, v234, s[50:51] offset:2176 sc1
	global_load_dword v143, v234, s[50:51] offset:2432 sc1
	global_load_dword v144, v234, s[50:51] offset:2688 sc1
	global_load_dword v145, v234, s[50:51] offset:2944 sc1
	v_mul_f32_e32 v98, v98, v236
	v_mul_f32_e32 v99, v99, v237
	v_mul_f32_e32 v100, v100, v238
	v_mul_f32_e32 v101, v101, v239
	v_mul_f32_e32 v102, v102, v240
	v_mul_f32_e32 v103, v103, v241
	v_mul_f32_e32 v104, v104, v242
	v_mul_f32_e32 v105, v105, v243
	v_mul_f32_e32 v106, v106, v244
	v_mul_f32_e32 v107, v107, v245
	v_mul_f32_e32 v108, v108, v246
	v_mul_f32_e32 v109, v109, v247
	v_mul_f32_e32 v110, v110, v248
	v_mul_f32_e32 v111, v111, v249
	v_mul_f32_e32 v112, v112, v250
	v_mul_f32_e32 v113, v113, v251
	s_waitcnt vmcnt(15)
	v_lshlrev_b32_e32 v130, v220, v130
	v_and_b32_e32 v130, 0xffff0000, v130
	v_fma_f32 v98, -v98, s79, v130
	v_fmac_f32_e32 v146, v98, v98
	s_waitcnt vmcnt(14)
	v_lshlrev_b32_e32 v131, v220, v131
	v_and_b32_e32 v131, 0xffff0000, v131
	v_fma_f32 v99, -v99, s79, v131
	v_fmac_f32_e32 v147, v99, v99
	s_waitcnt vmcnt(13)
	v_lshlrev_b32_e32 v132, v220, v132
	v_and_b32_e32 v132, 0xffff0000, v132
	v_fma_f32 v100, -v100, s79, v132
	v_fmac_f32_e32 v148, v100, v100
	s_waitcnt vmcnt(12)
	v_lshlrev_b32_e32 v133, v220, v133
	v_and_b32_e32 v133, 0xffff0000, v133
	v_fma_f32 v101, -v101, s79, v133
	v_fmac_f32_e32 v149, v101, v101
	s_waitcnt vmcnt(11)
	v_lshlrev_b32_e32 v134, v220, v134
	v_and_b32_e32 v134, 0xffff0000, v134
	v_fma_f32 v102, -v102, s79, v134
	v_fmac_f32_e32 v150, v102, v102
	s_waitcnt vmcnt(10)
	v_lshlrev_b32_e32 v135, v220, v135
	v_and_b32_e32 v135, 0xffff0000, v135
	v_fma_f32 v103, -v103, s79, v135
	v_fmac_f32_e32 v151, v103, v103
	s_waitcnt vmcnt(9)
	v_lshlrev_b32_e32 v136, v220, v136
	v_and_b32_e32 v136, 0xffff0000, v136
	v_fma_f32 v104, -v104, s79, v136
	v_fmac_f32_e32 v152, v104, v104
	s_waitcnt vmcnt(8)
	v_lshlrev_b32_e32 v137, v220, v137
	v_and_b32_e32 v137, 0xffff0000, v137
	v_fma_f32 v105, -v105, s79, v137
	v_fmac_f32_e32 v153, v105, v105
	s_waitcnt vmcnt(7)
	v_lshlrev_b32_e32 v138, v220, v138
	v_and_b32_e32 v138, 0xffff0000, v138
	v_fma_f32 v106, -v106, s79, v138
	v_fmac_f32_e32 v154, v106, v106
	s_waitcnt vmcnt(6)
	v_lshlrev_b32_e32 v139, v220, v139
	v_and_b32_e32 v139, 0xffff0000, v139
	v_fma_f32 v107, -v107, s79, v139
	v_fmac_f32_e32 v155, v107, v107
	s_waitcnt vmcnt(5)
	v_lshlrev_b32_e32 v140, v220, v140
	v_and_b32_e32 v140, 0xffff0000, v140
	v_fma_f32 v108, -v108, s79, v140
	v_fmac_f32_e32 v156, v108, v108
	s_waitcnt vmcnt(4)
	v_lshlrev_b32_e32 v141, v220, v141
	v_and_b32_e32 v141, 0xffff0000, v141
	v_fma_f32 v109, -v109, s79, v141
	v_fmac_f32_e32 v157, v109, v109
	s_waitcnt vmcnt(3)
	v_lshlrev_b32_e32 v142, v220, v142
	v_and_b32_e32 v142, 0xffff0000, v142
	v_fma_f32 v110, -v110, s79, v142
	v_fmac_f32_e32 v158, v110, v110
	s_waitcnt vmcnt(2)
	v_lshlrev_b32_e32 v143, v220, v143
	v_and_b32_e32 v143, 0xffff0000, v143
	v_fma_f32 v111, -v111, s79, v143
	v_fmac_f32_e32 v159, v111, v111
	s_waitcnt vmcnt(1)
	v_lshlrev_b32_e32 v144, v220, v144
	v_and_b32_e32 v144, 0xffff0000, v144
	v_fma_f32 v112, -v112, s79, v144
	v_fmac_f32_e32 v160, v112, v112
	s_waitcnt vmcnt(0)
	v_lshlrev_b32_e32 v145, v220, v145
	v_and_b32_e32 v145, 0xffff0000, v145
	v_fma_f32 v113, -v113, s79, v145
	v_fmac_f32_e32 v161, v113, v113
	global_load_dword v130, v221, s[50:51] offset:192 sc1
	global_load_dword v131, v221, s[50:51] offset:448 sc1
	global_load_dword v132, v221, s[50:51] offset:704 sc1
	global_load_dword v133, v221, s[50:51] offset:960 sc1
	global_load_dword v134, v221, s[50:51] offset:2240 sc1
	global_load_dword v135, v221, s[50:51] offset:2496 sc1
	global_load_dword v136, v221, s[50:51] offset:2752 sc1
	global_load_dword v137, v221, s[50:51] offset:3008 sc1
	global_load_dword v138, v234, s[50:51] offset:192 sc1
	global_load_dword v139, v234, s[50:51] offset:448 sc1
	global_load_dword v140, v234, s[50:51] offset:704 sc1
	global_load_dword v141, v234, s[50:51] offset:960 sc1
	global_load_dword v142, v234, s[50:51] offset:2240 sc1
	global_load_dword v143, v234, s[50:51] offset:2496 sc1
	global_load_dword v144, v234, s[50:51] offset:2752 sc1
	global_load_dword v145, v234, s[50:51] offset:3008 sc1
	v_mul_f32_e32 v114, v114, v236
	v_mul_f32_e32 v115, v115, v237
	v_mul_f32_e32 v116, v116, v238
	v_mul_f32_e32 v117, v117, v239
	v_mul_f32_e32 v118, v118, v240
	v_mul_f32_e32 v119, v119, v241
	v_mul_f32_e32 v120, v120, v242
	v_mul_f32_e32 v121, v121, v243
	v_mul_f32_e32 v122, v122, v244
	v_mul_f32_e32 v123, v123, v245
	v_mul_f32_e32 v124, v124, v246
	v_mul_f32_e32 v125, v125, v247
	v_mul_f32_e32 v126, v126, v248
	v_mul_f32_e32 v127, v127, v249
	v_mul_f32_e32 v128, v128, v250
	v_mul_f32_e32 v129, v129, v251
	s_waitcnt vmcnt(15)
	v_lshlrev_b32_e32 v130, v220, v130
	v_and_b32_e32 v130, 0xffff0000, v130
	v_fma_f32 v114, -v114, s79, v130
	v_fmac_f32_e32 v146, v114, v114
	s_waitcnt vmcnt(14)
	v_lshlrev_b32_e32 v131, v220, v131
	v_and_b32_e32 v131, 0xffff0000, v131
	v_fma_f32 v115, -v115, s79, v131
	v_fmac_f32_e32 v147, v115, v115
	s_waitcnt vmcnt(13)
	v_lshlrev_b32_e32 v132, v220, v132
	v_and_b32_e32 v132, 0xffff0000, v132
	v_fma_f32 v116, -v116, s79, v132
	v_fmac_f32_e32 v148, v116, v116
	s_waitcnt vmcnt(12)
	v_lshlrev_b32_e32 v133, v220, v133
	v_and_b32_e32 v133, 0xffff0000, v133
	v_fma_f32 v117, -v117, s79, v133
	v_fmac_f32_e32 v149, v117, v117
	s_waitcnt vmcnt(11)
	v_lshlrev_b32_e32 v134, v220, v134
	v_and_b32_e32 v134, 0xffff0000, v134
	v_fma_f32 v118, -v118, s79, v134
	v_fmac_f32_e32 v150, v118, v118
	s_waitcnt vmcnt(10)
	v_lshlrev_b32_e32 v135, v220, v135
	v_and_b32_e32 v135, 0xffff0000, v135
	v_fma_f32 v119, -v119, s79, v135
	v_fmac_f32_e32 v151, v119, v119
	s_waitcnt vmcnt(9)
	v_lshlrev_b32_e32 v136, v220, v136
	v_and_b32_e32 v136, 0xffff0000, v136
	v_fma_f32 v120, -v120, s79, v136
	v_fmac_f32_e32 v152, v120, v120
	s_waitcnt vmcnt(8)
	v_lshlrev_b32_e32 v137, v220, v137
	v_and_b32_e32 v137, 0xffff0000, v137
	v_fma_f32 v121, -v121, s79, v137
	v_fmac_f32_e32 v153, v121, v121
	s_waitcnt vmcnt(7)
	v_lshlrev_b32_e32 v138, v220, v138
	v_and_b32_e32 v138, 0xffff0000, v138
	v_fma_f32 v122, -v122, s79, v138
	v_fmac_f32_e32 v154, v122, v122
	s_waitcnt vmcnt(6)
	v_lshlrev_b32_e32 v139, v220, v139
	v_and_b32_e32 v139, 0xffff0000, v139
	v_fma_f32 v123, -v123, s79, v139
	v_fmac_f32_e32 v155, v123, v123
	s_waitcnt vmcnt(5)
	v_lshlrev_b32_e32 v140, v220, v140
	v_and_b32_e32 v140, 0xffff0000, v140
	v_fma_f32 v124, -v124, s79, v140
	v_fmac_f32_e32 v156, v124, v124
	s_waitcnt vmcnt(4)
	v_lshlrev_b32_e32 v141, v220, v141
	v_and_b32_e32 v141, 0xffff0000, v141
	v_fma_f32 v125, -v125, s79, v141
	v_fmac_f32_e32 v157, v125, v125
	s_waitcnt vmcnt(3)
	v_lshlrev_b32_e32 v142, v220, v142
	v_and_b32_e32 v142, 0xffff0000, v142
	v_fma_f32 v126, -v126, s79, v142
	v_fmac_f32_e32 v158, v126, v126
	s_waitcnt vmcnt(2)
	v_lshlrev_b32_e32 v143, v220, v143
	v_and_b32_e32 v143, 0xffff0000, v143
	v_fma_f32 v127, -v127, s79, v143
	v_fmac_f32_e32 v159, v127, v127
	s_waitcnt vmcnt(1)
	v_lshlrev_b32_e32 v144, v220, v144
	v_and_b32_e32 v144, 0xffff0000, v144
	v_fma_f32 v128, -v128, s79, v144
	v_fmac_f32_e32 v160, v128, v128
	s_waitcnt vmcnt(0)
	v_lshlrev_b32_e32 v145, v220, v145
	v_and_b32_e32 v145, 0xffff0000, v145
	v_fma_f32 v129, -v129, s79, v145
	v_fmac_f32_e32 v161, v129, v129
	s_nop 1
	v_add_f32_dpp v146, v146, v146 quad_perm:[1,0,3,2] row_mask:0xf bank_mask:0xf bound_ctrl:1
	s_nop 1
	v_add_f32_dpp v146, v146, v146 quad_perm:[2,3,0,1] row_mask:0xf bank_mask:0xf bound_ctrl:1
	s_nop 1
	v_add_f32_dpp v146, v146, v146 row_half_mirror row_mask:0xf bank_mask:0xf bound_ctrl:1
	s_nop 1
	v_add_f32_dpp v146, v146, v146 row_mirror row_mask:0xf bank_mask:0xf bound_ctrl:1
	s_nop 1
	v_add_f32_dpp v147, v147, v147 quad_perm:[1,0,3,2] row_mask:0xf bank_mask:0xf bound_ctrl:1
	s_nop 1
	v_add_f32_dpp v147, v147, v147 quad_perm:[2,3,0,1] row_mask:0xf bank_mask:0xf bound_ctrl:1
	s_nop 1
	v_add_f32_dpp v147, v147, v147 row_half_mirror row_mask:0xf bank_mask:0xf bound_ctrl:1
	s_nop 1
	v_add_f32_dpp v147, v147, v147 row_mirror row_mask:0xf bank_mask:0xf bound_ctrl:1
	s_nop 1
	v_add_f32_dpp v148, v148, v148 quad_perm:[1,0,3,2] row_mask:0xf bank_mask:0xf bound_ctrl:1
	s_nop 1
	v_add_f32_dpp v148, v148, v148 quad_perm:[2,3,0,1] row_mask:0xf bank_mask:0xf bound_ctrl:1
	s_nop 1
	v_add_f32_dpp v148, v148, v148 row_half_mirror row_mask:0xf bank_mask:0xf bound_ctrl:1
	s_nop 1
	v_add_f32_dpp v148, v148, v148 row_mirror row_mask:0xf bank_mask:0xf bound_ctrl:1
	s_nop 1
	v_add_f32_dpp v149, v149, v149 quad_perm:[1,0,3,2] row_mask:0xf bank_mask:0xf bound_ctrl:1
	s_nop 1
	v_add_f32_dpp v149, v149, v149 quad_perm:[2,3,0,1] row_mask:0xf bank_mask:0xf bound_ctrl:1
	s_nop 1
	v_add_f32_dpp v149, v149, v149 row_half_mirror row_mask:0xf bank_mask:0xf bound_ctrl:1
	s_nop 1
	v_add_f32_dpp v149, v149, v149 row_mirror row_mask:0xf bank_mask:0xf bound_ctrl:1
	s_nop 1
	v_add_f32_dpp v150, v150, v150 quad_perm:[1,0,3,2] row_mask:0xf bank_mask:0xf bound_ctrl:1
	s_nop 1
	v_add_f32_dpp v150, v150, v150 quad_perm:[2,3,0,1] row_mask:0xf bank_mask:0xf bound_ctrl:1
	s_nop 1
	v_add_f32_dpp v150, v150, v150 row_half_mirror row_mask:0xf bank_mask:0xf bound_ctrl:1
	s_nop 1
	v_add_f32_dpp v150, v150, v150 row_mirror row_mask:0xf bank_mask:0xf bound_ctrl:1
	s_nop 1
	v_add_f32_dpp v151, v151, v151 quad_perm:[1,0,3,2] row_mask:0xf bank_mask:0xf bound_ctrl:1
	s_nop 1
	v_add_f32_dpp v151, v151, v151 quad_perm:[2,3,0,1] row_mask:0xf bank_mask:0xf bound_ctrl:1
	s_nop 1
	v_add_f32_dpp v151, v151, v151 row_half_mirror row_mask:0xf bank_mask:0xf bound_ctrl:1
	s_nop 1
	v_add_f32_dpp v151, v151, v151 row_mirror row_mask:0xf bank_mask:0xf bound_ctrl:1
	s_nop 1
	v_add_f32_dpp v152, v152, v152 quad_perm:[1,0,3,2] row_mask:0xf bank_mask:0xf bound_ctrl:1
	s_nop 1
	v_add_f32_dpp v152, v152, v152 quad_perm:[2,3,0,1] row_mask:0xf bank_mask:0xf bound_ctrl:1
	s_nop 1
	v_add_f32_dpp v152, v152, v152 row_half_mirror row_mask:0xf bank_mask:0xf bound_ctrl:1
	s_nop 1
	v_add_f32_dpp v152, v152, v152 row_mirror row_mask:0xf bank_mask:0xf bound_ctrl:1
	s_nop 1
	v_add_f32_dpp v153, v153, v153 quad_perm:[1,0,3,2] row_mask:0xf bank_mask:0xf bound_ctrl:1
	s_nop 1
	v_add_f32_dpp v153, v153, v153 quad_perm:[2,3,0,1] row_mask:0xf bank_mask:0xf bound_ctrl:1
	s_nop 1
	v_add_f32_dpp v153, v153, v153 row_half_mirror row_mask:0xf bank_mask:0xf bound_ctrl:1
	s_nop 1
	v_add_f32_dpp v153, v153, v153 row_mirror row_mask:0xf bank_mask:0xf bound_ctrl:1
	s_nop 1
	v_add_f32_dpp v154, v154, v154 quad_perm:[1,0,3,2] row_mask:0xf bank_mask:0xf bound_ctrl:1
	s_nop 1
	v_add_f32_dpp v154, v154, v154 quad_perm:[2,3,0,1] row_mask:0xf bank_mask:0xf bound_ctrl:1
	s_nop 1
	v_add_f32_dpp v154, v154, v154 row_half_mirror row_mask:0xf bank_mask:0xf bound_ctrl:1
	s_nop 1
	v_add_f32_dpp v154, v154, v154 row_mirror row_mask:0xf bank_mask:0xf bound_ctrl:1
	s_nop 1
	v_add_f32_dpp v155, v155, v155 quad_perm:[1,0,3,2] row_mask:0xf bank_mask:0xf bound_ctrl:1
	s_nop 1
	v_add_f32_dpp v155, v155, v155 quad_perm:[2,3,0,1] row_mask:0xf bank_mask:0xf bound_ctrl:1
	s_nop 1
	v_add_f32_dpp v155, v155, v155 row_half_mirror row_mask:0xf bank_mask:0xf bound_ctrl:1
	s_nop 1
	v_add_f32_dpp v155, v155, v155 row_mirror row_mask:0xf bank_mask:0xf bound_ctrl:1
	s_nop 1
	v_add_f32_dpp v156, v156, v156 quad_perm:[1,0,3,2] row_mask:0xf bank_mask:0xf bound_ctrl:1
	s_nop 1
	v_add_f32_dpp v156, v156, v156 quad_perm:[2,3,0,1] row_mask:0xf bank_mask:0xf bound_ctrl:1
	s_nop 1
	v_add_f32_dpp v156, v156, v156 row_half_mirror row_mask:0xf bank_mask:0xf bound_ctrl:1
	s_nop 1
	v_add_f32_dpp v156, v156, v156 row_mirror row_mask:0xf bank_mask:0xf bound_ctrl:1
	s_nop 1
	v_add_f32_dpp v157, v157, v157 quad_perm:[1,0,3,2] row_mask:0xf bank_mask:0xf bound_ctrl:1
	s_nop 1
	v_add_f32_dpp v157, v157, v157 quad_perm:[2,3,0,1] row_mask:0xf bank_mask:0xf bound_ctrl:1
	s_nop 1
	v_add_f32_dpp v157, v157, v157 row_half_mirror row_mask:0xf bank_mask:0xf bound_ctrl:1
	s_nop 1
	v_add_f32_dpp v157, v157, v157 row_mirror row_mask:0xf bank_mask:0xf bound_ctrl:1
	s_nop 1
	v_add_f32_dpp v158, v158, v158 quad_perm:[1,0,3,2] row_mask:0xf bank_mask:0xf bound_ctrl:1
	s_nop 1
	v_add_f32_dpp v158, v158, v158 quad_perm:[2,3,0,1] row_mask:0xf bank_mask:0xf bound_ctrl:1
	s_nop 1
	v_add_f32_dpp v158, v158, v158 row_half_mirror row_mask:0xf bank_mask:0xf bound_ctrl:1
	s_nop 1
	v_add_f32_dpp v158, v158, v158 row_mirror row_mask:0xf bank_mask:0xf bound_ctrl:1
	s_nop 1
	v_add_f32_dpp v159, v159, v159 quad_perm:[1,0,3,2] row_mask:0xf bank_mask:0xf bound_ctrl:1
	s_nop 1
	v_add_f32_dpp v159, v159, v159 quad_perm:[2,3,0,1] row_mask:0xf bank_mask:0xf bound_ctrl:1
	s_nop 1
	v_add_f32_dpp v159, v159, v159 row_half_mirror row_mask:0xf bank_mask:0xf bound_ctrl:1
	s_nop 1
	v_add_f32_dpp v159, v159, v159 row_mirror row_mask:0xf bank_mask:0xf bound_ctrl:1
	s_nop 1
	v_add_f32_dpp v160, v160, v160 quad_perm:[1,0,3,2] row_mask:0xf bank_mask:0xf bound_ctrl:1
	s_nop 1
	v_add_f32_dpp v160, v160, v160 quad_perm:[2,3,0,1] row_mask:0xf bank_mask:0xf bound_ctrl:1
	s_nop 1
	v_add_f32_dpp v160, v160, v160 row_half_mirror row_mask:0xf bank_mask:0xf bound_ctrl:1
	s_nop 1
	v_add_f32_dpp v160, v160, v160 row_mirror row_mask:0xf bank_mask:0xf bound_ctrl:1
	s_nop 1
	v_add_f32_dpp v161, v161, v161 quad_perm:[1,0,3,2] row_mask:0xf bank_mask:0xf bound_ctrl:1
	s_nop 1
	v_add_f32_dpp v161, v161, v161 quad_perm:[2,3,0,1] row_mask:0xf bank_mask:0xf bound_ctrl:1
	s_nop 1
	v_add_f32_dpp v161, v161, v161 row_half_mirror row_mask:0xf bank_mask:0xf bound_ctrl:1
	s_nop 1
	v_add_f32_dpp v161, v161, v161 row_mirror row_mask:0xf bank_mask:0xf bound_ctrl:1
	ds_swizzle_b32 v130, v146 offset:0x401f
	ds_swizzle_b32 v131, v147 offset:0x401f
	ds_swizzle_b32 v132, v148 offset:0x401f
	ds_swizzle_b32 v133, v149 offset:0x401f
	ds_swizzle_b32 v134, v150 offset:0x401f
	ds_swizzle_b32 v135, v151 offset:0x401f
	ds_swizzle_b32 v136, v152 offset:0x401f
	ds_swizzle_b32 v137, v153 offset:0x401f
	ds_swizzle_b32 v138, v154 offset:0x401f
	ds_swizzle_b32 v139, v155 offset:0x401f
	ds_swizzle_b32 v140, v156 offset:0x401f
	ds_swizzle_b32 v141, v157 offset:0x401f
	ds_swizzle_b32 v142, v158 offset:0x401f
	ds_swizzle_b32 v143, v159 offset:0x401f
	ds_swizzle_b32 v144, v160 offset:0x401f
	ds_swizzle_b32 v145, v161 offset:0x401f
	s_waitcnt lgkmcnt(0)
	v_mov_b32_e32 v222, 0x3b800000
	v_mov_b32_e32 v223, 0x358637bd
	v_add_f32_e32 v146, v146, v130
	v_fma_f32 v146, v146, v222, v223
	v_add_f32_e32 v147, v147, v131
	v_fma_f32 v147, v147, v222, v223
	v_add_f32_e32 v148, v148, v132
	v_fma_f32 v148, v148, v222, v223
	v_add_f32_e32 v149, v149, v133
	v_fma_f32 v149, v149, v222, v223
	v_add_f32_e32 v150, v150, v134
	v_fma_f32 v150, v150, v222, v223
	v_add_f32_e32 v151, v151, v135
	v_fma_f32 v151, v151, v222, v223
	v_add_f32_e32 v152, v152, v136
	v_fma_f32 v152, v152, v222, v223
	v_add_f32_e32 v153, v153, v137
	v_fma_f32 v153, v153, v222, v223
	v_add_f32_e32 v154, v154, v138
	v_fma_f32 v154, v154, v222, v223
	v_add_f32_e32 v155, v155, v139
	v_fma_f32 v155, v155, v222, v223
	v_add_f32_e32 v156, v156, v140
	v_fma_f32 v156, v156, v222, v223
	v_add_f32_e32 v157, v157, v141
	v_fma_f32 v157, v157, v222, v223
	v_add_f32_e32 v158, v158, v142
	v_fma_f32 v158, v158, v222, v223
	v_add_f32_e32 v159, v159, v143
	v_fma_f32 v159, v159, v222, v223
	v_add_f32_e32 v160, v160, v144
	v_fma_f32 v160, v160, v222, v223
	v_add_f32_e32 v161, v161, v145
	v_fma_f32 v161, v161, v222, v223
	v_rsq_f32_e32 v146, v146
	v_rsq_f32_e32 v147, v147
	v_rsq_f32_e32 v148, v148
	v_rsq_f32_e32 v149, v149
	v_rsq_f32_e32 v150, v150
	v_rsq_f32_e32 v151, v151
	v_rsq_f32_e32 v152, v152
	v_rsq_f32_e32 v153, v153
	v_rsq_f32_e32 v154, v154
	v_rsq_f32_e32 v155, v155
	v_rsq_f32_e32 v156, v156
	v_rsq_f32_e32 v157, v157
	v_rsq_f32_e32 v158, v158
	v_rsq_f32_e32 v159, v159
	v_rsq_f32_e32 v160, v160
	v_rsq_f32_e32 v161, v161
	s_nop 0
	v_mul_f32_e32 v146, s88, v146
	v_mul_f32_e32 v147, s88, v147
	v_mul_f32_e32 v148, s88, v148
	v_mul_f32_e32 v149, s88, v149
	v_mul_f32_e32 v150, s88, v150
	v_mul_f32_e32 v151, s88, v151
	v_mul_f32_e32 v152, s88, v152
	v_mul_f32_e32 v153, s88, v153
	v_mul_f32_e32 v154, s88, v154
	v_mul_f32_e32 v155, s88, v155
	v_mul_f32_e32 v156, s88, v156
	v_mul_f32_e32 v157, s88, v157
	v_mul_f32_e32 v158, s88, v158
	v_mul_f32_e32 v159, s88, v159
	v_mul_f32_e32 v160, s88, v160
	v_mul_f32_e32 v161, s88, v161
	v_mul_f32_e32 v0, v0, v146
	v_mul_f32_e32 v1, v1, v147
	v_mul_f32_e32 v2, v2, v148
	v_mul_f32_e32 v3, v3, v149
	v_mul_f32_e32 v4, v4, v150
	v_mul_f32_e32 v5, v5, v151
	v_mul_f32_e32 v6, v6, v152
	v_mul_f32_e32 v7, v7, v153
	v_mul_f32_e32 v8, v8, v154
	v_mul_f32_e32 v9, v9, v155
	v_mul_f32_e32 v10, v10, v156
	v_mul_f32_e32 v11, v11, v157
	v_mul_f32_e32 v12, v12, v158
	v_mul_f32_e32 v13, v13, v159
	v_mul_f32_e32 v14, v14, v160
	v_mul_f32_e32 v15, v15, v161
	v_mul_f32_e32 v0, v0, v212
	v_mul_f32_e32 v1, v1, v212
	v_mul_f32_e32 v2, v2, v212
	v_mul_f32_e32 v3, v3, v212
	v_mul_f32_e32 v4, v4, v212
	v_mul_f32_e32 v5, v5, v212
	v_mul_f32_e32 v6, v6, v212
	v_mul_f32_e32 v7, v7, v212
	v_mul_f32_e32 v8, v8, v212
	v_mul_f32_e32 v9, v9, v212
	v_mul_f32_e32 v10, v10, v212
	v_mul_f32_e32 v11, v11, v212
	v_mul_f32_e32 v12, v12, v212
	v_mul_f32_e32 v13, v13, v212
	v_mul_f32_e32 v14, v14, v212
	v_mul_f32_e32 v15, v15, v212
	v_mov_b32_dpp v130, v0 quad_perm:[1,0,3,2] row_mask:0xf bank_mask:0xf
	v_mov_b32_dpp v131, v1 quad_perm:[1,0,3,2] row_mask:0xf bank_mask:0xf
	v_mov_b32_dpp v132, v2 quad_perm:[1,0,3,2] row_mask:0xf bank_mask:0xf
	v_mov_b32_dpp v133, v3 quad_perm:[1,0,3,2] row_mask:0xf bank_mask:0xf
	v_mov_b32_dpp v134, v4 quad_perm:[1,0,3,2] row_mask:0xf bank_mask:0xf
	v_mov_b32_dpp v135, v5 quad_perm:[1,0,3,2] row_mask:0xf bank_mask:0xf
	v_mov_b32_dpp v136, v6 quad_perm:[1,0,3,2] row_mask:0xf bank_mask:0xf
	v_mov_b32_dpp v137, v7 quad_perm:[1,0,3,2] row_mask:0xf bank_mask:0xf
	v_mov_b32_dpp v138, v8 quad_perm:[1,0,3,2] row_mask:0xf bank_mask:0xf
	v_mov_b32_dpp v139, v9 quad_perm:[1,0,3,2] row_mask:0xf bank_mask:0xf
	v_mov_b32_dpp v140, v10 quad_perm:[1,0,3,2] row_mask:0xf bank_mask:0xf
	v_mov_b32_dpp v141, v11 quad_perm:[1,0,3,2] row_mask:0xf bank_mask:0xf
	v_mov_b32_dpp v142, v12 quad_perm:[1,0,3,2] row_mask:0xf bank_mask:0xf
	v_mov_b32_dpp v143, v13 quad_perm:[1,0,3,2] row_mask:0xf bank_mask:0xf
	v_mov_b32_dpp v144, v14 quad_perm:[1,0,3,2] row_mask:0xf bank_mask:0xf
	v_mov_b32_dpp v145, v15 quad_perm:[1,0,3,2] row_mask:0xf bank_mask:0xf
	v_cvt_pk_bf16_f32 v0, v0, v130
	v_cvt_pk_bf16_f32 v1, v1, v131
	v_cvt_pk_bf16_f32 v2, v2, v132
	v_cvt_pk_bf16_f32 v3, v3, v133
	v_cvt_pk_bf16_f32 v4, v4, v134
	v_cvt_pk_bf16_f32 v5, v5, v135
	v_cvt_pk_bf16_f32 v6, v6, v136
	v_cvt_pk_bf16_f32 v7, v7, v137
	v_cvt_pk_bf16_f32 v8, v8, v138
	v_cvt_pk_bf16_f32 v9, v9, v139
	v_cvt_pk_bf16_f32 v10, v10, v140
	v_cvt_pk_bf16_f32 v11, v11, v141
	v_cvt_pk_bf16_f32 v12, v12, v142
	v_cvt_pk_bf16_f32 v13, v13, v143
	v_cvt_pk_bf16_f32 v14, v14, v144
	v_cvt_pk_bf16_f32 v15, v15, v145
	v_mul_f32_e32 v16, v16, v146
	v_mul_f32_e32 v17, v17, v147
	v_mul_f32_e32 v18, v18, v148
	v_mul_f32_e32 v19, v19, v149
	v_mul_f32_e32 v20, v20, v150
	v_mul_f32_e32 v21, v21, v151
	v_mul_f32_e32 v22, v22, v152
	v_mul_f32_e32 v23, v23, v153
	v_mul_f32_e32 v24, v24, v154
	v_mul_f32_e32 v25, v25, v155
	v_mul_f32_e32 v26, v26, v156
	v_mul_f32_e32 v27, v27, v157
	v_mul_f32_e32 v28, v28, v158
	v_mul_f32_e32 v29, v29, v159
	v_mul_f32_e32 v30, v30, v160
	v_mul_f32_e32 v31, v31, v161
	v_mul_f32_e32 v16, v16, v213
	v_mul_f32_e32 v17, v17, v213
	v_mul_f32_e32 v18, v18, v213
	v_mul_f32_e32 v19, v19, v213
	v_mul_f32_e32 v20, v20, v213
	v_mul_f32_e32 v21, v21, v213
	v_mul_f32_e32 v22, v22, v213
	v_mul_f32_e32 v23, v23, v213
	v_mul_f32_e32 v24, v24, v213
	v_mul_f32_e32 v25, v25, v213
	v_mul_f32_e32 v26, v26, v213
	v_mul_f32_e32 v27, v27, v213
	v_mul_f32_e32 v28, v28, v213
	v_mul_f32_e32 v29, v29, v213
	v_mul_f32_e32 v30, v30, v213
	v_mul_f32_e32 v31, v31, v213
	v_mov_b32_dpp v130, v16 quad_perm:[1,0,3,2] row_mask:0xf bank_mask:0xf
	v_mov_b32_dpp v131, v17 quad_perm:[1,0,3,2] row_mask:0xf bank_mask:0xf
	v_mov_b32_dpp v132, v18 quad_perm:[1,0,3,2] row_mask:0xf bank_mask:0xf
	v_mov_b32_dpp v133, v19 quad_perm:[1,0,3,2] row_mask:0xf bank_mask:0xf
	v_mov_b32_dpp v134, v20 quad_perm:[1,0,3,2] row_mask:0xf bank_mask:0xf
	v_mov_b32_dpp v135, v21 quad_perm:[1,0,3,2] row_mask:0xf bank_mask:0xf
	v_mov_b32_dpp v136, v22 quad_perm:[1,0,3,2] row_mask:0xf bank_mask:0xf
	v_mov_b32_dpp v137, v23 quad_perm:[1,0,3,2] row_mask:0xf bank_mask:0xf
	v_mov_b32_dpp v138, v24 quad_perm:[1,0,3,2] row_mask:0xf bank_mask:0xf
	v_mov_b32_dpp v139, v25 quad_perm:[1,0,3,2] row_mask:0xf bank_mask:0xf
	v_mov_b32_dpp v140, v26 quad_perm:[1,0,3,2] row_mask:0xf bank_mask:0xf
	v_mov_b32_dpp v141, v27 quad_perm:[1,0,3,2] row_mask:0xf bank_mask:0xf
	v_mov_b32_dpp v142, v28 quad_perm:[1,0,3,2] row_mask:0xf bank_mask:0xf
	v_mov_b32_dpp v143, v29 quad_perm:[1,0,3,2] row_mask:0xf bank_mask:0xf
	v_mov_b32_dpp v144, v30 quad_perm:[1,0,3,2] row_mask:0xf bank_mask:0xf
	v_mov_b32_dpp v145, v31 quad_perm:[1,0,3,2] row_mask:0xf bank_mask:0xf
	v_cvt_pk_bf16_f32 v16, v16, v130
	v_cvt_pk_bf16_f32 v17, v17, v131
	v_cvt_pk_bf16_f32 v18, v18, v132
	v_cvt_pk_bf16_f32 v19, v19, v133
	v_cvt_pk_bf16_f32 v20, v20, v134
	v_cvt_pk_bf16_f32 v21, v21, v135
	v_cvt_pk_bf16_f32 v22, v22, v136
	v_cvt_pk_bf16_f32 v23, v23, v137
	v_cvt_pk_bf16_f32 v24, v24, v138
	v_cvt_pk_bf16_f32 v25, v25, v139
	v_cvt_pk_bf16_f32 v26, v26, v140
	v_cvt_pk_bf16_f32 v27, v27, v141
	v_cvt_pk_bf16_f32 v28, v28, v142
	v_cvt_pk_bf16_f32 v29, v29, v143
	v_cvt_pk_bf16_f32 v30, v30, v144
	v_cvt_pk_bf16_f32 v31, v31, v145
	v_mul_f32_e32 v32, v32, v146
	v_mul_f32_e32 v33, v33, v147
	v_mul_f32_e32 v34, v34, v148
	v_mul_f32_e32 v35, v35, v149
	v_mul_f32_e32 v36, v36, v150
	v_mul_f32_e32 v37, v37, v151
	v_mul_f32_e32 v38, v38, v152
	v_mul_f32_e32 v39, v39, v153
	v_mul_f32_e32 v40, v40, v154
	v_mul_f32_e32 v41, v41, v155
	v_mul_f32_e32 v42, v42, v156
	v_mul_f32_e32 v43, v43, v157
	v_mul_f32_e32 v44, v44, v158
	v_mul_f32_e32 v45, v45, v159
	v_mul_f32_e32 v46, v46, v160
	v_mul_f32_e32 v47, v47, v161
	v_mul_f32_e32 v32, v32, v214
	v_mul_f32_e32 v33, v33, v214
	v_mul_f32_e32 v34, v34, v214
	v_mul_f32_e32 v35, v35, v214
	v_mul_f32_e32 v36, v36, v214
	v_mul_f32_e32 v37, v37, v214
	v_mul_f32_e32 v38, v38, v214
	v_mul_f32_e32 v39, v39, v214
	v_mul_f32_e32 v40, v40, v214
	v_mul_f32_e32 v41, v41, v214
	v_mul_f32_e32 v42, v42, v214
	v_mul_f32_e32 v43, v43, v214
	v_mul_f32_e32 v44, v44, v214
	v_mul_f32_e32 v45, v45, v214
	v_mul_f32_e32 v46, v46, v214
	v_mul_f32_e32 v47, v47, v214
	v_mov_b32_dpp v130, v32 quad_perm:[1,0,3,2] row_mask:0xf bank_mask:0xf
	v_mov_b32_dpp v131, v33 quad_perm:[1,0,3,2] row_mask:0xf bank_mask:0xf
	v_mov_b32_dpp v132, v34 quad_perm:[1,0,3,2] row_mask:0xf bank_mask:0xf
	v_mov_b32_dpp v133, v35 quad_perm:[1,0,3,2] row_mask:0xf bank_mask:0xf
	v_mov_b32_dpp v134, v36 quad_perm:[1,0,3,2] row_mask:0xf bank_mask:0xf
	v_mov_b32_dpp v135, v37 quad_perm:[1,0,3,2] row_mask:0xf bank_mask:0xf
	v_mov_b32_dpp v136, v38 quad_perm:[1,0,3,2] row_mask:0xf bank_mask:0xf
	v_mov_b32_dpp v137, v39 quad_perm:[1,0,3,2] row_mask:0xf bank_mask:0xf
	v_mov_b32_dpp v138, v40 quad_perm:[1,0,3,2] row_mask:0xf bank_mask:0xf
	v_mov_b32_dpp v139, v41 quad_perm:[1,0,3,2] row_mask:0xf bank_mask:0xf
	v_mov_b32_dpp v140, v42 quad_perm:[1,0,3,2] row_mask:0xf bank_mask:0xf
	v_mov_b32_dpp v141, v43 quad_perm:[1,0,3,2] row_mask:0xf bank_mask:0xf
	v_mov_b32_dpp v142, v44 quad_perm:[1,0,3,2] row_mask:0xf bank_mask:0xf
	v_mov_b32_dpp v143, v45 quad_perm:[1,0,3,2] row_mask:0xf bank_mask:0xf
	v_mov_b32_dpp v144, v46 quad_perm:[1,0,3,2] row_mask:0xf bank_mask:0xf
	v_mov_b32_dpp v145, v47 quad_perm:[1,0,3,2] row_mask:0xf bank_mask:0xf
	v_cvt_pk_bf16_f32 v32, v32, v130
	v_cvt_pk_bf16_f32 v33, v33, v131
	v_cvt_pk_bf16_f32 v34, v34, v132
	v_cvt_pk_bf16_f32 v35, v35, v133
	v_cvt_pk_bf16_f32 v36, v36, v134
	v_cvt_pk_bf16_f32 v37, v37, v135
	v_cvt_pk_bf16_f32 v38, v38, v136
	v_cvt_pk_bf16_f32 v39, v39, v137
	v_cvt_pk_bf16_f32 v40, v40, v138
	v_cvt_pk_bf16_f32 v41, v41, v139
	v_cvt_pk_bf16_f32 v42, v42, v140
	v_cvt_pk_bf16_f32 v43, v43, v141
	v_cvt_pk_bf16_f32 v44, v44, v142
	v_cvt_pk_bf16_f32 v45, v45, v143
	v_cvt_pk_bf16_f32 v46, v46, v144
	v_cvt_pk_bf16_f32 v47, v47, v145
	v_mul_f32_e32 v48, v48, v146
	v_mul_f32_e32 v49, v49, v147
	v_mul_f32_e32 v50, v50, v148
	v_mul_f32_e32 v51, v51, v149
	v_mul_f32_e32 v52, v52, v150
	v_mul_f32_e32 v53, v53, v151
	v_mul_f32_e32 v54, v54, v152
	v_mul_f32_e32 v55, v55, v153
	v_mul_f32_e32 v56, v56, v154
	v_mul_f32_e32 v57, v57, v155
	v_mul_f32_e32 v58, v58, v156
	v_mul_f32_e32 v59, v59, v157
	v_mul_f32_e32 v60, v60, v158
	v_mul_f32_e32 v61, v61, v159
	v_mul_f32_e32 v62, v62, v160
	v_mul_f32_e32 v63, v63, v161
	v_mul_f32_e32 v48, v48, v215
	v_mul_f32_e32 v49, v49, v215
	v_mul_f32_e32 v50, v50, v215
	v_mul_f32_e32 v51, v51, v215
	v_mul_f32_e32 v52, v52, v215
	v_mul_f32_e32 v53, v53, v215
	v_mul_f32_e32 v54, v54, v215
	v_mul_f32_e32 v55, v55, v215
	v_mul_f32_e32 v56, v56, v215
	v_mul_f32_e32 v57, v57, v215
	v_mul_f32_e32 v58, v58, v215
	v_mul_f32_e32 v59, v59, v215
	v_mul_f32_e32 v60, v60, v215
	v_mul_f32_e32 v61, v61, v215
	v_mul_f32_e32 v62, v62, v215
	v_mul_f32_e32 v63, v63, v215
	v_mov_b32_dpp v130, v48 quad_perm:[1,0,3,2] row_mask:0xf bank_mask:0xf
	v_mov_b32_dpp v131, v49 quad_perm:[1,0,3,2] row_mask:0xf bank_mask:0xf
	v_mov_b32_dpp v132, v50 quad_perm:[1,0,3,2] row_mask:0xf bank_mask:0xf
	v_mov_b32_dpp v133, v51 quad_perm:[1,0,3,2] row_mask:0xf bank_mask:0xf
	v_mov_b32_dpp v134, v52 quad_perm:[1,0,3,2] row_mask:0xf bank_mask:0xf
	v_mov_b32_dpp v135, v53 quad_perm:[1,0,3,2] row_mask:0xf bank_mask:0xf
	v_mov_b32_dpp v136, v54 quad_perm:[1,0,3,2] row_mask:0xf bank_mask:0xf
	v_mov_b32_dpp v137, v55 quad_perm:[1,0,3,2] row_mask:0xf bank_mask:0xf
	v_mov_b32_dpp v138, v56 quad_perm:[1,0,3,2] row_mask:0xf bank_mask:0xf
	v_mov_b32_dpp v139, v57 quad_perm:[1,0,3,2] row_mask:0xf bank_mask:0xf
	v_mov_b32_dpp v140, v58 quad_perm:[1,0,3,2] row_mask:0xf bank_mask:0xf
	v_mov_b32_dpp v141, v59 quad_perm:[1,0,3,2] row_mask:0xf bank_mask:0xf
	v_mov_b32_dpp v142, v60 quad_perm:[1,0,3,2] row_mask:0xf bank_mask:0xf
	v_mov_b32_dpp v143, v61 quad_perm:[1,0,3,2] row_mask:0xf bank_mask:0xf
	v_mov_b32_dpp v144, v62 quad_perm:[1,0,3,2] row_mask:0xf bank_mask:0xf
	v_mov_b32_dpp v145, v63 quad_perm:[1,0,3,2] row_mask:0xf bank_mask:0xf
	v_cvt_pk_bf16_f32 v48, v48, v130
	v_cvt_pk_bf16_f32 v49, v49, v131
	v_cvt_pk_bf16_f32 v50, v50, v132
	v_cvt_pk_bf16_f32 v51, v51, v133
	v_cvt_pk_bf16_f32 v52, v52, v134
	v_cvt_pk_bf16_f32 v53, v53, v135
	v_cvt_pk_bf16_f32 v54, v54, v136
	v_cvt_pk_bf16_f32 v55, v55, v137
	v_cvt_pk_bf16_f32 v56, v56, v138
	v_cvt_pk_bf16_f32 v57, v57, v139
	v_cvt_pk_bf16_f32 v58, v58, v140
	v_cvt_pk_bf16_f32 v59, v59, v141
	v_cvt_pk_bf16_f32 v60, v60, v142
	v_cvt_pk_bf16_f32 v61, v61, v143
	v_cvt_pk_bf16_f32 v62, v62, v144
	v_cvt_pk_bf16_f32 v63, v63, v145
	v_mul_f32_e32 v64, v64, v146
	v_mul_f32_e32 v65, v65, v147
	v_mul_f32_e32 v66, v66, v148
	v_mul_f32_e32 v67, v67, v149
	v_mul_f32_e32 v68, v68, v150
	v_mul_f32_e32 v69, v69, v151
	v_mul_f32_e32 v70, v70, v152
	v_mul_f32_e32 v71, v71, v153
	v_mul_f32_e32 v72, v72, v154
	v_mul_f32_e32 v73, v73, v155
	v_mul_f32_e32 v74, v74, v156
	v_mul_f32_e32 v75, v75, v157
	v_mul_f32_e32 v76, v76, v158
	v_mul_f32_e32 v77, v77, v159
	v_mul_f32_e32 v78, v78, v160
	v_mul_f32_e32 v79, v79, v161
	v_mul_f32_e32 v64, v64, v216
	v_mul_f32_e32 v65, v65, v216
	v_mul_f32_e32 v66, v66, v216
	v_mul_f32_e32 v67, v67, v216
	v_mul_f32_e32 v68, v68, v216
	v_mul_f32_e32 v69, v69, v216
	v_mul_f32_e32 v70, v70, v216
	v_mul_f32_e32 v71, v71, v216
	v_mul_f32_e32 v72, v72, v216
	v_mul_f32_e32 v73, v73, v216
	v_mul_f32_e32 v74, v74, v216
	v_mul_f32_e32 v75, v75, v216
	v_mul_f32_e32 v76, v76, v216
	v_mul_f32_e32 v77, v77, v216
	v_mul_f32_e32 v78, v78, v216
	v_mul_f32_e32 v79, v79, v216
	v_mov_b32_dpp v130, v64 quad_perm:[1,0,3,2] row_mask:0xf bank_mask:0xf
	v_mov_b32_dpp v131, v65 quad_perm:[1,0,3,2] row_mask:0xf bank_mask:0xf
	v_mov_b32_dpp v132, v66 quad_perm:[1,0,3,2] row_mask:0xf bank_mask:0xf
	v_mov_b32_dpp v133, v67 quad_perm:[1,0,3,2] row_mask:0xf bank_mask:0xf
	v_mov_b32_dpp v134, v68 quad_perm:[1,0,3,2] row_mask:0xf bank_mask:0xf
	v_mov_b32_dpp v135, v69 quad_perm:[1,0,3,2] row_mask:0xf bank_mask:0xf
	v_mov_b32_dpp v136, v70 quad_perm:[1,0,3,2] row_mask:0xf bank_mask:0xf
	v_mov_b32_dpp v137, v71 quad_perm:[1,0,3,2] row_mask:0xf bank_mask:0xf
	v_mov_b32_dpp v138, v72 quad_perm:[1,0,3,2] row_mask:0xf bank_mask:0xf
	v_mov_b32_dpp v139, v73 quad_perm:[1,0,3,2] row_mask:0xf bank_mask:0xf
	v_mov_b32_dpp v140, v74 quad_perm:[1,0,3,2] row_mask:0xf bank_mask:0xf
	v_mov_b32_dpp v141, v75 quad_perm:[1,0,3,2] row_mask:0xf bank_mask:0xf
	v_mov_b32_dpp v142, v76 quad_perm:[1,0,3,2] row_mask:0xf bank_mask:0xf
	v_mov_b32_dpp v143, v77 quad_perm:[1,0,3,2] row_mask:0xf bank_mask:0xf
	v_mov_b32_dpp v144, v78 quad_perm:[1,0,3,2] row_mask:0xf bank_mask:0xf
	v_mov_b32_dpp v145, v79 quad_perm:[1,0,3,2] row_mask:0xf bank_mask:0xf
	v_cvt_pk_bf16_f32 v64, v64, v130
	v_cvt_pk_bf16_f32 v65, v65, v131
	v_cvt_pk_bf16_f32 v66, v66, v132
	v_cvt_pk_bf16_f32 v67, v67, v133
	v_cvt_pk_bf16_f32 v68, v68, v134
	v_cvt_pk_bf16_f32 v69, v69, v135
	v_cvt_pk_bf16_f32 v70, v70, v136
	v_cvt_pk_bf16_f32 v71, v71, v137
	v_cvt_pk_bf16_f32 v72, v72, v138
	v_cvt_pk_bf16_f32 v73, v73, v139
	v_cvt_pk_bf16_f32 v74, v74, v140
	v_cvt_pk_bf16_f32 v75, v75, v141
	v_cvt_pk_bf16_f32 v76, v76, v142
	v_cvt_pk_bf16_f32 v77, v77, v143
	v_cvt_pk_bf16_f32 v78, v78, v144
	v_cvt_pk_bf16_f32 v79, v79, v145
	v_mul_f32_e32 v80, v80, v146
	v_mul_f32_e32 v81, v81, v147
	v_mul_f32_e32 v82, v82, v148
	v_mul_f32_e32 v83, v83, v149
	v_mul_f32_e32 v84, v84, v150
	v_mul_f32_e32 v85, v85, v151
	v_mul_f32_e32 v86, v86, v152
	v_mul_f32_e32 v87, v87, v153
	v_mul_f32_e32 v88, v88, v154
	v_mul_f32_e32 v89, v89, v155
	v_mul_f32_e32 v90, v90, v156
	v_mul_f32_e32 v91, v91, v157
	v_mul_f32_e32 v92, v92, v158
	v_mul_f32_e32 v93, v93, v159
	v_mul_f32_e32 v94, v94, v160
	v_mul_f32_e32 v95, v95, v161
	v_mul_f32_e32 v80, v80, v217
	v_mul_f32_e32 v81, v81, v217
	v_mul_f32_e32 v82, v82, v217
	v_mul_f32_e32 v83, v83, v217
	v_mul_f32_e32 v84, v84, v217
	v_mul_f32_e32 v85, v85, v217
	v_mul_f32_e32 v86, v86, v217
	v_mul_f32_e32 v87, v87, v217
	v_mul_f32_e32 v88, v88, v217
	v_mul_f32_e32 v89, v89, v217
	v_mul_f32_e32 v90, v90, v217
	v_mul_f32_e32 v91, v91, v217
	v_mul_f32_e32 v92, v92, v217
	v_mul_f32_e32 v93, v93, v217
	v_mul_f32_e32 v94, v94, v217
	v_mul_f32_e32 v95, v95, v217
	v_mov_b32_dpp v130, v80 quad_perm:[1,0,3,2] row_mask:0xf bank_mask:0xf
	v_mov_b32_dpp v131, v81 quad_perm:[1,0,3,2] row_mask:0xf bank_mask:0xf
	v_mov_b32_dpp v132, v82 quad_perm:[1,0,3,2] row_mask:0xf bank_mask:0xf
	v_mov_b32_dpp v133, v83 quad_perm:[1,0,3,2] row_mask:0xf bank_mask:0xf
	v_mov_b32_dpp v134, v84 quad_perm:[1,0,3,2] row_mask:0xf bank_mask:0xf
	v_mov_b32_dpp v135, v85 quad_perm:[1,0,3,2] row_mask:0xf bank_mask:0xf
	v_mov_b32_dpp v136, v86 quad_perm:[1,0,3,2] row_mask:0xf bank_mask:0xf
	v_mov_b32_dpp v137, v87 quad_perm:[1,0,3,2] row_mask:0xf bank_mask:0xf
	v_mov_b32_dpp v138, v88 quad_perm:[1,0,3,2] row_mask:0xf bank_mask:0xf
	v_mov_b32_dpp v139, v89 quad_perm:[1,0,3,2] row_mask:0xf bank_mask:0xf
	v_mov_b32_dpp v140, v90 quad_perm:[1,0,3,2] row_mask:0xf bank_mask:0xf
	v_mov_b32_dpp v141, v91 quad_perm:[1,0,3,2] row_mask:0xf bank_mask:0xf
	v_mov_b32_dpp v142, v92 quad_perm:[1,0,3,2] row_mask:0xf bank_mask:0xf
	v_mov_b32_dpp v143, v93 quad_perm:[1,0,3,2] row_mask:0xf bank_mask:0xf
	v_mov_b32_dpp v144, v94 quad_perm:[1,0,3,2] row_mask:0xf bank_mask:0xf
	v_mov_b32_dpp v145, v95 quad_perm:[1,0,3,2] row_mask:0xf bank_mask:0xf
	v_cvt_pk_bf16_f32 v80, v80, v130
	v_cvt_pk_bf16_f32 v81, v81, v131
	v_cvt_pk_bf16_f32 v82, v82, v132
	v_cvt_pk_bf16_f32 v83, v83, v133
	v_cvt_pk_bf16_f32 v84, v84, v134
	v_cvt_pk_bf16_f32 v85, v85, v135
	v_cvt_pk_bf16_f32 v86, v86, v136
	v_cvt_pk_bf16_f32 v87, v87, v137
	v_cvt_pk_bf16_f32 v88, v88, v138
	v_cvt_pk_bf16_f32 v89, v89, v139
	v_cvt_pk_bf16_f32 v90, v90, v140
	v_cvt_pk_bf16_f32 v91, v91, v141
	v_cvt_pk_bf16_f32 v92, v92, v142
	v_cvt_pk_bf16_f32 v93, v93, v143
	v_cvt_pk_bf16_f32 v94, v94, v144
	v_cvt_pk_bf16_f32 v95, v95, v145
	v_mul_f32_e32 v98, v98, v146
	v_mul_f32_e32 v99, v99, v147
	v_mul_f32_e32 v100, v100, v148
	v_mul_f32_e32 v101, v101, v149
	v_mul_f32_e32 v102, v102, v150
	v_mul_f32_e32 v103, v103, v151
	v_mul_f32_e32 v104, v104, v152
	v_mul_f32_e32 v105, v105, v153
	v_mul_f32_e32 v106, v106, v154
	v_mul_f32_e32 v107, v107, v155
	v_mul_f32_e32 v108, v108, v156
	v_mul_f32_e32 v109, v109, v157
	v_mul_f32_e32 v110, v110, v158
	v_mul_f32_e32 v111, v111, v159
	v_mul_f32_e32 v112, v112, v160
	v_mul_f32_e32 v113, v113, v161
	v_mul_f32_e32 v98, v98, v218
	v_mul_f32_e32 v99, v99, v218
	v_mul_f32_e32 v100, v100, v218
	v_mul_f32_e32 v101, v101, v218
	v_mul_f32_e32 v102, v102, v218
	v_mul_f32_e32 v103, v103, v218
	v_mul_f32_e32 v104, v104, v218
	v_mul_f32_e32 v105, v105, v218
	v_mul_f32_e32 v106, v106, v218
	v_mul_f32_e32 v107, v107, v218
	v_mul_f32_e32 v108, v108, v218
	v_mul_f32_e32 v109, v109, v218
	v_mul_f32_e32 v110, v110, v218
	v_mul_f32_e32 v111, v111, v218
	v_mul_f32_e32 v112, v112, v218
	v_mul_f32_e32 v113, v113, v218
	v_mov_b32_dpp v130, v98 quad_perm:[1,0,3,2] row_mask:0xf bank_mask:0xf
	v_mov_b32_dpp v131, v99 quad_perm:[1,0,3,2] row_mask:0xf bank_mask:0xf
	v_mov_b32_dpp v132, v100 quad_perm:[1,0,3,2] row_mask:0xf bank_mask:0xf
	v_mov_b32_dpp v133, v101 quad_perm:[1,0,3,2] row_mask:0xf bank_mask:0xf
	v_mov_b32_dpp v134, v102 quad_perm:[1,0,3,2] row_mask:0xf bank_mask:0xf
	v_mov_b32_dpp v135, v103 quad_perm:[1,0,3,2] row_mask:0xf bank_mask:0xf
	v_mov_b32_dpp v136, v104 quad_perm:[1,0,3,2] row_mask:0xf bank_mask:0xf
	v_mov_b32_dpp v137, v105 quad_perm:[1,0,3,2] row_mask:0xf bank_mask:0xf
	v_mov_b32_dpp v138, v106 quad_perm:[1,0,3,2] row_mask:0xf bank_mask:0xf
	v_mov_b32_dpp v139, v107 quad_perm:[1,0,3,2] row_mask:0xf bank_mask:0xf
	v_mov_b32_dpp v140, v108 quad_perm:[1,0,3,2] row_mask:0xf bank_mask:0xf
	v_mov_b32_dpp v141, v109 quad_perm:[1,0,3,2] row_mask:0xf bank_mask:0xf
	v_mov_b32_dpp v142, v110 quad_perm:[1,0,3,2] row_mask:0xf bank_mask:0xf
	v_mov_b32_dpp v143, v111 quad_perm:[1,0,3,2] row_mask:0xf bank_mask:0xf
	v_mov_b32_dpp v144, v112 quad_perm:[1,0,3,2] row_mask:0xf bank_mask:0xf
	v_mov_b32_dpp v145, v113 quad_perm:[1,0,3,2] row_mask:0xf bank_mask:0xf
	v_cvt_pk_bf16_f32 v98, v98, v130
	v_cvt_pk_bf16_f32 v99, v99, v131
	v_cvt_pk_bf16_f32 v100, v100, v132
	v_cvt_pk_bf16_f32 v101, v101, v133
	v_cvt_pk_bf16_f32 v102, v102, v134
	v_cvt_pk_bf16_f32 v103, v103, v135
	v_cvt_pk_bf16_f32 v104, v104, v136
	v_cvt_pk_bf16_f32 v105, v105, v137
	v_cvt_pk_bf16_f32 v106, v106, v138
	v_cvt_pk_bf16_f32 v107, v107, v139
	v_cvt_pk_bf16_f32 v108, v108, v140
	v_cvt_pk_bf16_f32 v109, v109, v141
	v_cvt_pk_bf16_f32 v110, v110, v142
	v_cvt_pk_bf16_f32 v111, v111, v143
	v_cvt_pk_bf16_f32 v112, v112, v144
	v_cvt_pk_bf16_f32 v113, v113, v145
	v_mul_f32_e32 v114, v114, v146
	v_mul_f32_e32 v115, v115, v147
	v_mul_f32_e32 v116, v116, v148
	v_mul_f32_e32 v117, v117, v149
	v_mul_f32_e32 v118, v118, v150
	v_mul_f32_e32 v119, v119, v151
	v_mul_f32_e32 v120, v120, v152
	v_mul_f32_e32 v121, v121, v153
	v_mul_f32_e32 v122, v122, v154
	v_mul_f32_e32 v123, v123, v155
	v_mul_f32_e32 v124, v124, v156
	v_mul_f32_e32 v125, v125, v157
	v_mul_f32_e32 v126, v126, v158
	v_mul_f32_e32 v127, v127, v159
	v_mul_f32_e32 v128, v128, v160
	v_mul_f32_e32 v129, v129, v161
	v_mul_f32_e32 v114, v114, v219
	v_mul_f32_e32 v115, v115, v219
	v_mul_f32_e32 v116, v116, v219
	v_mul_f32_e32 v117, v117, v219
	v_mul_f32_e32 v118, v118, v219
	v_mul_f32_e32 v119, v119, v219
	v_mul_f32_e32 v120, v120, v219
	v_mul_f32_e32 v121, v121, v219
	v_mul_f32_e32 v122, v122, v219
	v_mul_f32_e32 v123, v123, v219
	v_mul_f32_e32 v124, v124, v219
	v_mul_f32_e32 v125, v125, v219
	v_mul_f32_e32 v126, v126, v219
	v_mul_f32_e32 v127, v127, v219
	v_mul_f32_e32 v128, v128, v219
	v_mul_f32_e32 v129, v129, v219
	v_mov_b32_dpp v130, v114 quad_perm:[1,0,3,2] row_mask:0xf bank_mask:0xf
	v_mov_b32_dpp v131, v115 quad_perm:[1,0,3,2] row_mask:0xf bank_mask:0xf
	v_mov_b32_dpp v132, v116 quad_perm:[1,0,3,2] row_mask:0xf bank_mask:0xf
	v_mov_b32_dpp v133, v117 quad_perm:[1,0,3,2] row_mask:0xf bank_mask:0xf
	v_mov_b32_dpp v134, v118 quad_perm:[1,0,3,2] row_mask:0xf bank_mask:0xf
	v_mov_b32_dpp v135, v119 quad_perm:[1,0,3,2] row_mask:0xf bank_mask:0xf
	v_mov_b32_dpp v136, v120 quad_perm:[1,0,3,2] row_mask:0xf bank_mask:0xf
	v_mov_b32_dpp v137, v121 quad_perm:[1,0,3,2] row_mask:0xf bank_mask:0xf
	v_mov_b32_dpp v138, v122 quad_perm:[1,0,3,2] row_mask:0xf bank_mask:0xf
	v_mov_b32_dpp v139, v123 quad_perm:[1,0,3,2] row_mask:0xf bank_mask:0xf
	v_mov_b32_dpp v140, v124 quad_perm:[1,0,3,2] row_mask:0xf bank_mask:0xf
	v_mov_b32_dpp v141, v125 quad_perm:[1,0,3,2] row_mask:0xf bank_mask:0xf
	v_mov_b32_dpp v142, v126 quad_perm:[1,0,3,2] row_mask:0xf bank_mask:0xf
	v_mov_b32_dpp v143, v127 quad_perm:[1,0,3,2] row_mask:0xf bank_mask:0xf
	v_mov_b32_dpp v144, v128 quad_perm:[1,0,3,2] row_mask:0xf bank_mask:0xf
	v_mov_b32_dpp v145, v129 quad_perm:[1,0,3,2] row_mask:0xf bank_mask:0xf
	v_cvt_pk_bf16_f32 v114, v114, v130
	v_cvt_pk_bf16_f32 v115, v115, v131
	v_cvt_pk_bf16_f32 v116, v116, v132
	v_cvt_pk_bf16_f32 v117, v117, v133
	v_cvt_pk_bf16_f32 v118, v118, v134
	v_cvt_pk_bf16_f32 v119, v119, v135
	v_cvt_pk_bf16_f32 v120, v120, v136
	v_cvt_pk_bf16_f32 v121, v121, v137
	v_cvt_pk_bf16_f32 v122, v122, v138
	v_cvt_pk_bf16_f32 v123, v123, v139
	v_cvt_pk_bf16_f32 v124, v124, v140
	v_cvt_pk_bf16_f32 v125, v125, v141
	v_cvt_pk_bf16_f32 v126, v126, v142
	v_cvt_pk_bf16_f32 v127, v127, v143
	v_cvt_pk_bf16_f32 v128, v128, v144
	v_cvt_pk_bf16_f32 v129, v129, v145
	s_lshr_b32 s21, s10, 1
	s_lshr_b32 s74, s21, 3
	s_and_b32 s21, s21, 7
	s_lshl_b32 s74, s74, 13
	s_lshl_b32 s52, s8, 8
	s_add_i32 s74, s74, s52
	s_lshl_b32 s52, s15, 5
	s_add_i32 s74, s74, s52
	s_lshl_b32 s21, s21, 9
	s_add_u32 s52, s0, 0x1eaac000
	s_addc_u32 s53, s1, 0
	s_add_u32 s52, s52, s21
	s_addc_u32 s53, s53, 0
	s_lshl_b64 s[74:75], s[74:75], 12
	s_add_u32 s52, s52, s74
	s_addc_u32 s53, s53, s75
	s_mov_b32 s75, 0
	v_lshlrev_b32_e32 v221, 14, v229
	v_lshl_add_u32 v221, v231, 1, v221
	s_mov_b64 s[48:49], exec
	s_mov_b32 s50, 0x55555555
	s_mov_b32 s51, 0x55555555
	s_mov_b64 exec, s[50:51]
	v_add_u32_e32 v222, 0x0, v221
	global_store_dword v222, v0, s[52:53] offset:0
	global_store_dword v222, v16, s[52:53] offset:64
	global_store_dword v222, v32, s[52:53] offset:128
	global_store_dword v222, v48, s[52:53] offset:192
	global_store_dword v222, v64, s[52:53] offset:256
	global_store_dword v222, v80, s[52:53] offset:320
	global_store_dword v222, v98, s[52:53] offset:384
	global_store_dword v222, v114, s[52:53] offset:448
	v_add_u32_e32 v222, 0x1000, v221
	global_store_dword v222, v1, s[52:53] offset:0
	global_store_dword v222, v17, s[52:53] offset:64
	global_store_dword v222, v33, s[52:53] offset:128
	global_store_dword v222, v49, s[52:53] offset:192
	global_store_dword v222, v65, s[52:53] offset:256
	global_store_dword v222, v81, s[52:53] offset:320
	global_store_dword v222, v99, s[52:53] offset:384
	global_store_dword v222, v115, s[52:53] offset:448
	v_add_u32_e32 v222, 0x2000, v221
	global_store_dword v222, v2, s[52:53] offset:0
	global_store_dword v222, v18, s[52:53] offset:64
	global_store_dword v222, v34, s[52:53] offset:128
	global_store_dword v222, v50, s[52:53] offset:192
	global_store_dword v222, v66, s[52:53] offset:256
	global_store_dword v222, v82, s[52:53] offset:320
	global_store_dword v222, v100, s[52:53] offset:384
	global_store_dword v222, v116, s[52:53] offset:448
	v_add_u32_e32 v222, 0x3000, v221
	global_store_dword v222, v3, s[52:53] offset:0
	global_store_dword v222, v19, s[52:53] offset:64
	global_store_dword v222, v35, s[52:53] offset:128
	global_store_dword v222, v51, s[52:53] offset:192
	global_store_dword v222, v67, s[52:53] offset:256
	global_store_dword v222, v83, s[52:53] offset:320
	global_store_dword v222, v101, s[52:53] offset:384
	global_store_dword v222, v117, s[52:53] offset:448
	v_add_u32_e32 v222, 0x8000, v221
	global_store_dword v222, v4, s[52:53] offset:0
	global_store_dword v222, v20, s[52:53] offset:64
	global_store_dword v222, v36, s[52:53] offset:128
	global_store_dword v222, v52, s[52:53] offset:192
	global_store_dword v222, v68, s[52:53] offset:256
	global_store_dword v222, v84, s[52:53] offset:320
	global_store_dword v222, v102, s[52:53] offset:384
	global_store_dword v222, v118, s[52:53] offset:448
	v_add_u32_e32 v222, 0x9000, v221
	global_store_dword v222, v5, s[52:53] offset:0
	global_store_dword v222, v21, s[52:53] offset:64
	global_store_dword v222, v37, s[52:53] offset:128
	global_store_dword v222, v53, s[52:53] offset:192
	global_store_dword v222, v69, s[52:53] offset:256
	global_store_dword v222, v85, s[52:53] offset:320
	global_store_dword v222, v103, s[52:53] offset:384
	global_store_dword v222, v119, s[52:53] offset:448
	v_add_u32_e32 v222, 0xa000, v221
	global_store_dword v222, v6, s[52:53] offset:0
	global_store_dword v222, v22, s[52:53] offset:64
	global_store_dword v222, v38, s[52:53] offset:128
	global_store_dword v222, v54, s[52:53] offset:192
	global_store_dword v222, v70, s[52:53] offset:256
	global_store_dword v222, v86, s[52:53] offset:320
	global_store_dword v222, v104, s[52:53] offset:384
	global_store_dword v222, v120, s[52:53] offset:448
	v_add_u32_e32 v222, 0xb000, v221
	global_store_dword v222, v7, s[52:53] offset:0
	global_store_dword v222, v23, s[52:53] offset:64
	global_store_dword v222, v39, s[52:53] offset:128
	global_store_dword v222, v55, s[52:53] offset:192
	global_store_dword v222, v71, s[52:53] offset:256
	global_store_dword v222, v87, s[52:53] offset:320
	global_store_dword v222, v105, s[52:53] offset:384
	global_store_dword v222, v121, s[52:53] offset:448
	v_add_u32_e32 v222, 0x10000, v221
	global_store_dword v222, v8, s[52:53] offset:0
	global_store_dword v222, v24, s[52:53] offset:64
	global_store_dword v222, v40, s[52:53] offset:128
	global_store_dword v222, v56, s[52:53] offset:192
	global_store_dword v222, v72, s[52:53] offset:256
	global_store_dword v222, v88, s[52:53] offset:320
	global_store_dword v222, v106, s[52:53] offset:384
	global_store_dword v222, v122, s[52:53] offset:448
	v_add_u32_e32 v222, 0x11000, v221
	global_store_dword v222, v9, s[52:53] offset:0
	global_store_dword v222, v25, s[52:53] offset:64
	global_store_dword v222, v41, s[52:53] offset:128
	global_store_dword v222, v57, s[52:53] offset:192
	global_store_dword v222, v73, s[52:53] offset:256
	global_store_dword v222, v89, s[52:53] offset:320
	global_store_dword v222, v107, s[52:53] offset:384
	global_store_dword v222, v123, s[52:53] offset:448
	v_add_u32_e32 v222, 0x12000, v221
	global_store_dword v222, v10, s[52:53] offset:0
	global_store_dword v222, v26, s[52:53] offset:64
	global_store_dword v222, v42, s[52:53] offset:128
	global_store_dword v222, v58, s[52:53] offset:192
	global_store_dword v222, v74, s[52:53] offset:256
	global_store_dword v222, v90, s[52:53] offset:320
	global_store_dword v222, v108, s[52:53] offset:384
	global_store_dword v222, v124, s[52:53] offset:448
	v_add_u32_e32 v222, 0x13000, v221
	global_store_dword v222, v11, s[52:53] offset:0
	global_store_dword v222, v27, s[52:53] offset:64
	global_store_dword v222, v43, s[52:53] offset:128
	global_store_dword v222, v59, s[52:53] offset:192
	global_store_dword v222, v75, s[52:53] offset:256
	global_store_dword v222, v91, s[52:53] offset:320
	global_store_dword v222, v109, s[52:53] offset:384
	global_store_dword v222, v125, s[52:53] offset:448
	v_add_u32_e32 v222, 0x18000, v221
	global_store_dword v222, v12, s[52:53] offset:0
	global_store_dword v222, v28, s[52:53] offset:64
	global_store_dword v222, v44, s[52:53] offset:128
	global_store_dword v222, v60, s[52:53] offset:192
	global_store_dword v222, v76, s[52:53] offset:256
	global_store_dword v222, v92, s[52:53] offset:320
	global_store_dword v222, v110, s[52:53] offset:384
	global_store_dword v222, v126, s[52:53] offset:448
	v_add_u32_e32 v222, 0x19000, v221
	global_store_dword v222, v13, s[52:53] offset:0
	global_store_dword v222, v29, s[52:53] offset:64
	global_store_dword v222, v45, s[52:53] offset:128
	global_store_dword v222, v61, s[52:53] offset:192
	global_store_dword v222, v77, s[52:53] offset:256
	global_store_dword v222, v93, s[52:53] offset:320
	global_store_dword v222, v111, s[52:53] offset:384
	global_store_dword v222, v127, s[52:53] offset:448
	v_add_u32_e32 v222, 0x1a000, v221
	global_store_dword v222, v14, s[52:53] offset:0
	global_store_dword v222, v30, s[52:53] offset:64
	global_store_dword v222, v46, s[52:53] offset:128
	global_store_dword v222, v62, s[52:53] offset:192
	global_store_dword v222, v78, s[52:53] offset:256
	global_store_dword v222, v94, s[52:53] offset:320
	global_store_dword v222, v112, s[52:53] offset:384
	global_store_dword v222, v128, s[52:53] offset:448
	v_add_u32_e32 v222, 0x1b000, v221
	global_store_dword v222, v15, s[52:53] offset:0
	global_store_dword v222, v31, s[52:53] offset:64
	global_store_dword v222, v47, s[52:53] offset:128
	global_store_dword v222, v63, s[52:53] offset:192
	global_store_dword v222, v79, s[52:53] offset:256
	global_store_dword v222, v95, s[52:53] offset:320
	global_store_dword v222, v113, s[52:53] offset:384
	global_store_dword v222, v129, s[52:53] offset:448
	s_mov_b64 exec, s[48:49]
.Lfa_epi_done:
	s_add_i32 s9, s9, 1
	s_cmp_lt_u32 s9, 4
	s_cbranch_scc1 .Lfa_block
	s_add_i32 s2, s2, s7
	s_branch .Lfa_task

.LBB0_595:
	s_cmp_le_i32 s58, s2
	s_cselect_b64 s[0:1], -1, 0
	s_cmp_lt_i32 s2, s59
	s_cselect_b64 s[4:5], -1, 0
	s_and_b64 s[4:5], s[0:1], s[4:5]
	s_mov_b64 s[0:1], -1
	s_and_b64 vcc, exec, s[4:5]
	s_waitcnt lgkmcnt(0)
	s_add_i32 s7, s6, 3
	s_mov_b64 s[0:1], 0

.LBB0_696:
	s_and_b64 vcc, exec, s[0:1]
	s_cbranch_vccnz .LBB0_845
	s_mul_i32 s0, s11, 0x18000
	s_add_u32 s28, s48, s0
	s_addc_u32 s29, s49, 0
	s_lshl_b32 s74, s11, 4
	s_lshl_b64 s[0:1], s[74:75], 2
	s_add_u32 s30, s50, s0
	s_addc_u32 s31, s51, s1
	s_add_u32 s34, s34, s0
	s_addc_u32 s35, s35, s1
	s_add_u32 s21, s88, 0x382ac000
	s_addc_u32 s82, s89, 0
	s_add_u32 s83, s88, 0x402ac000
	s_addc_u32 s84, s89, 0
	s_add_u32 s92, s88, 0x482ac000
	s_addc_u32 s93, s89, 0
	s_add_u32 s8, s88, 0x4c2ac000
	s_addc_u32 s9, s89, 0
	s_add_u32 s38, s88, 0x582ac000
	s_addc_u32 s39, s89, 0
	s_add_u32 s44, s88, 0x332ac000
	s_addc_u32 s45, s89, 0
	s_mov_b32 s89, -1
	s_mov_b32 s88, s94
	s_waitcnt vmcnt(0)
	s_branch .LBB0_700

.LBB0_710:
	v_cmp_gt_i32_e32 vcc, 64, v84
	v_mov_b32_e32 v100, 0
	v_mov_b32_e32 v101, 0
	s_and_saveexec_b64 s[0:1], vcc
	s_cbranch_execz .LBB0_712
	s_lshl_b32 s4, s10, 2
	s_load_dword s36, s[30:31], s4
	s_load_dword s37, s[34:35], s4
	s_waitcnt lgkmcnt(0)
	v_mov_b32_e32 v61, s36
	v_mov_b32_e32 v101, s37
	v_mul_f32_e32 v100, 0x3fb8aa3b, v61
.LBB0_712:
	s_or_b64 exec, exec, s[0:1]
	v_lshlrev_b32_e32 v85, 3, v84
	v_and_b32_e32 v106, 0x78, v85
	v_lshl_add_u32 v60, v106, 2, 0
	v_add_u32_e32 v107, 0x20c00, v60
	ds_read_b128 v[62:65], v107
	ds_read_b128 v[66:69], v107 offset:16
	ds_read_b128 v[70:73], v107 offset:512
	ds_read_b128 v[74:77], v107 offset:528
	ds_read_b128 v[78:81], v107 offset:1024
	ds_read_b128 v[86:89], v107 offset:1040
	ds_read_b128 v[90:93], v107 offset:1536
	ds_read_b128 v[116:119], v107 offset:1552
	s_waitcnt vmcnt(12)
	v_lshlrev_b32_e32 v60, 16, v7
	v_and_b32_e32 v61, 0xffff0000, v7
	v_lshlrev_b32_e32 v82, 16, v3
	v_and_b32_e32 v83, 0xffff0000, v3
	s_waitcnt lgkmcnt(6)
	v_pk_mul_f32 v[60:61], v[68:69], v[60:61]
	v_lshlrev_b32_e32 v94, 16, v11
	v_and_b32_e32 v95, 0xffff0000, v11
	s_waitcnt lgkmcnt(4)
	v_pk_fma_f32 v[60:61], v[76:77], v[82:83], v[60:61]
	v_lshlrev_b32_e32 v98, 16, v15
	v_and_b32_e32 v99, 0xffff0000, v15
	s_waitcnt lgkmcnt(2)
	v_pk_fma_f32 v[60:61], v[88:89], v[94:95], v[60:61]
	v_lshlrev_b32_e32 v120, 16, v2
	s_waitcnt lgkmcnt(0)
	v_pk_fma_f32 v[60:61], v[118:119], v[98:99], v[60:61]
	v_and_b32_e32 v121, 0xffff0000, v2
	v_mul_f32_e32 v96, 0xbfb8aa3b, v60
	v_exp_f32_e32 v108, v96
	v_mul_f32_e32 v96, 0xbfb8aa3b, v61
	v_exp_f32_e32 v109, v96
	v_lshlrev_b32_e32 v122, 16, v10
	v_add_f32_e32 v108, 1.0, v108
	v_rcp_f32_e32 v110, v108
	v_add_f32_e32 v111, 1.0, v109
	v_lshlrev_b32_e32 v108, 16, v6
	v_and_b32_e32 v109, 0xffff0000, v6
	v_pk_mul_f32 v[108:109], v[66:67], v[108:109]
	v_and_b32_e32 v123, 0xffff0000, v10
	v_pk_fma_f32 v[108:109], v[74:75], v[120:121], v[108:109]
	v_lshlrev_b32_e32 v124, 16, v14
	v_and_b32_e32 v125, 0xffff0000, v14
	v_pk_fma_f32 v[108:109], v[86:87], v[122:123], v[108:109]
	v_lshlrev_b32_e32 v134, 16, v5
	v_pk_fma_f32 v[126:127], v[116:117], v[124:125], v[108:109]
	v_and_b32_e32 v135, 0xffff0000, v5
	v_mul_f32_e32 v108, 0xbfb8aa3b, v126
	v_exp_f32_e32 v108, v108
	v_mul_f32_e32 v109, 0xbfb8aa3b, v127
	v_exp_f32_e32 v109, v109
	v_pk_mul_f32 v[134:135], v[64:65], v[134:135]
	v_add_f32_e32 v108, 1.0, v108
	v_rcp_f32_e32 v128, v108
	v_add_f32_e32 v108, 1.0, v109
	v_rcp_f32_e32 v129, v108
	v_lshlrev_b32_e32 v130, 16, v9
	v_and_b32_e32 v131, 0xffff0000, v9
	v_lshlrev_b32_e32 v132, 16, v13
	v_pk_mul_f32 v[126:127], v[126:127], v[128:129]
	v_lshlrev_b32_e32 v128, 16, v1
	v_and_b32_e32 v129, 0xffff0000, v1
	v_pk_fma_f32 v[134:135], v[72:73], v[128:129], v[134:135]
	v_and_b32_e32 v133, 0xffff0000, v13
	v_pk_fma_f32 v[134:135], v[80:81], v[130:131], v[134:135]
	v_lshlrev_b32_e32 v146, 16, v4
	v_pk_fma_f32 v[134:135], v[92:93], v[132:133], v[134:135]
	v_and_b32_e32 v147, 0xffff0000, v4
	v_mul_f32_e32 v109, 0xbfb8aa3b, v134
	v_exp_f32_e32 v109, v109
	v_mul_f32_e32 v136, 0xbfb8aa3b, v135
	v_exp_f32_e32 v139, v136
	v_lshlrev_b32_e32 v140, 16, v0
	v_and_b32_e32 v141, 0xffff0000, v0
	v_pk_mul_f32 v[146:147], v[62:63], v[146:147]
	v_lshlrev_b32_e32 v142, 16, v8
	v_and_b32_e32 v143, 0xffff0000, v8
	v_pk_fma_f32 v[146:147], v[70:71], v[140:141], v[146:147]
	v_add_f32_e32 v109, 1.0, v109
	v_lshlrev_b32_e32 v144, 16, v12
	v_and_b32_e32 v145, 0xffff0000, v12
	v_pk_fma_f32 v[146:147], v[78:79], v[142:143], v[146:147]
	v_rcp_f32_e32 v138, v109
	v_add_f32_e32 v109, 1.0, v139
	v_pk_fma_f32 v[146:147], v[90:91], v[144:145], v[146:147]
	v_rcp_f32_e32 v139, v109
	v_mul_f32_e32 v109, 0xbfb8aa3b, v146
	v_exp_f32_e32 v109, v109
	v_mul_f32_e32 v148, 0xbfb8aa3b, v147
	v_exp_f32_e32 v148, v148
	v_pk_mul_f32 v[68:69], v[68:69], v[82:83]
	v_add_f32_e32 v109, 1.0, v109
	v_pk_fma_f32 v[68:69], v[76:77], v[94:95], v[68:69]
	v_pk_mul_f32 v[134:135], v[134:135], v[138:139]
	v_rcp_f32_e32 v138, v109
	v_add_f32_e32 v109, 1.0, v148
	v_lshlrev_b32_e32 v148, 16, v19
	v_and_b32_e32 v149, 0xffff0000, v19
	v_pk_fma_f32 v[68:69], v[88:89], v[98:99], v[68:69]
	v_pk_mul_f32 v[66:67], v[66:67], v[120:121]
	v_pk_fma_f32 v[68:69], v[118:119], v[148:149], v[68:69]
	v_pk_fma_f32 v[66:67], v[74:75], v[122:123], v[66:67]
	v_mul_f32_e32 v76, 0xbfb8aa3b, v68
	v_mul_f32_e32 v77, 0xbfb8aa3b, v69
	v_exp_f32_e32 v76, v76
	v_exp_f32_e32 v77, v77
	v_pk_fma_f32 v[66:67], v[86:87], v[124:125], v[66:67]
	v_pk_mul_f32 v[62:63], v[62:63], v[140:141]
	v_add_f32_e32 v76, 1.0, v76
	v_add_f32_e32 v77, 1.0, v77
	v_rcp_f32_e32 v76, v76
	v_rcp_f32_e32 v77, v77
	v_pk_mul_f32 v[64:65], v[64:65], v[128:129]
	v_pk_fma_f32 v[62:63], v[70:71], v[142:143], v[62:63]
	v_pk_fma_f32 v[64:65], v[72:73], v[130:131], v[64:65]
	v_pk_mul_f32 v[68:69], v[68:69], v[76:77]
	v_lshlrev_b32_e32 v76, 16, v18
	v_and_b32_e32 v77, 0xffff0000, v18
	v_pk_fma_f32 v[66:67], v[116:117], v[76:77], v[66:67]
	v_pk_fma_f32 v[62:63], v[78:79], v[144:145], v[62:63]
	v_mul_f32_e32 v74, 0xbfb8aa3b, v66
	v_exp_f32_e32 v76, v74
	v_mul_f32_e32 v74, 0xbfb8aa3b, v67
	v_exp_f32_e32 v77, v74
	v_lshlrev_b32_e32 v86, 16, v17
	v_add_f32_e32 v76, 1.0, v76
	v_rcp_f32_e32 v76, v76
	v_add_f32_e32 v77, 1.0, v77
	v_rcp_f32_e32 v77, v77
	v_and_b32_e32 v87, 0xffff0000, v17
	v_pk_fma_f32 v[64:65], v[80:81], v[132:133], v[64:65]
	v_rcp_f32_e32 v139, v109
	v_pk_mul_f32 v[66:67], v[66:67], v[76:77]
	v_lshlrev_b32_e32 v76, 16, v16
	v_and_b32_e32 v77, 0xffff0000, v16
	v_pk_fma_f32 v[62:63], v[90:91], v[76:77], v[62:63]
	v_pk_fma_f32 v[64:65], v[92:93], v[86:87], v[64:65]
	v_mul_f32_e32 v70, 0xbfb8aa3b, v62
	v_mul_f32_e32 v71, 0xbfb8aa3b, v63
	v_mul_f32_e32 v72, 0xbfb8aa3b, v64
	v_mul_f32_e32 v73, 0xbfb8aa3b, v65
	v_exp_f32_e32 v70, v70
	v_exp_f32_e32 v71, v71
	v_exp_f32_e32 v72, v72
	v_exp_f32_e32 v73, v73
	v_add_f32_e32 v70, 1.0, v70
	v_add_f32_e32 v71, 1.0, v71
	v_add_f32_e32 v72, 1.0, v72
	v_add_f32_e32 v73, 1.0, v73
	v_rcp_f32_e32 v70, v70
	v_rcp_f32_e32 v71, v71
	v_rcp_f32_e32 v72, v72
	v_rcp_f32_e32 v73, v73
	v_pk_mul_f32 v[88:89], v[146:147], v[138:139]
	v_pk_mul_f32 v[70:71], v[62:63], v[70:71]
	v_rcp_f32_e32 v111, v111
	v_pk_mul_f32 v[94:95], v[88:89], v[88:89]
	v_pk_mul_f32 v[72:73], v[64:65], v[72:73]
	v_pk_mul_f32 v[62:63], v[70:71], v[70:71]
	v_pk_mul_f32 v[82:83], v[134:135], v[134:135]
	v_pk_mul_f32 v[64:65], v[72:73], v[72:73]
	v_mov_b32_e32 v78, v62
	v_mov_b32_e32 v79, v94
	v_mov_b32_e32 v94, v63
	v_pk_add_f32 v[62:63], v[78:79], v[94:95]
	v_mov_b32_e32 v78, v64
	v_mov_b32_e32 v79, v82
	v_pk_mul_f32 v[136:137], v[126:127], v[126:127]
	v_pk_mul_f32 v[76:77], v[66:67], v[66:67]
	v_pk_add_f32 v[62:63], v[78:79], v[62:63]
	v_mov_b32_e32 v82, v65
	v_pk_mul_f32 v[60:61], v[60:61], v[110:111]
	v_pk_add_f32 v[62:63], v[82:83], v[62:63]
	v_mov_b32_e32 v64, v76
	v_mov_b32_e32 v65, v136
	v_pk_mul_f32 v[110:111], v[60:61], v[60:61]
	v_pk_mul_f32 v[74:75], v[68:69], v[68:69]
	v_pk_add_f32 v[62:63], v[64:65], v[62:63]
	v_mov_b32_e32 v136, v77
	v_pk_add_f32 v[62:63], v[136:137], v[62:63]
	v_mov_b32_e32 v64, v74
	v_mov_b32_e32 v65, v110
	v_pk_add_f32 v[62:63], v[64:65], v[62:63]
	v_mov_b32_e32 v110, v75
	v_pk_add_f32 v[62:63], v[110:111], v[62:63]
	s_mov_b32 s10, 0x358637bd
	v_ashrrev_i32_e32 v96, 3, v84
	v_mov_b32_dpp v65, v63 quad_perm:[1,0,3,2] row_mask:0xf bank_mask:0xf bound_ctrl:1
	v_mov_b32_dpp v64, v62 quad_perm:[1,0,3,2] row_mask:0xf bank_mask:0xf bound_ctrl:1
	v_pk_add_f32 v[62:63], v[62:63], v[64:65]
	v_and_b32_e32 v108, -2, v96
	v_lshl_add_u32 v76, v106, 1, 0
	v_mov_b32_dpp v65, v63 quad_perm:[2,3,0,1] row_mask:0xf bank_mask:0xf bound_ctrl:1
	v_mov_b32_dpp v64, v62 quad_perm:[2,3,0,1] row_mask:0xf bank_mask:0xf bound_ctrl:1
	v_pk_add_f32 v[62:63], v[62:63], v[64:65]
	v_mad_u64_u32 v[86:87], s[4:5], v108, s13, v[76:77]
	s_nop 0
	v_mov_b32_dpp v65, v63 row_half_mirror row_mask:0xf bank_mask:0xf bound_ctrl:1
	v_mov_b32_dpp v64, v62 row_half_mirror row_mask:0xf bank_mask:0xf bound_ctrl:1
	v_pk_add_f32 v[62:63], v[62:63], v[64:65]
	v_lshlrev_b32_e32 v92, 16, v27
	v_and_b32_e32 v93, 0xffff0000, v27
	v_mov_b32_dpp v65, v63 row_mirror row_mask:0xf bank_mask:0xf bound_ctrl:1
	v_mov_b32_dpp v64, v62 row_mirror row_mask:0xf bank_mask:0xf bound_ctrl:1
	v_pk_add_f32 v[62:63], v[62:63], v[64:65]
	v_lshlrev_b32_e32 v94, 16, v31
	v_pk_add_f32 v[74:75], v[62:63], s[10:11] op_sel_hi:[1,0]
	v_and_b32_e32 v95, 0xffff0000, v31
	v_mul_f32_e32 v62, 0x4b800000, v75
	v_cmp_gt_f32_e64 s[0:1], s17, v75
	v_lshlrev_b32_e32 v98, 16, v35
	v_and_b32_e32 v99, 0xffff0000, v35
	v_cndmask_b32_e64 v62, v75, v62, s[0:1]
	v_rsq_f32_e32 v62, v62
	v_lshlrev_b32_e32 v120, 16, v22
	v_and_b32_e32 v121, 0xffff0000, v22
	v_lshlrev_b32_e32 v124, 16, v26
	v_mul_f32_e32 v63, 0x45800000, v62
	v_cndmask_b32_e64 v62, v62, v63, s[0:1]
	v_mul_f32_e32 v78, 0x3db504f3, v62
	v_pk_mul_f32 v[62:63], v[88:89], v[78:79] op_sel_hi:[1,0]
	v_pk_mul_f32 v[64:65], v[134:135], v[78:79] op_sel_hi:[1,0]
	v_cvt_pk_bf16_f32 v62, v62, v63
	v_cvt_pk_bf16_f32 v63, v64, v65
	v_pk_mul_f32 v[64:65], v[126:127], v[78:79] op_sel_hi:[1,0]
	v_cmp_gt_f32_e64 s[0:1], s17, v74
	v_cvt_pk_bf16_f32 v64, v64, v65
	v_mul_f32_e32 v65, 0x4b800000, v74
	v_cndmask_b32_e64 v65, v74, v65, s[0:1]
	v_rsq_f32_e32 v74, v65
	v_pk_mul_f32 v[60:61], v[60:61], v[78:79] op_sel_hi:[1,0]
	v_and_b32_e32 v125, 0xffff0000, v26
	v_cvt_pk_bf16_f32 v65, v60, v61
	v_mul_f32_e32 v60, 0x45800000, v74
	v_cndmask_b32_e64 v60, v74, v60, s[0:1]
	ds_write_b128 v86, v[62:65]
	v_mul_f32_e32 v64, 0x3db504f3, v60
	v_pk_mul_f32 v[60:61], v[70:71], v[64:65] op_sel_hi:[1,0]
	v_pk_mul_f32 v[62:63], v[72:73], v[64:65] op_sel_hi:[1,0]
	v_cvt_pk_bf16_f32 v60, v60, v61
	v_cvt_pk_bf16_f32 v61, v62, v63
	v_pk_mul_f32 v[62:63], v[66:67], v[64:65] op_sel_hi:[1,0]
	v_pk_mul_f32 v[64:65], v[68:69], v[64:65] op_sel_hi:[1,0]
	v_cvt_pk_bf16_f32 v62, v62, v63
	v_cvt_pk_bf16_f32 v63, v64, v65
	v_or_b32_e32 v64, 1, v96
	v_mad_u64_u32 v[88:89], s[0:1], v64, s13, v[76:77]
	ds_write_b128 v88, v[60:63]
	ds_read_b128 v[68:71], v107 offset:2064
	ds_read_b128 v[72:75], v107 offset:2576
	ds_read_b128 v[76:79], v107 offset:3088
	ds_read_b128 v[80:83], v107 offset:3600
	v_lshlrev_b32_e32 v60, 16, v23
	v_and_b32_e32 v61, 0xffff0000, v23
	s_waitcnt lgkmcnt(3)
	v_pk_mul_f32 v[60:61], v[70:71], v[60:61]
	v_pk_mul_f32 v[70:71], v[70:71], v[92:93]
	s_waitcnt lgkmcnt(2)
	v_pk_fma_f32 v[64:65], v[74:75], v[92:93], v[60:61]
	v_pk_mul_f32 v[120:121], v[68:69], v[120:121]
	s_waitcnt lgkmcnt(1)
	v_pk_fma_f32 v[90:91], v[78:79], v[94:95], v[64:65]
	v_pk_fma_f32 v[70:71], v[74:75], v[94:95], v[70:71]
	s_waitcnt lgkmcnt(0)
	v_pk_fma_f32 v[90:91], v[82:83], v[98:99], v[90:91]
	v_lshlrev_b32_e32 v126, 16, v30
	v_mul_f32_e32 v87, 0xbfb8aa3b, v90
	v_exp_f32_e32 v87, v87
	v_mul_f32_e32 v89, 0xbfb8aa3b, v91
	v_exp_f32_e32 v89, v89
	v_and_b32_e32 v127, 0xffff0000, v30
	v_pk_fma_f32 v[120:121], v[72:73], v[124:125], v[120:121]
	v_lshlrev_b32_e32 v152, 16, v39
	v_and_b32_e32 v153, 0xffff0000, v39
	v_pk_fma_f32 v[70:71], v[78:79], v[98:99], v[70:71]
	v_lshlrev_b32_e32 v128, 16, v34
	v_and_b32_e32 v129, 0xffff0000, v34
	v_pk_fma_f32 v[120:121], v[76:77], v[126:127], v[120:121]
	v_pk_fma_f32 v[70:71], v[82:83], v[152:153], v[70:71]
	v_add_f32_e32 v87, 1.0, v87
	v_pk_fma_f32 v[130:131], v[80:81], v[128:129], v[120:121]
	v_mul_f32_e32 v74, 0xbfb8aa3b, v70
	v_mul_f32_e32 v75, 0xbfb8aa3b, v71
	v_rcp_f32_e32 v110, v87
	v_add_f32_e32 v87, 1.0, v89
	v_mul_f32_e32 v89, 0xbfb8aa3b, v130
	v_exp_f32_e32 v74, v74
	v_exp_f32_e32 v75, v75
	v_exp_f32_e32 v89, v89
	v_mul_f32_e32 v109, 0xbfb8aa3b, v131
	v_exp_f32_e32 v109, v109
	v_add_f32_e32 v74, 1.0, v74
	v_add_f32_e32 v75, 1.0, v75
	v_rcp_f32_e32 v111, v87
	v_add_f32_e32 v87, 1.0, v89
	v_rcp_f32_e32 v74, v74
	v_rcp_f32_e32 v75, v75
	v_rcp_f32_e32 v132, v87
	v_add_f32_e32 v87, 1.0, v109
	ds_read_b128 v[116:119], v107 offset:2048
	ds_read_b128 v[120:123], v107 offset:2560
	v_rcp_f32_e32 v133, v87
	v_pk_mul_f32 v[68:69], v[68:69], v[124:125]
	ds_read_b128 v[60:63], v107 offset:3072
	ds_read_b128 v[64:67], v107 offset:3584
	v_pk_fma_f32 v[68:69], v[72:73], v[126:127], v[68:69]
	v_pk_mul_f32 v[70:71], v[70:71], v[74:75]
	v_lshlrev_b32_e32 v74, 16, v38
	v_and_b32_e32 v75, 0xffff0000, v38
	v_pk_fma_f32 v[68:69], v[76:77], v[128:129], v[68:69]
	v_pk_mul_f32 v[130:131], v[130:131], v[132:133]
	v_pk_fma_f32 v[68:69], v[80:81], v[74:75], v[68:69]
	v_lshlrev_b32_e32 v132, 16, v25
	v_and_b32_e32 v133, 0xffff0000, v25
	v_lshlrev_b32_e32 v138, 16, v21
	v_and_b32_e32 v139, 0xffff0000, v21
	v_mul_f32_e32 v72, 0xbfb8aa3b, v68
	v_lshlrev_b32_e32 v134, 16, v29
	v_and_b32_e32 v135, 0xffff0000, v29
	s_waitcnt lgkmcnt(3)
	v_pk_mul_f32 v[138:139], v[118:119], v[138:139]
	v_exp_f32_e32 v74, v72
	v_mul_f32_e32 v72, 0xbfb8aa3b, v69
	v_pk_mul_f32 v[80:81], v[118:119], v[132:133]
	v_lshlrev_b32_e32 v136, 16, v33
	v_and_b32_e32 v137, 0xffff0000, v33
	s_waitcnt lgkmcnt(2)
	v_pk_fma_f32 v[138:139], v[122:123], v[132:133], v[138:139]
	v_exp_f32_e32 v75, v72
	v_pk_fma_f32 v[80:81], v[122:123], v[134:135], v[80:81]
	s_waitcnt lgkmcnt(1)
	v_pk_fma_f32 v[138:139], v[62:63], v[134:135], v[138:139]
	v_lshlrev_b32_e32 v76, 16, v37
	v_and_b32_e32 v77, 0xffff0000, v37
	v_pk_fma_f32 v[62:63], v[62:63], v[136:137], v[80:81]
	s_waitcnt lgkmcnt(0)
	v_pk_fma_f32 v[138:139], v[66:67], v[136:137], v[138:139]
	v_pk_fma_f32 v[62:63], v[66:67], v[76:77], v[62:63]
	v_add_f32_e32 v74, 1.0, v74
	v_mul_f32_e32 v66, 0xbfb8aa3b, v62
	v_add_f32_e32 v75, 1.0, v75
	v_exp_f32_e32 v76, v66
	v_mul_f32_e32 v66, 0xbfb8aa3b, v63
	v_mul_f32_e32 v87, 0xbfb8aa3b, v138
	v_rcp_f32_e32 v74, v74
	v_rcp_f32_e32 v75, v75
	v_exp_f32_e32 v77, v66
	v_exp_f32_e32 v87, v87
	v_mul_f32_e32 v89, 0xbfb8aa3b, v139
	v_exp_f32_e32 v89, v89
	v_lshlrev_b32_e32 v150, 16, v20
	v_and_b32_e32 v151, 0xffff0000, v20
	v_lshlrev_b32_e32 v144, 16, v24
	v_and_b32_e32 v145, 0xffff0000, v24
	v_pk_mul_f32 v[150:151], v[116:117], v[150:151]
	v_lshlrev_b32_e32 v146, 16, v28
	v_and_b32_e32 v147, 0xffff0000, v28
	v_pk_fma_f32 v[150:151], v[120:121], v[144:145], v[150:151]
	v_pk_mul_f32 v[66:67], v[68:69], v[74:75]
	v_add_f32_e32 v68, 1.0, v76
	v_add_f32_e32 v69, 1.0, v77
	v_pk_mul_f32 v[76:77], v[116:117], v[144:145]
	v_add_f32_e32 v87, 1.0, v87
	v_lshlrev_b32_e32 v148, 16, v32
	v_and_b32_e32 v149, 0xffff0000, v32
	v_pk_fma_f32 v[150:151], v[60:61], v[146:147], v[150:151]
	v_pk_fma_f32 v[76:77], v[120:121], v[146:147], v[76:77]
	v_rcp_f32_e32 v142, v87
	v_add_f32_e32 v87, 1.0, v89
	v_pk_fma_f32 v[150:151], v[64:65], v[148:149], v[150:151]
	v_lshlrev_b32_e32 v74, 16, v36
	v_and_b32_e32 v75, 0xffff0000, v36
	v_pk_fma_f32 v[60:61], v[60:61], v[148:149], v[76:77]
	v_rcp_f32_e32 v143, v87
	v_mul_f32_e32 v87, 0xbfb8aa3b, v150
	v_pk_fma_f32 v[60:61], v[64:65], v[74:75], v[60:61]
	v_exp_f32_e32 v87, v87
	v_mul_f32_e32 v89, 0xbfb8aa3b, v151
	v_mul_f32_e32 v64, 0xbfb8aa3b, v60
	v_mul_f32_e32 v65, 0xbfb8aa3b, v61
	v_exp_f32_e32 v89, v89
	v_exp_f32_e32 v64, v64
	v_exp_f32_e32 v65, v65
	v_add_f32_e32 v87, 1.0, v87
	v_pk_mul_f32 v[138:139], v[138:139], v[142:143]
	v_rcp_f32_e32 v142, v87
	v_add_f32_e32 v87, 1.0, v89
	v_add_f32_e32 v64, 1.0, v64
	v_add_f32_e32 v65, 1.0, v65
	v_rcp_f32_e32 v143, v87
	v_rcp_f32_e32 v64, v64
	v_rcp_f32_e32 v65, v65
	v_rcp_f32_e32 v68, v68
	v_rcp_f32_e32 v69, v69
	v_pk_mul_f32 v[82:83], v[150:151], v[142:143]
	v_pk_mul_f32 v[64:65], v[60:61], v[64:65]
	v_pk_mul_f32 v[92:93], v[82:83], v[82:83]
	v_pk_mul_f32 v[68:69], v[62:63], v[68:69]
	v_pk_mul_f32 v[60:61], v[64:65], v[64:65]
	v_pk_mul_f32 v[78:79], v[138:139], v[138:139]
	v_pk_mul_f32 v[62:63], v[68:69], v[68:69]
	v_mov_b32_e32 v76, v60
	v_mov_b32_e32 v77, v92
	v_mov_b32_e32 v92, v61
	v_pk_add_f32 v[60:61], v[76:77], v[92:93]
	v_mov_b32_e32 v76, v62
	v_mov_b32_e32 v77, v78
	v_pk_mul_f32 v[140:141], v[130:131], v[130:131]
	v_pk_mul_f32 v[74:75], v[66:67], v[66:67]
	v_pk_add_f32 v[60:61], v[76:77], v[60:61]
	v_mov_b32_e32 v78, v63
	v_pk_mul_f32 v[90:91], v[90:91], v[110:111]
	v_pk_add_f32 v[60:61], v[78:79], v[60:61]
	v_mov_b32_e32 v62, v74
	v_mov_b32_e32 v63, v140
	v_pk_mul_f32 v[110:111], v[90:91], v[90:91]
	v_pk_mul_f32 v[72:73], v[70:71], v[70:71]
	v_pk_add_f32 v[60:61], v[62:63], v[60:61]
	v_mov_b32_e32 v140, v75
	v_pk_add_f32 v[60:61], v[140:141], v[60:61]
	v_mov_b32_e32 v62, v72
	v_mov_b32_e32 v63, v110
	v_pk_add_f32 v[60:61], v[62:63], v[60:61]
	v_mov_b32_e32 v110, v73
	v_pk_add_f32 v[60:61], v[110:111], v[60:61]
	v_lshlrev_b32_e32 v94, 16, v40
	v_lshlrev_b32_e32 v95, 16, v44
	v_mov_b32_dpp v63, v61 quad_perm:[1,0,3,2] row_mask:0xf bank_mask:0xf bound_ctrl:1
	v_mov_b32_dpp v62, v60 quad_perm:[1,0,3,2] row_mask:0xf bank_mask:0xf bound_ctrl:1
	v_pk_add_f32 v[60:61], v[60:61], v[62:63]
	v_lshlrev_b32_e32 v99, 16, v48
	v_mov_b32_e32 v98, v95
	v_mov_b32_dpp v63, v61 quad_perm:[2,3,0,1] row_mask:0xf bank_mask:0xf bound_ctrl:1
	v_mov_b32_dpp v62, v60 quad_perm:[2,3,0,1] row_mask:0xf bank_mask:0xf bound_ctrl:1
	v_pk_add_f32 v[60:61], v[60:61], v[62:63]
	v_lshlrev_b32_e32 v117, 16, v52
	v_mov_b32_e32 v116, v99
	v_mov_b32_dpp v63, v61 row_half_mirror row_mask:0xf bank_mask:0xf bound_ctrl:1
	v_mov_b32_dpp v62, v60 row_half_mirror row_mask:0xf bank_mask:0xf bound_ctrl:1
	v_pk_add_f32 v[60:61], v[60:61], v[62:63]
	v_lshlrev_b32_e32 v111, 16, v56
	v_mov_b32_e32 v110, v117
	v_mov_b32_dpp v63, v61 row_mirror row_mask:0xf bank_mask:0xf bound_ctrl:1
	v_mov_b32_dpp v62, v60 row_mirror row_mask:0xf bank_mask:0xf bound_ctrl:1
	v_pk_add_f32 v[60:61], v[60:61], v[62:63]
	v_and_b32_e32 v109, 0xffff0000, v44
	v_pk_add_f32 v[72:73], v[60:61], s[10:11] op_sel_hi:[1,0]
	v_and_b32_e32 v119, 0xffff0000, v56
	v_mul_f32_e32 v60, 0x4b800000, v73
	v_cmp_gt_f32_e64 s[0:1], s17, v73
	s_ashr_i32 s4, s88, 5
	s_lshl_b32 s5, s14, 7
	v_cndmask_b32_e64 v60, v73, v60, s[0:1]
	v_rsq_f32_e32 v60, v60
	s_add_i32 s48, s5, s4
	v_mul_f32_e32 v61, 0x45800000, v60
	v_cndmask_b32_e64 v74, v60, v61, s[0:1]
	v_pk_mul_f32 v[60:61], v[82:83], v[74:75] op_sel_hi:[1,0]
	v_pk_mul_f32 v[62:63], v[138:139], v[74:75] op_sel_hi:[1,0]
	v_cvt_pk_bf16_f32 v60, v60, v61
	v_cvt_pk_bf16_f32 v61, v62, v63
	v_pk_mul_f32 v[62:63], v[130:131], v[74:75] op_sel_hi:[1,0]
	v_cmp_gt_f32_e64 s[0:1], s17, v72
	v_cvt_pk_bf16_f32 v62, v62, v63
	v_mul_f32_e32 v63, 0x4b800000, v72
	v_cndmask_b32_e64 v63, v72, v63, s[0:1]
	v_rsq_f32_e32 v75, v63
	s_nop 0
	v_pk_mul_f32 v[72:73], v[90:91], v[74:75] op_sel_hi:[1,0]
	s_nop 0
	v_cvt_pk_bf16_f32 v63, v72, v73
	ds_write_b128 v86, v[60:63] offset:17408
	v_mul_f32_e32 v60, 0x45800000, v75
	v_cndmask_b32_e64 v72, v75, v60, s[0:1]
	v_pk_mul_f32 v[60:61], v[64:65], v[72:73] op_sel_hi:[1,0]
	v_pk_mul_f32 v[62:63], v[68:69], v[72:73] op_sel_hi:[1,0]
	v_cvt_pk_bf16_f32 v60, v60, v61
	v_cvt_pk_bf16_f32 v61, v62, v63
	v_pk_mul_f32 v[62:63], v[66:67], v[72:73] op_sel_hi:[1,0]
	v_pk_mul_f32 v[64:65], v[70:71], v[72:73] op_sel_hi:[1,0]
	v_cvt_pk_bf16_f32 v62, v62, v63
	v_cvt_pk_bf16_f32 v63, v64, v65
	ds_write_b128 v88, v[60:63] offset:17408
	ds_read_b128 v[68:71], v107 offset:4096
	ds_read_b128 v[60:63], v107 offset:4112
	ds_read_b128 v[72:75], v107 offset:4608
	ds_read_b128 v[64:67], v107 offset:4624
	ds_read_b128 v[76:79], v107 offset:5120
	ds_read_b128 v[80:83], v107 offset:5136
	ds_read_b128 v[86:89], v107 offset:5632
	ds_read_b128 v[90:93], v107 offset:5648
	s_waitcnt lgkmcnt(7)
	v_pk_mul_f32 v[94:95], v[68:69], v[94:95] op_sel_hi:[0,1]
	s_waitcnt lgkmcnt(5)
	v_pk_fma_f32 v[94:95], v[72:73], v[98:99], v[94:95] op_sel_hi:[0,1,1]
	s_waitcnt lgkmcnt(3)
	v_pk_fma_f32 v[94:95], v[76:77], v[116:117], v[94:95] op_sel_hi:[0,1,1]
	s_waitcnt lgkmcnt(1)
	v_pk_fma_f32 v[94:95], v[86:87], v[110:111], v[94:95] op_sel_hi:[0,1,1]
	v_mul_f32_e32 v98, 0xbfb8aa3b, v94
	v_mul_f32_e32 v99, 0xbfb8aa3b, v95
	v_exp_f32_e32 v98, v98
	v_exp_f32_e32 v99, v99
	v_lshlrev_b32_e32 v107, 1, v108
	v_and_b32_e32 v108, 0xffff0000, v40
	v_and_b32_e32 v111, 0xffff0000, v48
	v_mov_b32_e32 v110, v109
	v_pk_mul_f32 v[68:69], v[68:69], v[108:109] op_sel:[1,0]
	v_add_f32_e32 v98, 1.0, v98
	v_add_f32_e32 v99, 1.0, v99
	v_and_b32_e32 v117, 0xffff0000, v52
	v_mov_b32_e32 v116, v111
	v_pk_fma_f32 v[68:69], v[72:73], v[110:111], v[68:69] op_sel:[1,0,0]
	v_rcp_f32_e32 v98, v98
	v_rcp_f32_e32 v99, v99
	v_mov_b32_e32 v118, v117
	v_pk_fma_f32 v[68:69], v[76:77], v[116:117], v[68:69] op_sel:[1,0,0]
	v_lshlrev_b32_e32 v109, 16, v53
	v_pk_fma_f32 v[68:69], v[86:87], v[118:119], v[68:69] op_sel:[1,0,0]
	v_lshlrev_b32_e32 v86, 16, v41
	v_mul_f32_e32 v72, 0xbfb8aa3b, v68
	v_exp_f32_e32 v76, v72
	v_mul_f32_e32 v72, 0xbfb8aa3b, v69
	v_lshlrev_b32_e32 v87, 16, v45
	v_exp_f32_e32 v77, v72
	v_pk_mul_f32 v[72:73], v[94:95], v[98:99]
	v_lshlrev_b32_e32 v95, 16, v49
	v_mov_b32_e32 v94, v87
	v_pk_mul_f32 v[86:87], v[70:71], v[86:87] op_sel_hi:[0,1]
	v_mov_b32_e32 v108, v95
	v_pk_fma_f32 v[86:87], v[74:75], v[94:95], v[86:87] op_sel_hi:[0,1,1]
	v_lshlrev_b32_e32 v99, 16, v57
	v_mov_b32_e32 v98, v109
	v_pk_fma_f32 v[86:87], v[78:79], v[108:109], v[86:87] op_sel_hi:[0,1,1]
	v_pk_fma_f32 v[86:87], v[88:89], v[98:99], v[86:87] op_sel_hi:[0,1,1]
	v_mul_f32_e32 v70, 0xbfb8aa3b, v86
	v_add_f32_e32 v76, 1.0, v76
	v_add_f32_e32 v77, 1.0, v77
	v_exp_f32_e32 v70, v70
	v_mul_f32_e32 v74, 0xbfb8aa3b, v87
	v_rcp_f32_e32 v76, v76
	v_rcp_f32_e32 v77, v77
	v_exp_f32_e32 v74, v74
	v_add_f32_e32 v70, 1.0, v70
	v_and_b32_e32 v95, 0xffff0000, v45
	v_pk_mul_f32 v[68:69], v[68:69], v[76:77]
	v_rcp_f32_e32 v76, v70
	v_add_f32_e32 v70, 1.0, v74
	v_rcp_f32_e32 v77, v70
	v_and_b32_e32 v94, 0xffff0000, v41
	v_mov_b32_e32 v70, v71
	v_and_b32_e32 v99, 0xffff0000, v49
	v_mov_b32_e32 v98, v95
	v_pk_mul_f32 v[70:71], v[70:71], v[94:95] op_sel_hi:[0,1]
	v_mov_b32_e32 v74, v75
	v_and_b32_e32 v109, 0xffff0000, v53
	v_mov_b32_e32 v108, v99
	v_pk_fma_f32 v[70:71], v[74:75], v[98:99], v[70:71] op_sel_hi:[0,1,1]
	v_mov_b32_e32 v74, v79
	v_and_b32_e32 v111, 0xffff0000, v57
	v_mov_b32_e32 v110, v109
	v_pk_fma_f32 v[70:71], v[74:75], v[108:109], v[70:71] op_sel_hi:[0,1,1]
	v_mov_b32_e32 v74, v89
	v_pk_fma_f32 v[70:71], v[74:75], v[110:111], v[70:71] op_sel_hi:[0,1,1]
	v_mul_f32_e32 v74, 0xbfb8aa3b, v70
	v_exp_f32_e32 v78, v74
	v_mul_f32_e32 v74, 0xbfb8aa3b, v71
	v_exp_f32_e32 v79, v74
	v_pk_mul_f32 v[74:75], v[86:87], v[76:77]
	v_add_f32_e32 v76, 1.0, v78
	v_lshlrev_b32_e32 v78, 16, v42
	v_add_f32_e32 v77, 1.0, v79
	v_lshlrev_b32_e32 v79, 16, v46
	v_lshlrev_b32_e32 v87, 16, v50
	v_mov_b32_e32 v86, v79
	v_pk_mul_f32 v[78:79], v[60:61], v[78:79] op_sel_hi:[0,1]
	v_lshlrev_b32_e32 v95, 16, v54
	v_mov_b32_e32 v94, v87
	v_pk_fma_f32 v[78:79], v[64:65], v[86:87], v[78:79] op_sel_hi:[0,1,1]
	v_lshlrev_b32_e32 v89, 16, v58
	v_mov_b32_e32 v88, v95
	v_pk_fma_f32 v[78:79], v[80:81], v[94:95], v[78:79] op_sel_hi:[0,1,1]
	s_waitcnt lgkmcnt(0)
	v_pk_fma_f32 v[78:79], v[90:91], v[88:89], v[78:79] op_sel_hi:[0,1,1]
	v_mul_f32_e32 v86, 0xbfb8aa3b, v78
	v_mul_f32_e32 v87, 0xbfb8aa3b, v79
	v_rcp_f32_e32 v76, v76
	v_rcp_f32_e32 v77, v77
	v_exp_f32_e32 v86, v86
	v_exp_f32_e32 v87, v87
	v_and_b32_e32 v89, 0xffff0000, v50
	v_pk_mul_f32 v[70:71], v[70:71], v[76:77]
	v_add_f32_e32 v76, 1.0, v86
	v_add_f32_e32 v77, 1.0, v87
	v_and_b32_e32 v87, 0xffff0000, v46
	v_and_b32_e32 v86, 0xffff0000, v42
	v_mov_b32_e32 v88, v87
	v_pk_mul_f32 v[60:61], v[60:61], v[86:87] op_sel:[1,0]
	v_and_b32_e32 v95, 0xffff0000, v54
	v_mov_b32_e32 v94, v89
	v_pk_fma_f32 v[60:61], v[64:65], v[88:89], v[60:61] op_sel:[1,0,0]
	v_and_b32_e32 v99, 0xffff0000, v58
	v_pk_fma_f32 v[60:61], v[80:81], v[94:95], v[60:61] op_sel:[1,0,0]
	v_lshlrev_b32_e32 v80, 16, v43
	v_lshlrev_b32_e32 v81, 16, v47
	v_mov_b32_e32 v98, v95
	v_lshlrev_b32_e32 v87, 16, v51
	v_mov_b32_e32 v86, v81
	v_pk_mul_f32 v[80:81], v[62:63], v[80:81] op_sel_hi:[0,1]
	v_pk_fma_f32 v[60:61], v[90:91], v[98:99], v[60:61] op_sel:[1,0,0]
	v_lshlrev_b32_e32 v91, 16, v55
	v_mov_b32_e32 v90, v87
	v_pk_fma_f32 v[80:81], v[66:67], v[86:87], v[80:81] op_sel_hi:[0,1,1]
	v_lshlrev_b32_e32 v89, 16, v59
	v_mov_b32_e32 v88, v91
	v_pk_fma_f32 v[80:81], v[82:83], v[90:91], v[80:81] op_sel_hi:[0,1,1]
	v_pk_fma_f32 v[80:81], v[92:93], v[88:89], v[80:81] op_sel_hi:[0,1,1]
	v_mul_f32_e32 v66, 0xbfb8aa3b, v81
	v_exp_f32_e32 v66, v66
	v_and_b32_e32 v87, 0xffff0000, v47
	v_and_b32_e32 v86, 0xffff0000, v43
	v_and_b32_e32 v89, 0xffff0000, v51
	v_add_f32_e32 v92, 1.0, v66
	v_mov_b32_e32 v66, v63
	v_mov_b32_e32 v88, v87
	v_pk_mul_f32 v[86:87], v[66:67], v[86:87] op_sel_hi:[0,1]
	v_mov_b32_e32 v66, v67
	v_and_b32_e32 v91, 0xffff0000, v55
	v_mov_b32_e32 v90, v89
	v_pk_fma_f32 v[66:67], v[66:67], v[88:89], v[86:87] op_sel_hi:[0,1,1]
	v_mov_b32_e32 v82, v83
	v_and_b32_e32 v95, 0xffff0000, v59
	v_mov_b32_e32 v94, v91
	v_pk_fma_f32 v[66:67], v[82:83], v[90:91], v[66:67] op_sel_hi:[0,1,1]
	v_mov_b32_e32 v82, v93
	v_pk_fma_f32 v[66:67], v[82:83], v[94:95], v[66:67] op_sel_hi:[0,1,1]
	v_mul_f32_e32 v63, 0xbfb8aa3b, v66
	v_mul_f32_e32 v64, 0xbfb8aa3b, v60
	v_mul_f32_e32 v65, 0xbfb8aa3b, v61
	v_exp_f32_e32 v82, v63
	v_mul_f32_e32 v63, 0xbfb8aa3b, v67
	v_exp_f32_e32 v64, v64
	v_exp_f32_e32 v65, v65
	v_exp_f32_e32 v83, v63
	v_mul_f32_e32 v62, 0xbfb8aa3b, v80
	v_add_f32_e32 v64, 1.0, v64
	v_add_f32_e32 v65, 1.0, v65
	v_exp_f32_e32 v62, v62
	v_add_f32_e32 v82, 1.0, v82
	v_add_f32_e32 v83, 1.0, v83
	v_rcp_f32_e32 v64, v64
	v_rcp_f32_e32 v65, v65
	v_rcp_f32_e32 v82, v82
	v_rcp_f32_e32 v83, v83
	v_rcp_f32_e32 v76, v76
	v_rcp_f32_e32 v77, v77
	v_add_f32_e32 v62, 1.0, v62
	v_rcp_f32_e32 v62, v62
	v_rcp_f32_e32 v63, v92
	v_pk_mul_f32 v[60:61], v[60:61], v[64:65]
	v_pk_mul_f32 v[64:65], v[66:67], v[82:83]
	v_mul_u32_u24_e32 v67, 0x90, v106
	v_add3_u32 v67, 0, v107, v67
	v_cvt_pk_bf16_f32 v66, v72, v73
	v_cvt_pk_bf16_f32 v68, v68, v69
	v_add_u32_e32 v67, 0xac00, v67
	v_pk_mul_f32 v[76:77], v[78:79], v[76:77]
	ds_write2_b32 v67, v66, v68 offset1:36
	v_cvt_pk_bf16_f32 v66, v74, v75
	v_cvt_pk_bf16_f32 v68, v70, v71
	v_pk_mul_f32 v[62:63], v[80:81], v[62:63]
	ds_write2_b32 v67, v66, v68 offset0:72 offset1:108
	v_cvt_pk_bf16_f32 v66, v76, v77
	v_cvt_pk_bf16_f32 v60, v60, v61
	ds_write2_b32 v67, v66, v60 offset0:144 offset1:180
	v_cvt_pk_bf16_f32 v60, v62, v63
	v_cvt_pk_bf16_f32 v61, v64, v65
	ds_write2_b32 v67, v60, v61 offset0:216 offset1:252
	s_and_saveexec_b64 s[4:5], vcc
	s_cbranch_execz .LBB0_721
	v_pk_add_f32 v[60:61], v[104:105], v[102:103]
	s_mov_b32 s0, 0x41a00000
	v_add_f32_e32 v60, v60, v61
	v_add_f32_e32 v60, v60, v101
	v_cmp_nlt_f32_e32 vcc, s0, v60
	s_and_saveexec_b64 s[36:37], vcc
	s_cbranch_execz .LBB0_719
	v_mul_f32_e32 v61, 0x3fb8aa3b, v60
	v_exp_f32_e32 v61, v61
	s_mov_b32 s0, 0xc1000000
	v_cmp_ngt_f32_e32 vcc, s0, v60
	s_and_saveexec_b64 s[0:1], vcc
	s_xor_b64 s[40:41], exec, s[0:1]
	s_cbranch_execz .LBB0_716
	v_add_f32_e32 v60, 1.0, v61
	v_cmp_gt_f32_e32 vcc, s17, v60
	s_mov_b32 s0, 0x3f317217
	s_nop 0
	v_cndmask_b32_e64 v61, 0, 32, vcc
	v_ldexp_f32 v60, v60, v61
	v_log_f32_e32 v60, v60
	s_nop 0
	v_mul_f32_e32 v61, 0x3f317217, v60
	v_fma_f32 v61, v60, s0, -v61
	v_fmac_f32_e32 v61, 0x3377d1cf, v60
	s_mov_b32 s0, 0x7f800000
	v_fmac_f32_e32 v61, 0x3f317217, v60
	v_cmp_lt_f32_e64 s[0:1], |v60|, s0
	s_nop 1
	v_cndmask_b32_e64 v60, v60, v61, s[0:1]
	v_cndmask_b32_e32 v61, 0, v225, vcc
	v_sub_f32_e32 v60, v60, v61

.LBB0_899:
	s_andn2_b64 vcc, exec, s[0:1]
	s_cbranch_vccnz .LBB0_957
	s_mov_b64 s[0:1], s[46:47]
	s_waitcnt vmcnt(0)
	v_mbcnt_lo_u32_b32 v0, -1, 0
	v_mbcnt_hi_u32_b32 v0, -1, v0
	v_readlane_b32 s4, v254, 46
	v_add_u32_e32 v0, s3, v0
	v_readlane_b32 s5, v254, 47
	s_andn2_b64 vcc, exec, s[4:5]
	v_readfirstlane_b32 s4, v0
	s_cbranch_vccnz .LBB0_905
	s_load_dwordx2 s[0:1], s[0:1], 0xd8
	v_and_b32_e32 v157, 15, v0
	v_bfe_u32 v4, v0, 4, 2
	v_lshlrev_b32_e32 v160, 4, v4
	v_mov_b32_e32 v161, v97
	s_waitcnt lgkmcnt(0)
	s_add_u32 s2, s0, 0x402ac000
	s_addc_u32 s7, s1, 0
	s_add_u32 s8, s0, 0x582ac000
	s_addc_u32 s9, s1, 0
	s_ashr_i32 s4, s4, 2
	v_bfi_b32 v0, -16, s4, v0
	v_ashrrev_i32_e32 v1, 31, v0
	v_lshlrev_b64 v[0:1], 8, v[0:1]
	v_lshl_add_u64 v[2:3], s[0:1], 0, v[0:1]
	s_and_b32 s28, s4, -16
	v_lshl_add_u64 v[2:3], v[2:3], 0, v[160:161]
	s_mov_b64 s[4:5], 0x382ac000
	v_lshl_add_u64 v[174:175], v[2:3], 0, s[4:5]
	s_ashr_i32 s29, s28, 31
	v_mul_u32_u24_e32 v3, 0x88, v157
	v_lshlrev_b32_e32 v158, 3, v4
	v_lshl_add_u32 v161, v3, 1, 0
	s_lshl_b32 s4, s28, 1
	s_lshl_b64 s[30:31], s[28:29], 1
	v_add3_u32 v228, v161, s4, v158
	s_add_u32 s4, s2, s30
	v_mov_b32_e32 v159, v97
	s_addc_u32 s5, s7, s31
	v_lshlrev_b32_e32 v2, 2, v4
	v_lshl_add_u64 v[176:177], s[4:5], 0, v[158:159]
	v_or_b32_e32 v4, s30, v158
	v_mov_b32_e32 v5, s31
	s_mov_b64 s[4:5], 0x502ac000
	v_lshl_add_u64 v[178:179], v[4:5], 0, s[4:5]
	v_or_b32_e32 v0, v0, v160
	s_mov_b64 s[4:5], 0x382e4080
	v_lshl_add_u64 v[180:181], v[0:1], 0, s[4:5]
	v_lshlrev_b32_e32 v182, 1, v2
	s_mov_b32 s15, s94
	v_mbcnt_lo_u32_b32 v239, -1, 0
	v_mbcnt_hi_u32_b32 v239, -1, v239
	s_lshr_b32 s4, s3, 6
	s_lshl_b32 s5, s4, 1
	v_lshrrev_b32_e32 v240, 5, v239
	v_add_u32_e32 v240, s5, v240
	v_and_b32_e32 v241, 31, v239
	v_lshlrev_b32_e32 v241, 3, v241
	v_mul_u32_u24_e32 v238, 0x110, v240
	v_add_u32_e32 v238, v238, v241
	v_lshl_add_u32 v244, v240, 8, v241
	v_and_b32_e32 v240, 15, v239
	v_lshlrev_b32_e32 v240, 8, v240
	v_lshrrev_b32_e32 v241, 4, v239
	v_lshl_add_u32 v240, v241, 3, v240
	s_lshl_b32 s5, s4, 5
	v_add_u32_e32 v240, s5, v240
	v_sub_u32_e32 v244, v244, v240
	v_ashrrev_i32_e32 v245, 31, v244

.LBB0_903:
	s_nop 2
	v_cvt_pk_bf16_f32 v134, v118, v119
	v_cvt_pk_bf16_f32 v135, v120, v121
	s_waitcnt vmcnt(44)
	v_lshlrev_b32_e32 v122, 16, v192
	v_and_b32_e32 v123, 0xffff0000, v192
	ds_write_b64 v228, v[134:135]
	s_waitcnt vmcnt(43)
	v_pk_fma_f32 v[140:141], v[118:119], v[0:1], v[122:123] op_sel_hi:[1,0,1]
	v_lshlrev_b32_e32 v118, 16, v193
	v_and_b32_e32 v119, 0xffff0000, v193
	s_waitcnt lgkmcnt(0)
	s_barrier
	v_pk_fma_f32 v[142:143], v[120:121], v[0:1], v[118:119] op_sel_hi:[1,0,1]
	v_add_u32_e32 v1, v161, v160
	ds_read_b64 v[240:241], v238
	ds_read_b128 v[144:147], v1
	ds_read_b128 v[148:151], v1 offset:64
	ds_read_b128 v[230:233], v1 offset:128
	ds_read_b128 v[234:237], v1 offset:192
	s_waitcnt lgkmcnt(3)
	v_mfma_f32_16x16x32_bf16 v[4:7], v[4:7], v[144:147], v[140:143]
	s_add_i32 s20, s20, 8
	v_lshl_add_u64 v[206:207], s[0:1], 0, v[186:187]
	s_mov_b32 s10, 0x402e4000
	s_waitcnt lgkmcnt(2)
	v_mfma_f32_16x16x32_bf16 v[4:7], v[8:11], v[148:151], v[4:7]
	v_add_co_u32_e32 v136, vcc, s10, v206
	s_add_u32 s38, s0, s4
	s_waitcnt lgkmcnt(1)
	v_mfma_f32_16x16x32_bf16 v[4:7], v[12:15], v[230:233], v[4:7]
	v_lshl_add_u64 v[130:131], s[0:1], 0, v[190:191]
	v_addc_co_u32_e32 v137, vcc, 0, v207, vcc
	s_waitcnt lgkmcnt(0)
	v_mfma_f32_16x16x32_bf16 v[4:7], v[16:19], v[234:237], v[4:7]
	s_addc_u32 s39, s1, s5
	v_lshl_add_u64 v[152:153], s[0:1], 0, v[188:189]
	global_load_dwordx4 v[118:121], v[130:131], off offset:-128
	global_load_dwordx4 v[122:125], v[130:131], off offset:-64
	global_load_dwordx4 v[126:129], v[130:131], off
	s_nop 0
	global_load_dwordx4 v[130:133], v[130:131], off offset:64
	s_waitcnt vmcnt(41)
	v_lshlrev_b32_e32 v8, 16, v194
	global_load_dwordx2 v[136:137], v[136:137], off
	v_and_b32_e32 v9, 0xffff0000, v194
	global_load_dword v138, v97, s[38:39]
	s_waitcnt vmcnt(42)
	v_pk_fma_f32 v[140:141], v[204:205], v[4:5], v[8:9] op_sel_hi:[0,1,1]
	v_lshl_add_u64 v[242:243], v[152:153], 0, v[244:245]
	global_store_dwordx2 v[242:243], v[240:241], off
	v_cvt_pk_bf16_f32 v134, v4, v5
	v_cvt_pk_bf16_f32 v135, v6, v7
	ds_write_b64 v228, v[134:135] offset:4352
	s_waitcnt lgkmcnt(0)
	s_barrier
	v_lshlrev_b32_e32 v4, 16, v195
	v_and_b32_e32 v5, 0xffff0000, v195
	ds_read_b64 v[240:241], v238 offset:4352
	ds_read_b128 v[144:147], v1 offset:4352
	ds_read_b128 v[148:151], v1 offset:4416
	ds_read_b128 v[230:233], v1 offset:4480
	ds_read_b128 v[234:237], v1 offset:4544
	v_pk_fma_f32 v[142:143], v[204:205], v[6:7], v[4:5] op_sel_hi:[0,1,1]
	s_min_u32 s10, s20, 0x77
	s_add_i32 s10, s10, 8
	s_waitcnt lgkmcnt(3)
	v_mfma_f32_16x16x32_bf16 v[20:23], v[20:23], v[144:147], v[140:143]
	s_add_u32 s38, s34, s10
	s_addc_u32 s39, s35, 0
	s_lshl_b64 s[38:39], s[38:39], 15
	s_waitcnt lgkmcnt(2)
	v_mfma_f32_16x16x32_bf16 v[20:23], v[24:27], v[148:151], v[20:23]
	s_lshl_b32 s10, s10, 2
	v_lshl_add_u64 v[16:17], v[174:175], 0, s[38:39]
	v_lshl_add_u64 v[152:153], v[184:185], 0, s[38:39]
	s_waitcnt lgkmcnt(1)
	v_mfma_f32_16x16x32_bf16 v[20:23], v[28:31], v[230:233], v[20:23]
	v_mov_b32_e32 v0, s10
	s_mov_b32 s10, 0x502b4000
	global_load_dwordx4 v[4:7], v[16:17], off
	global_load_dwordx4 v[8:11], v[16:17], off offset:64
	global_load_dwordx4 v[12:15], v[16:17], off offset:128
	s_nop 0
	global_load_dwordx4 v[16:19], v[16:17], off offset:192
	s_waitcnt lgkmcnt(0)
	v_mfma_f32_16x16x32_bf16 v[20:23], v[32:35], v[234:237], v[20:23]
	global_load_dwordx2 v[192:193], v[152:153], off
	s_waitcnt vmcnt(32)
	v_lshlrev_b32_e32 v24, 16, v196
	global_load_dword v0, v0, s[36:37]
	v_add_co_u32_e32 v152, vcc, s10, v206
	v_and_b32_e32 v25, 0xffff0000, v196
	s_nop 0
	v_addc_co_u32_e32 v153, vcc, 0, v207, vcc
	v_lshl_add_u64 v[242:243], v[152:153], 0, v[244:245]
	global_store_dwordx2 v[242:243], v[240:241], off
	v_cvt_pk_bf16_f32 v134, v20, v21
	v_cvt_pk_bf16_f32 v135, v22, v23
	ds_write_b64 v228, v[134:135]
	s_waitcnt lgkmcnt(0)
	s_barrier
	v_pk_fma_f32 v[140:141], v[2:3], v[20:21], v[24:25] op_sel_hi:[0,1,1]
	v_lshlrev_b32_e32 v20, 16, v197
	v_and_b32_e32 v21, 0xffff0000, v197
	ds_read_b64 v[240:241], v238
	ds_read_b128 v[144:147], v1
	ds_read_b128 v[148:151], v1 offset:64
	ds_read_b128 v[230:233], v1 offset:128
	ds_read_b128 v[234:237], v1 offset:192
	v_pk_fma_f32 v[142:143], v[2:3], v[22:23], v[20:21] op_sel_hi:[0,1,1]
	s_min_u32 s10, s20, 0x76
	s_add_i32 s10, s10, 9
	s_waitcnt lgkmcnt(3)
	v_mfma_f32_16x16x32_bf16 v[36:39], v[36:39], v[144:147], v[140:143]
	s_add_u32 s38, s34, s10
	s_addc_u32 s39, s35, 0
	s_lshl_b64 s[38:39], s[38:39], 15
	s_waitcnt lgkmcnt(2)
	v_mfma_f32_16x16x32_bf16 v[36:39], v[40:43], v[148:151], v[36:39]
	v_lshl_add_u64 v[2:3], v[174:175], 0, s[38:39]
	global_load_dwordx4 v[20:23], v[2:3], off
	global_load_dwordx4 v[24:27], v[2:3], off offset:64
	global_load_dwordx4 v[28:31], v[2:3], off offset:128
	global_load_dwordx4 v[32:35], v[2:3], off offset:192
	v_lshl_add_u64 v[2:3], v[184:185], 0, s[38:39]
	s_waitcnt lgkmcnt(1)
	v_mfma_f32_16x16x32_bf16 v[36:39], v[44:47], v[230:233], v[36:39]
	s_lshl_b32 s10, s10, 2
	global_load_dwordx2 v[194:195], v[2:3], off
	v_mov_b32_e32 v2, s10
	s_waitcnt lgkmcnt(0)
	v_mfma_f32_16x16x32_bf16 v[36:39], v[48:51], v[234:237], v[36:39]
	s_mov_b32 s10, 0x502bc000
	global_load_dword v204, v2, s[36:37]
	v_add_co_u32_e32 v2, vcc, s10, v206
	s_min_u32 s10, s20, 0x75
	s_nop 0
	v_addc_co_u32_e32 v3, vcc, 0, v207, vcc
	v_lshl_add_u64 v[242:243], v[2:3], 0, v[244:245]
	global_store_dwordx2 v[242:243], v[240:241], off
	s_nop 0
	v_cvt_pk_bf16_f32 v134, v36, v37
	v_cvt_pk_bf16_f32 v135, v38, v39
	ds_write_b64 v228, v[134:135] offset:4352
	s_waitcnt lgkmcnt(0)
	s_barrier
	s_waitcnt vmcnt(36)
	v_lshlrev_b32_e32 v2, 16, v198
	v_and_b32_e32 v3, 0xffff0000, v198
	v_pk_fma_f32 v[140:141], v[96:97], v[36:37], v[2:3] op_sel_hi:[0,1,1]
	v_lshlrev_b32_e32 v2, 16, v199
	v_and_b32_e32 v3, 0xffff0000, v199
	ds_read_b64 v[240:241], v238 offset:4352
	ds_read_b128 v[144:147], v1 offset:4352
	ds_read_b128 v[148:151], v1 offset:4416
	ds_read_b128 v[230:233], v1 offset:4480
	ds_read_b128 v[234:237], v1 offset:4544
	v_pk_fma_f32 v[142:143], v[96:97], v[38:39], v[2:3] op_sel_hi:[0,1,1]
	s_add_i32 s10, s10, 10
	s_add_u32 s38, s34, s10
	s_waitcnt lgkmcnt(3)
	v_mfma_f32_16x16x32_bf16 v[52:55], v[52:55], v[144:147], v[140:143]
	s_addc_u32 s39, s35, 0
	s_lshl_b64 s[38:39], s[38:39], 15
	v_lshl_add_u64 v[2:3], v[174:175], 0, s[38:39]
	s_waitcnt lgkmcnt(2)
	v_mfma_f32_16x16x32_bf16 v[52:55], v[56:59], v[148:151], v[52:55]
	global_load_dwordx4 v[36:39], v[2:3], off
	global_load_dwordx4 v[40:43], v[2:3], off offset:64
	global_load_dwordx4 v[44:47], v[2:3], off offset:128
	global_load_dwordx4 v[48:51], v[2:3], off offset:192
	v_lshl_add_u64 v[2:3], v[184:185], 0, s[38:39]
	s_lshl_b32 s10, s10, 2
	s_waitcnt lgkmcnt(1)
	v_mfma_f32_16x16x32_bf16 v[52:55], v[60:63], v[230:233], v[52:55]
	global_load_dwordx2 v[196:197], v[2:3], off
	v_mov_b32_e32 v2, s10
	s_mov_b32 s10, 0x502c4000
	s_waitcnt lgkmcnt(0)
	v_mfma_f32_16x16x32_bf16 v[52:55], v[64:67], v[234:237], v[52:55]
	v_add_co_u32_e32 v152, vcc, s10, v206
	global_load_dword v2, v2, s[36:37]
	s_nop 0
	v_addc_co_u32_e32 v153, vcc, 0, v207, vcc
	v_lshl_add_u64 v[242:243], v[152:153], 0, v[244:245]
	global_store_dwordx2 v[242:243], v[240:241], off
	s_nop 2
	v_cvt_pk_bf16_f32 v134, v52, v53
	v_cvt_pk_bf16_f32 v135, v54, v55
	ds_write_b64 v228, v[134:135]
	s_waitcnt vmcnt(38)
	v_lshlrev_b32_e32 v56, 16, v200
	v_and_b32_e32 v57, 0xffff0000, v200
	s_waitcnt lgkmcnt(0)
	s_barrier
	v_pk_fma_f32 v[140:141], v[154:155], v[52:53], v[56:57] op_sel_hi:[0,1,1]
	v_lshlrev_b32_e32 v52, 16, v201
	v_and_b32_e32 v53, 0xffff0000, v201
	v_pk_fma_f32 v[142:143], v[154:155], v[54:55], v[52:53] op_sel_hi:[0,1,1]
	ds_read_b64 v[240:241], v238
	ds_read_b128 v[144:147], v1
	ds_read_b128 v[148:151], v1 offset:64
	ds_read_b128 v[152:155], v1 offset:128
	ds_read_b128 v[230:233], v1 offset:192
	s_waitcnt lgkmcnt(3)
	v_mfma_f32_16x16x32_bf16 v[68:71], v[68:71], v[144:147], v[140:143]
	s_min_u32 s10, s20, 0x74
	s_add_i32 s10, s10, 11
	s_add_u32 s38, s34, s10
	s_waitcnt lgkmcnt(2)
	v_mfma_f32_16x16x32_bf16 v[68:71], v[72:75], v[148:151], v[68:71]
	s_addc_u32 s39, s35, 0
	s_lshl_b32 s10, s10, 2
	v_mov_b32_e32 v3, s10
	s_waitcnt lgkmcnt(1)
	v_mfma_f32_16x16x32_bf16 v[68:71], v[76:79], v[152:155], v[68:71]
	s_mov_b32 s10, 0x502cc000
	s_lshl_b64 s[38:39], s[38:39], 15
	v_add_co_u32_e32 v200, vcc, s10, v206
	s_waitcnt lgkmcnt(0)
	v_mfma_f32_16x16x32_bf16 v[68:71], v[80:83], v[230:233], v[68:71]
	v_lshl_add_u64 v[64:65], v[174:175], 0, s[38:39]
	v_lshl_add_u64 v[198:199], v[184:185], 0, s[38:39]
	v_addc_co_u32_e32 v201, vcc, 0, v207, vcc
	global_load_dwordx4 v[52:55], v[64:65], off
	global_load_dwordx4 v[56:59], v[64:65], off offset:64
	global_load_dwordx4 v[60:63], v[64:65], off offset:128
	s_nop 0
	global_load_dwordx4 v[64:67], v[64:65], off offset:192
	s_waitcnt vmcnt(37)
	v_lshlrev_b32_e32 v72, 16, v202
	global_load_dwordx2 v[198:199], v[198:199], off
	v_and_b32_e32 v73, 0xffff0000, v202
	global_load_dword v96, v3, s[36:37]
	v_pk_fma_f32 v[140:141], v[156:157], v[68:69], v[72:73] op_sel_hi:[0,1,1]
	v_lshl_add_u64 v[242:243], v[200:201], 0, v[244:245]
	global_store_dwordx2 v[242:243], v[240:241], off
	v_cvt_pk_bf16_f32 v134, v68, v69
	v_cvt_pk_bf16_f32 v135, v70, v71
	ds_write_b64 v228, v[134:135] offset:4352
	s_waitcnt lgkmcnt(0)
	s_barrier
	v_lshlrev_b32_e32 v68, 16, v203
	v_and_b32_e32 v69, 0xffff0000, v203
	ds_read_b64 v[240:241], v238 offset:4352
	ds_read_b128 v[144:147], v1 offset:4352
	ds_read_b128 v[148:151], v1 offset:4416
	ds_read_b128 v[230:233], v1 offset:4480
	ds_read_b128 v[234:237], v1 offset:4544
	v_pk_fma_f32 v[142:143], v[156:157], v[70:71], v[68:69] op_sel_hi:[0,1,1]
	s_min_u32 s10, s20, 0x73
	s_add_i32 s10, s10, 12
	s_waitcnt lgkmcnt(3)
	v_mfma_f32_16x16x32_bf16 v[84:87], v[84:87], v[144:147], v[140:143]
	s_add_u32 s38, s34, s10
	s_addc_u32 s39, s35, 0
	s_lshl_b64 s[38:39], s[38:39], 15
	s_waitcnt lgkmcnt(2)
	v_mfma_f32_16x16x32_bf16 v[84:87], v[88:91], v[148:151], v[84:87]
	s_lshl_b32 s10, s10, 2
	v_lshl_add_u64 v[80:81], v[174:175], 0, s[38:39]
	v_lshl_add_u64 v[152:153], v[184:185], 0, s[38:39]
	s_waitcnt lgkmcnt(1)
	v_mfma_f32_16x16x32_bf16 v[84:87], v[92:95], v[230:233], v[84:87]
	v_mov_b32_e32 v3, s10
	s_mov_b32 s10, 0x502d4000
	global_load_dwordx4 v[68:71], v[80:81], off
	global_load_dwordx4 v[72:75], v[80:81], off offset:64
	global_load_dwordx4 v[76:79], v[80:81], off offset:128
	s_nop 0
	global_load_dwordx4 v[80:83], v[80:81], off offset:192
	s_waitcnt lgkmcnt(0)
	v_mfma_f32_16x16x32_bf16 v[84:87], v[98:101], v[234:237], v[84:87]
	global_load_dwordx2 v[200:201], v[152:153], off
	global_load_dword v154, v3, s[36:37]
	v_add_co_u32_e32 v152, vcc, s10, v206
	s_waitcnt vmcnt(41)
	v_lshlrev_b32_e32 v88, 16, v208
	v_addc_co_u32_e32 v153, vcc, 0, v207, vcc
	v_lshl_add_u64 v[242:243], v[152:153], 0, v[244:245]
	global_store_dwordx2 v[242:243], v[240:241], off
	s_nop 0
	v_cvt_pk_bf16_f32 v134, v84, v85
	v_cvt_pk_bf16_f32 v135, v86, v87
	ds_write_b64 v228, v[134:135]
	s_waitcnt lgkmcnt(0)
	s_barrier
	v_and_b32_e32 v89, 0xffff0000, v208
	v_pk_fma_f32 v[140:141], v[210:211], v[84:85], v[88:89] op_sel_hi:[0,1,1]
	v_lshlrev_b32_e32 v84, 16, v209
	v_and_b32_e32 v85, 0xffff0000, v209
	ds_read_b64 v[240:241], v238
	ds_read_b128 v[144:147], v1
	ds_read_b128 v[148:151], v1 offset:64
	ds_read_b128 v[230:233], v1 offset:128
	ds_read_b128 v[234:237], v1 offset:192
	v_pk_fma_f32 v[142:143], v[210:211], v[86:87], v[84:85] op_sel_hi:[0,1,1]
	s_min_u32 s10, s20, 0x72
	s_add_i32 s10, s10, 13
	s_waitcnt lgkmcnt(3)
	v_mfma_f32_16x16x32_bf16 v[102:105], v[102:105], v[144:147], v[140:143]
	s_add_u32 s38, s34, s10
	s_addc_u32 s39, s35, 0
	s_lshl_b64 s[38:39], s[38:39], 15
	s_waitcnt lgkmcnt(2)
	v_mfma_f32_16x16x32_bf16 v[102:105], v[106:109], v[148:151], v[102:105]
	s_lshl_b32 s10, s10, 2
	v_lshl_add_u64 v[98:99], v[174:175], 0, s[38:39]
	v_lshl_add_u64 v[152:153], v[184:185], 0, s[38:39]
	s_waitcnt lgkmcnt(1)
	v_mfma_f32_16x16x32_bf16 v[102:105], v[110:113], v[230:233], v[102:105]
	v_mov_b32_e32 v3, s10
	s_mov_b32 s10, 0x502dc000
	global_load_dwordx4 v[84:87], v[98:99], off
	global_load_dwordx4 v[88:91], v[98:99], off offset:64
	global_load_dwordx4 v[92:95], v[98:99], off offset:128
	s_nop 0
	global_load_dwordx4 v[98:101], v[98:99], off offset:192
	s_waitcnt lgkmcnt(0)
	v_mfma_f32_16x16x32_bf16 v[102:105], v[114:117], v[234:237], v[102:105]
	global_load_dwordx2 v[202:203], v[152:153], off
	global_load_dword v156, v3, s[36:37]
	v_add_co_u32_e32 v152, vcc, s10, v206
	s_min_u32 s10, s20, 0x71
	s_add_i32 s10, s10, 14
	s_add_u32 s38, s34, s10
	v_addc_co_u32_e32 v153, vcc, 0, v207, vcc
	s_nop 0
	v_cvt_pk_bf16_f32 v212, v102, v103
	v_cvt_pk_bf16_f32 v213, v104, v105
	s_addc_u32 s39, s35, 0
	v_lshl_add_u64 v[242:243], v[152:153], 0, v[244:245]
	global_store_dwordx2 v[242:243], v[240:241], off
	ds_write_b64 v228, v[212:213] offset:4352
	s_waitcnt vmcnt(44)
	v_lshlrev_b32_e32 v106, 16, v136
	v_and_b32_e32 v107, 0xffff0000, v136
	s_lshl_b64 s[38:39], s[38:39], 15
	s_waitcnt lgkmcnt(0)
	s_barrier
	s_waitcnt vmcnt(43)
	v_pk_fma_f32 v[134:135], v[138:139], v[102:103], v[106:107] op_sel_hi:[0,1,1]
	v_lshlrev_b32_e32 v102, 16, v137
	v_and_b32_e32 v103, 0xffff0000, v137
	v_lshl_add_u64 v[114:115], v[174:175], 0, s[38:39]
	v_pk_fma_f32 v[136:137], v[138:139], v[104:105], v[102:103] op_sel_hi:[0,1,1]
	ds_read_b64 v[240:241], v238 offset:4352
	ds_read_b128 v[138:141], v1 offset:4352
	ds_read_b128 v[142:145], v1 offset:4416
	ds_read_b128 v[146:149], v1 offset:4480
	ds_read_b128 v[150:153], v1 offset:4544
	global_load_dwordx4 v[102:105], v[114:115], off
	global_load_dwordx4 v[106:109], v[114:115], off offset:64
	global_load_dwordx4 v[110:113], v[114:115], off offset:128
	s_nop 0
	global_load_dwordx4 v[114:117], v[114:115], off offset:192
	s_lshl_b32 s10, s10, 2
	v_lshl_add_u64 v[208:209], v[184:185], 0, s[38:39]
	v_mov_b32_e32 v1, s10
	global_load_dwordx2 v[208:209], v[208:209], off
	s_waitcnt lgkmcnt(3)
	v_mfma_f32_16x16x32_bf16 v[118:121], v[118:121], v[138:141], v[134:137]
	global_load_dword v210, v1, s[36:37]
	s_mov_b32 s10, 0x502e4000
	s_add_u32 s4, s4, 32
	s_waitcnt lgkmcnt(2)
	v_mfma_f32_16x16x32_bf16 v[118:121], v[122:125], v[142:145], v[118:121]
	v_add_co_u32_e32 v206, vcc, s10, v206
	s_addc_u32 s5, s5, 0
	s_waitcnt lgkmcnt(1)
	v_mfma_f32_16x16x32_bf16 v[118:121], v[126:129], v[146:149], v[118:121]
	v_addc_co_u32_e32 v207, vcc, 0, v207, vcc
	v_lshl_add_u64 v[186:187], v[186:187], 0, s[26:27]
	s_waitcnt lgkmcnt(0)
	v_mfma_f32_16x16x32_bf16 v[118:121], v[130:133], v[150:153], v[118:121]
	v_lshl_add_u64 v[188:189], v[188:189], 0, s[26:27]
	v_lshl_add_u64 v[190:191], v[190:191], 0, s[26:27]
	s_cmpk_gt_u32 s20, 0x77
	v_lshl_add_u64 v[242:243], v[206:207], 0, v[244:245]
	global_store_dwordx2 v[242:243], v[240:241], off
	s_cbranch_scc0 .LBB0_903
	s_waitcnt lgkmcnt(0)
	s_barrier
	s_load_dword s4, s[62:63], 0x0
	s_waitcnt lgkmcnt(0)
	s_add_i32 s15, s4, s15
	s_cmpk_gt_i32 s15, 0xff
	s_cbranch_scc0 .LBB0_902
